# GEMM MFMA phases at priority 3 instead of 1 (on top of QK double-buffer, merge-loop fix, unscaled fp8 MFMA)
# speedup vs baseline: 1.0025x; 1.0025x over previous
.LBB0_578:
	s_add_u32 s2, s2, 0x40000
	s_addc_u32 s3, s3, 0
	s_mov_b32 m0, s41
	v_lshl_add_u64 v[48:49], s[2:3], 0, v[192:193]
	global_load_lds_dwordx4 v[48:49], off
	v_lshl_add_u64 v[48:49], s[2:3], 0, v[196:197]
	s_mov_b32 m0, s52
	s_nop 0
	global_load_lds_dwordx4 v[48:49], off
	s_waitcnt lgkmcnt(8)
	s_barrier
	s_waitcnt lgkmcnt(0)
	s_setprio 3
	s_waitcnt lgkmcnt(0)
	v_mfma_f32_16x16x128_f8f6f4 v[188:191], v[8:15], v[40:47], v[188:191]
	v_mfma_f32_16x16x128_f8f6f4 v[180:183], v[0:7], v[40:47], v[180:183]
	v_mfma_f32_16x16x128_f8f6f4 v[172:175], v[8:15], v[32:39], v[172:175]
	v_mfma_f32_16x16x128_f8f6f4 v[164:167], v[0:7], v[32:39], v[164:167]
	v_mfma_f32_16x16x128_f8f6f4 v[156:159], v[8:15], v[24:31], v[156:159]
	v_mfma_f32_16x16x128_f8f6f4 v[148:151], v[0:7], v[24:31], v[148:151]
	v_mfma_f32_16x16x128_f8f6f4 v[140:143], v[8:15], v[16:23], v[140:143]
	v_mfma_f32_16x16x128_f8f6f4 v[132:135], v[0:7], v[16:23], v[132:135]
	s_setprio 0
	s_barrier
	s_add_i32 s78, 0, 0x1c000
	s_mov_b32 m0, s62
	v_add_u32_e32 v60, s78, v232
	v_lshl_add_u64 v[222:223], v[222:223], 0, s[28:29]
	ds_read_b128 v[48:51], v60
	ds_read_b128 v[52:55], v60 offset:1024
	ds_read_b128 v[56:59], v60 offset:2048
	ds_read_b128 v[60:63], v60 offset:3072
	global_load_lds_dwordx4 v[222:223], off
	v_lshl_add_u64 v[222:223], v[224:225], 0, s[28:29]
	s_mov_b32 m0, s96
	s_nop 0
	global_load_lds_dwordx4 v[222:223], off
	s_barrier
	s_waitcnt lgkmcnt(0)
	s_setprio 3
	s_waitcnt lgkmcnt(0)
	v_mfma_f32_16x16x128_f8f6f4 v[184:187], v[48:55], v[40:47], v[184:187]
	v_mfma_f32_16x16x128_f8f6f4 v[176:179], v[56:63], v[40:47], v[176:179]
	v_mfma_f32_16x16x128_f8f6f4 v[168:171], v[48:55], v[32:39], v[168:171]
	v_mfma_f32_16x16x128_f8f6f4 v[160:163], v[56:63], v[32:39], v[160:163]
	v_mfma_f32_16x16x128_f8f6f4 v[152:155], v[48:55], v[24:31], v[152:155]
	v_mfma_f32_16x16x128_f8f6f4 v[144:147], v[56:63], v[24:31], v[144:147]
	v_mfma_f32_16x16x128_f8f6f4 v[136:139], v[48:55], v[16:23], v[136:139]
	v_mfma_f32_16x16x128_f8f6f4 v[128:131], v[56:63], v[16:23], v[128:131]
	s_setprio 0
	s_mov_b32 m0, s97
	v_lshl_add_u64 v[222:223], v[226:227], 0, s[28:29]
	s_barrier
	ds_read_b128 v[16:19], v235 offset:49152
	ds_read_b128 v[20:23], v235 offset:50176
	ds_read_b128 v[24:27], v235 offset:51200
	ds_read_b128 v[28:31], v235 offset:52224
	ds_read_b128 v[32:35], v235 offset:53248
	ds_read_b128 v[36:39], v235 offset:54272
	ds_read_b128 v[40:43], v235 offset:55296
	ds_read_b128 v[44:47], v235 offset:56320
	global_load_lds_dwordx4 v[222:223], off
	v_lshl_add_u64 v[222:223], v[228:229], 0, s[28:29]
	s_mov_b32 m0, s39
	s_nop 0
	global_load_lds_dwordx4 v[222:223], off
	s_barrier
	s_waitcnt lgkmcnt(0)
	s_setprio 3
	s_waitcnt lgkmcnt(0)
	v_mfma_f32_16x16x128_f8f6f4 v[116:119], v[8:15], v[16:23], v[116:119]
	v_mfma_f32_16x16x128_f8f6f4 v[112:115], v[0:7], v[16:23], v[112:115]
	v_mfma_f32_16x16x128_f8f6f4 v[100:103], v[8:15], v[24:31], v[100:103]
	v_mfma_f32_16x16x128_f8f6f4 v[96:99], v[0:7], v[24:31], v[96:99]
	v_mfma_f32_16x16x128_f8f6f4 v[84:87], v[8:15], v[32:39], v[84:87]
	v_mfma_f32_16x16x128_f8f6f4 v[80:83], v[0:7], v[32:39], v[80:83]
	v_mfma_f32_16x16x128_f8f6f4 v[68:71], v[8:15], v[40:47], v[68:71]
	v_mfma_f32_16x16x128_f8f6f4 v[64:67], v[0:7], v[40:47], v[64:67]
	s_setprio 0
	s_barrier
	s_add_u32 s2, s76, 0x40080
	s_addc_u32 s3, s77, 0
	s_add_i32 s76, s78, s53
	v_lshl_add_u64 v[0:1], s[2:3], 0, v[194:195]
	s_mov_b32 m0, s76
	s_nop 0
	global_load_lds_dwordx4 v[0:1], off
	v_lshl_add_u64 v[0:1], s[2:3], 0, v[198:199]
	s_add_i32 m0, s76, 0x2000
	s_nop 0
	global_load_lds_dwordx4 v[0:1], off
	s_waitcnt vmcnt(6)
	s_barrier
	s_setprio 3
	v_mfma_f32_16x16x128_f8f6f4 v[124:127], v[48:55], v[16:23], v[124:127]
	v_mfma_f32_16x16x128_f8f6f4 v[120:123], v[56:63], v[16:23], v[120:123]
	v_mfma_f32_16x16x128_f8f6f4 v[108:111], v[48:55], v[24:31], v[108:111]
	v_mfma_f32_16x16x128_f8f6f4 v[104:107], v[56:63], v[24:31], v[104:107]
	v_mfma_f32_16x16x128_f8f6f4 v[92:95], v[48:55], v[32:39], v[92:95]
	v_mfma_f32_16x16x128_f8f6f4 v[88:91], v[56:63], v[32:39], v[88:91]
	v_mfma_f32_16x16x128_f8f6f4 v[76:79], v[48:55], v[40:47], v[76:79]
	v_mfma_f32_16x16x128_f8f6f4 v[72:75], v[56:63], v[40:47], v[72:75]
	s_setprio 0
	s_add_i32 s82, s82, 2
	s_add_u32 s36, s36, 0x100
	s_addc_u32 s37, s37, 0
	s_add_u32 s54, s54, 0x100
	s_addc_u32 s57, s57, 0
	s_cmp_gt_u32 s82, 13
	s_barrier
	s_cbranch_scc1 .LBB0_591
.LBB0_579:
	ds_read_b128 v[0:3], v234
	ds_read_b128 v[4:7], v234 offset:1024
	ds_read_b128 v[8:11], v234 offset:2048
	ds_read_b128 v[12:15], v234 offset:3072
	s_xor_b64 s[78:79], s[66:67], -1
	v_lshl_add_u64 v[16:17], s[36:37], 0, v[208:209]
	s_add_i32 m0, s9, 0xc000
	ds_read_b128 v[56:59], v235
	ds_read_b128 v[60:63], v235 offset:1024
	ds_read_b128 v[48:51], v235 offset:2048
	ds_read_b128 v[52:55], v235 offset:3072
	ds_read_b128 v[40:43], v235 offset:4096
	ds_read_b128 v[44:47], v235 offset:5120
	ds_read_b128 v[32:35], v235 offset:6144
	ds_read_b128 v[36:39], v235 offset:7168
	global_load_lds_dwordx4 v[16:17], off
	v_lshl_add_u64 v[16:17], s[36:37], 0, v[210:211]
	s_add_i32 m0, s9, 0xe000
	s_nop 0
	global_load_lds_dwordx4 v[16:17], off
	s_waitcnt lgkmcnt(8)
	s_barrier
	s_waitcnt lgkmcnt(0)
	s_setprio 3
	s_waitcnt lgkmcnt(0)
	v_mfma_f32_16x16x128_f8f6f4 v[188:191], v[0:7], v[56:63], v[188:191]
	v_mfma_f32_16x16x128_f8f6f4 v[180:183], v[8:15], v[56:63], v[180:183]
	v_mfma_f32_16x16x128_f8f6f4 v[172:175], v[0:7], v[48:55], v[172:175]
	v_mfma_f32_16x16x128_f8f6f4 v[164:167], v[8:15], v[48:55], v[164:167]
	v_mfma_f32_16x16x128_f8f6f4 v[156:159], v[0:7], v[40:47], v[156:159]
	v_mfma_f32_16x16x128_f8f6f4 v[148:151], v[8:15], v[40:47], v[148:151]
	v_mfma_f32_16x16x128_f8f6f4 v[140:143], v[0:7], v[32:39], v[140:143]
	v_mfma_f32_16x16x128_f8f6f4 v[132:135], v[8:15], v[32:39], v[132:135]
	s_setprio 0
	s_barrier
	ds_read_b128 v[24:27], v237
	ds_read_b128 v[28:31], v237 offset:1024
	ds_read_b128 v[16:19], v237 offset:2048
	ds_read_b128 v[20:23], v237 offset:3072
	s_and_b64 vcc, exec, s[78:79]
	s_cbranch_vccnz .LBB0_581
	v_add_u32_e32 v218, v231, v230
	ds_read2_b32 v[212:213], v218 offset1:32
	ds_read2_b32 v[214:215], v218 offset0:64 offset1:96
	ds_read2_b32 v[216:217], v218 offset0:128 offset1:160
	ds_read2_b32 v[218:219], v218 offset0:192 offset1:224

.LBB0_583:
	s_setprio 3
	s_waitcnt lgkmcnt(0)
	v_mfma_f32_16x16x128_f8f6f4 v[184:187], v[24:31], v[56:63], v[184:187]
	v_mfma_f32_16x16x128_f8f6f4 v[176:179], v[16:23], v[56:63], v[176:179]
	v_mfma_f32_16x16x128_f8f6f4 v[168:171], v[24:31], v[48:55], v[168:171]
	v_mfma_f32_16x16x128_f8f6f4 v[160:163], v[16:23], v[48:55], v[160:163]
	v_mfma_f32_16x16x128_f8f6f4 v[152:155], v[24:31], v[40:47], v[152:155]
	v_mfma_f32_16x16x128_f8f6f4 v[144:147], v[16:23], v[40:47], v[144:147]
	v_mfma_f32_16x16x128_f8f6f4 v[136:139], v[24:31], v[32:39], v[136:139]
	v_mfma_f32_16x16x128_f8f6f4 v[128:131], v[16:23], v[32:39], v[128:131]
	s_setprio 0
	s_barrier
	ds_read_b128 v[56:59], v235 offset:16384
	ds_read_b128 v[60:63], v235 offset:17408
	ds_read_b128 v[48:51], v235 offset:18432
	ds_read_b128 v[52:55], v235 offset:19456
	ds_read_b128 v[40:43], v235 offset:20480
	ds_read_b128 v[44:47], v235 offset:21504
	ds_read_b128 v[32:35], v235 offset:22528
	ds_read_b128 v[36:39], v235 offset:23552
	s_and_b64 vcc, exec, s[2:3]
	s_cbranch_vccnz .LBB0_585
	v_lshl_add_u64 v[226:227], v[204:205], 0, s[42:43]
	global_store_dwordx2 v[226:227], v[220:221], off
.LBB0_585:
	s_add_u32 s66, s36, 0xfffc0080
	s_addc_u32 s67, s37, -1
	s_and_b64 s[2:3], s[80:81], exec
	s_cselect_b32 s3, s5, s67
	s_cselect_b32 s2, s8, s66
	s_mov_b32 m0, s9
	v_lshl_add_u64 v[226:227], s[2:3], 0, v[192:193]
	global_load_lds_dwordx4 v[226:227], off
	v_lshl_add_u64 v[228:229], s[2:3], 0, v[196:197]
	s_mov_b32 m0, s15
	s_nop 0
	global_load_lds_dwordx4 v[228:229], off
	s_barrier
	s_waitcnt lgkmcnt(0)
	s_setprio 3
	s_waitcnt lgkmcnt(0)
	v_mfma_f32_16x16x128_f8f6f4 v[116:119], v[0:7], v[56:63], v[116:119]
	v_mfma_f32_16x16x128_f8f6f4 v[112:115], v[8:15], v[56:63], v[112:115]
	v_mfma_f32_16x16x128_f8f6f4 v[100:103], v[0:7], v[48:55], v[100:103]
	v_mfma_f32_16x16x128_f8f6f4 v[96:99], v[8:15], v[48:55], v[96:99]
	v_mfma_f32_16x16x128_f8f6f4 v[84:87], v[0:7], v[40:47], v[84:87]
	v_mfma_f32_16x16x128_f8f6f4 v[80:83], v[8:15], v[40:47], v[80:83]
	v_mfma_f32_16x16x128_f8f6f4 v[68:71], v[0:7], v[32:39], v[68:71]
	v_mfma_f32_16x16x128_f8f6f4 v[64:67], v[8:15], v[32:39], v[64:67]
	s_setprio 0
	s_barrier
	s_add_u32 s66, s76, 0x40000
	s_addc_u32 s67, s77, 0
	s_mov_b32 m0, s33
	v_lshl_add_u64 v[0:1], s[66:67], 0, v[194:195]
	global_load_lds_dwordx4 v[0:1], off
	v_lshl_add_u64 v[0:1], s[66:67], 0, v[198:199]
	s_mov_b32 m0, s40
	s_mov_b64 s[66:67], -1
	global_load_lds_dwordx4 v[0:1], off
	s_and_b64 vcc, exec, s[78:79]
	s_cbranch_vccz .LBB0_587
	s_waitcnt vmcnt(6)
	s_mov_b64 s[66:67], 0

;     __device__ __forceinline__ void decode(int j, size_t& soff, int& sld, size_t& doff) const {
;         if (gu) { const int e = j >> 11, r = j & 2047, nt = r >> 4, kt = r & 15, n0 = nt * 32, w = n0 & 255, tile = n0 >> 8;
;             const int sc = (w < 128) ? 128 * tile + w : 2048 + 128 * tile + (w - 128);
;             sld = 4096; soff = (size_t)e * 2048 * 4096 + (size_t)(kt * 128) * 4096 + sc; doff = (size_t)e * 4096 * 2048 + (size_t)n0 * 2048 + kt * 128; }
.LBB0_589:
	s_barrier
	s_setprio 3
	v_mfma_f32_16x16x128_f8f6f4 v[124:127], v[24:31], v[56:63], v[124:127]
	v_mfma_f32_16x16x128_f8f6f4 v[120:123], v[16:23], v[56:63], v[120:123]
	v_mfma_f32_16x16x128_f8f6f4 v[108:111], v[24:31], v[48:55], v[108:111]
	v_mfma_f32_16x16x128_f8f6f4 v[104:107], v[16:23], v[48:55], v[104:107]
	v_mfma_f32_16x16x128_f8f6f4 v[92:95], v[24:31], v[40:47], v[92:95]
	v_mfma_f32_16x16x128_f8f6f4 v[88:91], v[16:23], v[40:47], v[88:91]
	v_mfma_f32_16x16x128_f8f6f4 v[76:79], v[24:31], v[32:39], v[76:79]
	v_mfma_f32_16x16x128_f8f6f4 v[72:75], v[16:23], v[32:39], v[72:75]
	s_setprio 0
	v_add_u32_e32 v4, 0x18000, v233
	s_barrier
	ds_read_b128 v[8:11], v4
	ds_read_b128 v[12:15], v4 offset:1024
	ds_read_b128 v[0:3], v4 offset:2048
	ds_read_b128 v[4:7], v4 offset:3072
	ds_read_b128 v[40:43], v235 offset:32768
	ds_read_b128 v[44:47], v235 offset:33792
	ds_read_b128 v[32:35], v235 offset:34816
	ds_read_b128 v[36:39], v235 offset:35840
	ds_read_b128 v[24:27], v235 offset:36864
	ds_read_b128 v[28:31], v235 offset:37888
	ds_read_b128 v[16:19], v235 offset:38912
	ds_read_b128 v[20:23], v235 offset:39936
	s_mul_i32 s78, s63, s19
	s_add_i32 s78, s78, s18
	s_cmp_lt_i32 s78, 0xa000
	s_cselect_b64 s[66:67], -1, 0
	s_cmp_gt_i32 s78, 0x9fff
	s_cbranch_scc1 .LBB0_578
	s_lshl_b32 s43, s78, 1
	s_and_b32 s43, s43, 0xe0
	s_and_b32 s79, s78, 0x780
	s_or_b32 s80, s43, s79
	s_add_i32 s79, s79, s43
	s_ashr_i32 s42, s78, 11
	s_addk_i32 s79, 0x780
	s_cmpk_lt_u32 s43, 0x80
	s_cselect_b32 s79, s80, s79
	s_lshl_b32 s80, s78, 7
	s_and_b32 s83, s80, 0x780
	s_ashr_i32 s43, s42, 31
	s_lshl_b32 s80, s83, 12
	s_lshl_b64 s[42:43], s[42:43], 23
	s_or_b32 s79, s79, s80
	s_or_b32 s80, s42, s79
	s_mov_b32 s81, s43
	v_lshl_add_u64 v[48:49], s[80:81], 2, v[206:207]
	s_add_i32 m0, s10, 0x20000
	s_mov_b64 s[80:81], 0x20000
	global_load_lds_dwordx4 v[48:49], off nt
	v_lshl_add_u64 v[48:49], v[48:49], 0, s[80:81]
	s_mov_b32 m0, s48
	s_lshl_b32 s78, s78, 12
	global_load_lds_dwordx4 v[48:49], off nt
	s_and_b32 s78, s78, 0x7f0000
	s_or_b32 s78, s83, s78
	s_or_b32 s42, s42, s78
	s_add_i32 s63, s63, 1
	s_branch .LBB0_578

.LBB0_917:
	s_add_u32 s0, s0, 0x80000
	s_addc_u32 s1, s1, 0
	s_mov_b32 m0, s8
	v_lshl_add_u64 v[120:121], s[0:1], 0, v[200:201]
	global_load_lds_dwordx4 v[120:121], off
	v_lshl_add_u64 v[120:121], s[0:1], 0, v[204:205]
	s_mov_b32 m0, s9
	s_nop 0
	global_load_lds_dwordx4 v[120:121], off
	s_waitcnt lgkmcnt(8)
	s_barrier
	s_waitcnt lgkmcnt(0)
	s_setprio 3
	s_waitcnt lgkmcnt(0)
	v_mfma_f32_16x16x32_bf16 v[80:83], v[128:131], v[184:187], v[80:83]
	v_mfma_f32_16x16x32_bf16 v[148:151], v[132:135], v[188:191], v[80:83]
	v_mfma_f32_16x16x32_bf16 v[80:83], v[152:155], v[184:187], v[84:87]
	v_mfma_f32_16x16x32_bf16 v[144:147], v[156:159], v[188:191], v[80:83]
	v_mfma_f32_16x16x32_bf16 v[80:83], v[128:131], v[176:179], v[104:107]
	v_mfma_f32_16x16x32_bf16 v[124:127], v[132:135], v[180:183], v[80:83]
	v_mfma_f32_16x16x32_bf16 v[80:83], v[152:155], v[176:179], v[108:111]
	v_mfma_f32_16x16x32_bf16 v[120:123], v[156:159], v[180:183], v[80:83]
	v_mfma_f32_16x16x32_bf16 v[80:83], v[128:131], v[168:171], v[100:103]
	v_mfma_f32_16x16x32_bf16 v[100:103], v[132:135], v[172:175], v[80:83]
	v_mfma_f32_16x16x32_bf16 v[80:83], v[152:155], v[168:171], v[96:99]
	v_mfma_f32_16x16x32_bf16 v[76:79], v[128:131], v[160:163], v[76:79]
	v_mfma_f32_16x16x32_bf16 v[72:75], v[152:155], v[160:163], v[72:75]
	v_mfma_f32_16x16x32_bf16 v[96:99], v[156:159], v[172:175], v[80:83]
	v_mfma_f32_16x16x32_bf16 v[76:79], v[132:135], v[164:167], v[76:79]
	v_mfma_f32_16x16x32_bf16 v[72:75], v[156:159], v[164:167], v[72:75]
	s_setprio 0
	s_barrier
	s_add_i32 s34, 0, 0x1c000
	s_mov_b32 m0, s96
	v_add_u32_e32 v108, s34, v238
	v_lshl_add_u64 v[196:197], v[230:231], 0, s[44:45]
	ds_read_b128 v[80:83], v108
	ds_read_b128 v[84:87], v108 offset:1024
	ds_read_b128 v[104:107], v108 offset:2048
	ds_read_b128 v[108:111], v108 offset:3072
	global_load_lds_dwordx4 v[196:197], off
	v_lshl_add_u64 v[196:197], v[232:233], 0, s[44:45]
	s_mov_b32 m0, s97
	s_nop 0
	global_load_lds_dwordx4 v[196:197], off
	s_barrier
	s_waitcnt lgkmcnt(0)
	s_setprio 3
	s_waitcnt lgkmcnt(0)
	v_mfma_f32_16x16x32_bf16 v[140:143], v[80:83], v[184:187], v[140:143]
	v_mfma_f32_16x16x32_bf16 v[136:139], v[104:107], v[184:187], v[136:139]
	v_mfma_f32_16x16x32_bf16 v[116:119], v[80:83], v[176:179], v[116:119]
	v_mfma_f32_16x16x32_bf16 v[112:115], v[104:107], v[176:179], v[112:115]
	v_mfma_f32_16x16x32_bf16 v[92:95], v[80:83], v[168:171], v[92:95]
	v_mfma_f32_16x16x32_bf16 v[88:91], v[104:107], v[168:171], v[88:91]
	v_mfma_f32_16x16x32_bf16 v[68:71], v[80:83], v[160:163], v[68:71]
	v_mfma_f32_16x16x32_bf16 v[64:67], v[104:107], v[160:163], v[64:67]
	v_mfma_f32_16x16x32_bf16 v[140:143], v[84:87], v[188:191], v[140:143]
	v_mfma_f32_16x16x32_bf16 v[136:139], v[108:111], v[188:191], v[136:139]
	v_mfma_f32_16x16x32_bf16 v[116:119], v[84:87], v[180:183], v[116:119]
	v_mfma_f32_16x16x32_bf16 v[112:115], v[108:111], v[180:183], v[112:115]
	v_mfma_f32_16x16x32_bf16 v[92:95], v[84:87], v[172:175], v[92:95]
	v_mfma_f32_16x16x32_bf16 v[88:91], v[108:111], v[172:175], v[88:91]
	v_mfma_f32_16x16x32_bf16 v[68:71], v[84:87], v[164:167], v[68:71]
	v_mfma_f32_16x16x32_bf16 v[64:67], v[108:111], v[164:167], v[64:67]
	s_setprio 0
	s_mov_b32 m0, s48
	v_lshl_add_u64 v[192:193], v[192:193], 0, s[44:45]
	s_barrier
	ds_read_b128 v[160:163], v241 offset:49152
	ds_read_b128 v[164:167], v241 offset:50176
	ds_read_b128 v[168:171], v241 offset:51200
	ds_read_b128 v[172:175], v241 offset:52224
	ds_read_b128 v[176:179], v241 offset:53248
	ds_read_b128 v[180:183], v241 offset:54272
	ds_read_b128 v[184:187], v241 offset:55296
	ds_read_b128 v[188:191], v241 offset:56320
	global_load_lds_dwordx4 v[192:193], off
	v_lshl_add_u64 v[192:193], v[194:195], 0, s[44:45]
	s_mov_b32 m0, s49
	s_nop 0
	global_load_lds_dwordx4 v[192:193], off
	s_barrier
	s_waitcnt lgkmcnt(0)
	s_setprio 3
	s_waitcnt lgkmcnt(0)
	v_mfma_f32_16x16x32_bf16 v[60:63], v[128:131], v[160:163], v[60:63]
	v_mfma_f32_16x16x32_bf16 v[56:59], v[152:155], v[160:163], v[56:59]
	v_mfma_f32_16x16x32_bf16 v[36:39], v[128:131], v[168:171], v[36:39]
	v_mfma_f32_16x16x32_bf16 v[32:35], v[152:155], v[168:171], v[32:35]
	v_mfma_f32_16x16x32_bf16 v[20:23], v[128:131], v[176:179], v[20:23]
	v_mfma_f32_16x16x32_bf16 v[16:19], v[152:155], v[176:179], v[16:19]
	v_mfma_f32_16x16x32_bf16 v[4:7], v[128:131], v[184:187], v[4:7]
	v_mfma_f32_16x16x32_bf16 v[0:3], v[152:155], v[184:187], v[0:3]
	v_mfma_f32_16x16x32_bf16 v[60:63], v[132:135], v[164:167], v[60:63]
	v_mfma_f32_16x16x32_bf16 v[56:59], v[156:159], v[164:167], v[56:59]
	v_mfma_f32_16x16x32_bf16 v[36:39], v[132:135], v[172:175], v[36:39]
	v_mfma_f32_16x16x32_bf16 v[32:35], v[156:159], v[172:175], v[32:35]
	v_mfma_f32_16x16x32_bf16 v[20:23], v[132:135], v[180:183], v[20:23]
	v_mfma_f32_16x16x32_bf16 v[16:19], v[156:159], v[180:183], v[16:19]
	v_mfma_f32_16x16x32_bf16 v[4:7], v[132:135], v[188:191], v[4:7]
	v_mfma_f32_16x16x32_bf16 v[0:3], v[156:159], v[188:191], v[0:3]
	s_setprio 0
	s_barrier
	s_add_u32 s0, s30, 0x80080
	s_addc_u32 s1, s31, 0
	s_add_i32 s30, s34, s53
	v_lshl_add_u64 v[128:129], s[0:1], 0, v[202:203]
	s_mov_b32 m0, s30
	s_nop 0
	global_load_lds_dwordx4 v[128:129], off
	v_lshl_add_u64 v[128:129], s[0:1], 0, v[206:207]
	s_add_i32 m0, s30, 0x2000
	s_nop 0
	global_load_lds_dwordx4 v[128:129], off
	s_waitcnt vmcnt(6)
	s_barrier
	s_setprio 3
	v_mfma_f32_16x16x32_bf16 v[48:51], v[80:83], v[160:163], v[48:51]
	v_mfma_f32_16x16x32_bf16 v[52:55], v[104:107], v[160:163], v[52:55]
	v_mfma_f32_16x16x32_bf16 v[40:43], v[80:83], v[168:171], v[40:43]
	v_mfma_f32_16x16x32_bf16 v[44:47], v[104:107], v[168:171], v[44:47]
	v_mfma_f32_16x16x32_bf16 v[24:27], v[80:83], v[176:179], v[24:27]
	v_mfma_f32_16x16x32_bf16 v[28:31], v[104:107], v[176:179], v[28:31]
	v_mfma_f32_16x16x32_bf16 v[8:11], v[80:83], v[184:187], v[8:11]
	v_mfma_f32_16x16x32_bf16 v[12:15], v[104:107], v[184:187], v[12:15]
	v_mfma_f32_16x16x32_bf16 v[48:51], v[84:87], v[164:167], v[48:51]
	v_mfma_f32_16x16x32_bf16 v[52:55], v[108:111], v[164:167], v[52:55]
	v_mfma_f32_16x16x32_bf16 v[40:43], v[84:87], v[172:175], v[40:43]
	v_mfma_f32_16x16x32_bf16 v[44:47], v[108:111], v[172:175], v[44:47]
	v_mfma_f32_16x16x32_bf16 v[24:27], v[84:87], v[180:183], v[24:27]
	v_mfma_f32_16x16x32_bf16 v[28:31], v[108:111], v[180:183], v[28:31]
	v_mfma_f32_16x16x32_bf16 v[8:11], v[84:87], v[188:191], v[8:11]
	v_mfma_f32_16x16x32_bf16 v[12:15], v[108:111], v[188:191], v[12:15]
	s_setprio 0
	s_add_i32 s43, s43, 2
	s_add_u32 s28, s28, 0x100
	s_addc_u32 s29, s29, 0
	s_add_u32 s39, s39, 0x100
	s_addc_u32 s42, s42, 0
	s_cmp_gt_u32 s43, 29
	s_barrier
	s_cbranch_scc1 .LBB0_930
.LBB0_918:
	ds_read_b128 v[152:155], v240
	ds_read_b128 v[156:159], v240 offset:1024
	ds_read_b128 v[160:163], v240 offset:2048
	ds_read_b128 v[164:167], v240 offset:3072
	s_xor_b64 s[34:35], s[82:83], -1
	v_lshl_add_u64 v[80:81], s[28:29], 0, v[216:217]
	s_add_i32 m0, s60, 0xc000
	ds_read_b128 v[192:195], v241
	ds_read_b128 v[196:199], v241 offset:1024
	ds_read_b128 v[184:187], v241 offset:2048
	ds_read_b128 v[188:191], v241 offset:3072
	ds_read_b128 v[176:179], v241 offset:4096
	ds_read_b128 v[180:183], v241 offset:5120
	ds_read_b128 v[168:171], v241 offset:6144
	ds_read_b128 v[172:175], v241 offset:7168
	global_load_lds_dwordx4 v[80:81], off
	v_lshl_add_u64 v[80:81], s[28:29], 0, v[218:219]
	s_add_i32 m0, s60, 0xe000
	s_nop 0
	global_load_lds_dwordx4 v[80:81], off
	s_waitcnt lgkmcnt(8)
	s_barrier
	s_waitcnt lgkmcnt(0)
	s_setprio 3
	s_waitcnt lgkmcnt(0)
	v_mfma_f32_16x16x32_bf16 v[80:83], v[152:155], v[192:195], v[148:151]
	v_mfma_f32_16x16x32_bf16 v[84:87], v[160:163], v[192:195], v[144:147]
	v_mfma_f32_16x16x32_bf16 v[104:107], v[152:155], v[184:187], v[124:127]
	v_mfma_f32_16x16x32_bf16 v[108:111], v[160:163], v[184:187], v[120:123]
	v_mfma_f32_16x16x32_bf16 v[100:103], v[152:155], v[176:179], v[100:103]
	v_mfma_f32_16x16x32_bf16 v[96:99], v[160:163], v[176:179], v[96:99]
	v_mfma_f32_16x16x32_bf16 v[76:79], v[152:155], v[168:171], v[76:79]
	v_mfma_f32_16x16x32_bf16 v[72:75], v[160:163], v[168:171], v[72:75]
	v_mfma_f32_16x16x32_bf16 v[80:83], v[156:159], v[196:199], v[80:83]
	v_mfma_f32_16x16x32_bf16 v[84:87], v[164:167], v[196:199], v[84:87]
	v_mfma_f32_16x16x32_bf16 v[104:107], v[156:159], v[188:191], v[104:107]
	v_mfma_f32_16x16x32_bf16 v[108:111], v[164:167], v[188:191], v[108:111]
	v_mfma_f32_16x16x32_bf16 v[100:103], v[156:159], v[180:183], v[100:103]
	v_mfma_f32_16x16x32_bf16 v[96:99], v[164:167], v[180:183], v[96:99]
	v_mfma_f32_16x16x32_bf16 v[76:79], v[156:159], v[172:175], v[76:79]
	v_mfma_f32_16x16x32_bf16 v[72:75], v[164:167], v[172:175], v[72:75]
	s_setprio 0
	s_barrier
	ds_read_b128 v[120:123], v242
	ds_read_b128 v[124:127], v242 offset:1024
	ds_read_b128 v[128:131], v242 offset:2048
	ds_read_b128 v[132:135], v242 offset:3072
	s_and_b64 vcc, exec, s[34:35]
	s_cbranch_vccnz .LBB0_920
	v_add_u32_e32 v144, v237, v236
	ds_read2_b32 v[220:221], v144 offset1:32
	ds_read2_b32 v[222:223], v144 offset0:64 offset1:96
	ds_read2_b32 v[224:225], v144 offset0:128 offset1:160
	ds_read2_b32 v[226:227], v144 offset0:192 offset1:224

.LBB0_922:
	s_setprio 3
	s_waitcnt lgkmcnt(0)
	v_mfma_f32_16x16x32_bf16 v[140:143], v[120:123], v[192:195], v[140:143]
	v_mfma_f32_16x16x32_bf16 v[136:139], v[128:131], v[192:195], v[136:139]
	v_mfma_f32_16x16x32_bf16 v[116:119], v[120:123], v[184:187], v[116:119]
	v_mfma_f32_16x16x32_bf16 v[112:115], v[128:131], v[184:187], v[112:115]
	v_mfma_f32_16x16x32_bf16 v[92:95], v[120:123], v[176:179], v[92:95]
	v_mfma_f32_16x16x32_bf16 v[88:91], v[128:131], v[176:179], v[88:91]
	v_mfma_f32_16x16x32_bf16 v[68:71], v[120:123], v[168:171], v[68:71]
	v_mfma_f32_16x16x32_bf16 v[64:67], v[128:131], v[168:171], v[64:67]
	v_mfma_f32_16x16x32_bf16 v[140:143], v[124:127], v[196:199], v[140:143]
	v_mfma_f32_16x16x32_bf16 v[136:139], v[132:135], v[196:199], v[136:139]
	v_mfma_f32_16x16x32_bf16 v[116:119], v[124:127], v[188:191], v[116:119]
	v_mfma_f32_16x16x32_bf16 v[112:115], v[132:135], v[188:191], v[112:115]
	v_mfma_f32_16x16x32_bf16 v[92:95], v[124:127], v[180:183], v[92:95]
	v_mfma_f32_16x16x32_bf16 v[88:91], v[132:135], v[180:183], v[88:91]
	v_mfma_f32_16x16x32_bf16 v[68:71], v[124:127], v[172:175], v[68:71]
	v_mfma_f32_16x16x32_bf16 v[64:67], v[132:135], v[172:175], v[64:67]
	s_setprio 0
	s_barrier
	ds_read_b128 v[184:187], v241 offset:16384
	ds_read_b128 v[188:191], v241 offset:17408
	ds_read_b128 v[176:179], v241 offset:18432
	ds_read_b128 v[180:183], v241 offset:19456
	ds_read_b128 v[168:171], v241 offset:20480
	ds_read_b128 v[172:175], v241 offset:21504
	ds_read_b128 v[144:147], v241 offset:22528
	ds_read_b128 v[148:151], v241 offset:23552
	s_and_b64 vcc, exec, s[0:1]
	s_cbranch_vccnz .LBB0_924
	v_lshl_add_u64 v[192:193], v[212:213], 0, s[54:55]
	global_store_dwordx2 v[192:193], v[228:229], off
.LBB0_924:
	s_add_u32 s56, s28, 0xfff80080
	s_addc_u32 s57, s29, -1
	s_and_b64 s[0:1], s[36:37], exec
	s_cselect_b32 s1, s3, s57
	s_cselect_b32 s0, s4, s56
	s_mov_b32 m0, s60
	v_lshl_add_u64 v[192:193], s[0:1], 0, v[200:201]
	global_load_lds_dwordx4 v[192:193], off
	v_lshl_add_u64 v[194:195], s[0:1], 0, v[204:205]
	s_mov_b32 m0, s40
	s_nop 0
	global_load_lds_dwordx4 v[194:195], off
	s_barrier
	s_waitcnt lgkmcnt(0)
	s_setprio 3
	s_waitcnt lgkmcnt(0)
	v_mfma_f32_16x16x32_bf16 v[60:63], v[152:155], v[184:187], v[60:63]
	v_mfma_f32_16x16x32_bf16 v[56:59], v[160:163], v[184:187], v[56:59]
	v_mfma_f32_16x16x32_bf16 v[36:39], v[152:155], v[176:179], v[36:39]
	v_mfma_f32_16x16x32_bf16 v[32:35], v[160:163], v[176:179], v[32:35]
	v_mfma_f32_16x16x32_bf16 v[20:23], v[152:155], v[168:171], v[20:23]
	v_mfma_f32_16x16x32_bf16 v[16:19], v[160:163], v[168:171], v[16:19]
	v_mfma_f32_16x16x32_bf16 v[4:7], v[152:155], v[144:147], v[4:7]
	v_mfma_f32_16x16x32_bf16 v[0:3], v[160:163], v[144:147], v[0:3]
	v_mfma_f32_16x16x32_bf16 v[60:63], v[156:159], v[188:191], v[60:63]
	v_mfma_f32_16x16x32_bf16 v[56:59], v[164:167], v[188:191], v[56:59]
	v_mfma_f32_16x16x32_bf16 v[36:39], v[156:159], v[180:183], v[36:39]
	v_mfma_f32_16x16x32_bf16 v[32:35], v[164:167], v[180:183], v[32:35]
	v_mfma_f32_16x16x32_bf16 v[20:23], v[156:159], v[172:175], v[20:23]
	v_mfma_f32_16x16x32_bf16 v[16:19], v[164:167], v[172:175], v[16:19]
	v_mfma_f32_16x16x32_bf16 v[4:7], v[156:159], v[148:151], v[4:7]
	v_mfma_f32_16x16x32_bf16 v[0:3], v[164:167], v[148:151], v[0:3]
	s_setprio 0
	s_barrier
	s_add_u32 s36, s30, 0x80000
	s_addc_u32 s37, s31, 0
	s_mov_b32 m0, s41
	v_lshl_add_u64 v[152:153], s[36:37], 0, v[202:203]
	global_load_lds_dwordx4 v[152:153], off
	v_lshl_add_u64 v[152:153], s[36:37], 0, v[206:207]
	s_mov_b32 m0, s52
	s_mov_b64 s[36:37], -1
	global_load_lds_dwordx4 v[152:153], off
	s_and_b64 vcc, exec, s[34:35]
	s_cbranch_vccz .LBB0_926
	s_waitcnt vmcnt(6)
	s_mov_b64 s[36:37], 0

;     __device__ __forceinline__ void decode(int j, size_t& soff, int& sld, size_t& doff) const {
;         if (gu) { const int e = j >> 11, r = j & 2047, nt = r >> 4, kt = r & 15, n0 = nt * 32, w = n0 & 255, tile = n0 >> 8;
;             const int sc = (w < 128) ? 128 * tile + w : 2048 + 128 * tile + (w - 128);
;             sld = 4096; soff = (size_t)e * 2048 * 4096 + (size_t)(kt * 128) * 4096 + sc; doff = (size_t)e * 4096 * 2048 + (size_t)n0 * 2048 + kt * 128; }
.LBB0_928:
	s_barrier
	s_setprio 3
	v_mfma_f32_16x16x32_bf16 v[48:51], v[120:123], v[184:187], v[48:51]
	v_mfma_f32_16x16x32_bf16 v[52:55], v[128:131], v[184:187], v[52:55]
	v_mfma_f32_16x16x32_bf16 v[40:43], v[120:123], v[176:179], v[40:43]
	v_mfma_f32_16x16x32_bf16 v[44:47], v[128:131], v[176:179], v[44:47]
	v_mfma_f32_16x16x32_bf16 v[24:27], v[120:123], v[168:171], v[24:27]
	v_mfma_f32_16x16x32_bf16 v[28:31], v[128:131], v[168:171], v[28:31]
	v_mfma_f32_16x16x32_bf16 v[8:11], v[120:123], v[144:147], v[8:11]
	v_mfma_f32_16x16x32_bf16 v[12:15], v[128:131], v[144:147], v[12:15]
	v_mfma_f32_16x16x32_bf16 v[48:51], v[124:127], v[188:191], v[48:51]
	v_mfma_f32_16x16x32_bf16 v[52:55], v[132:135], v[188:191], v[52:55]
	v_mfma_f32_16x16x32_bf16 v[40:43], v[124:127], v[180:183], v[40:43]
	v_mfma_f32_16x16x32_bf16 v[44:47], v[132:135], v[180:183], v[44:47]
	v_mfma_f32_16x16x32_bf16 v[24:27], v[124:127], v[172:175], v[24:27]
	v_mfma_f32_16x16x32_bf16 v[28:31], v[132:135], v[172:175], v[28:31]
	v_mfma_f32_16x16x32_bf16 v[8:11], v[124:127], v[148:151], v[8:11]
	v_mfma_f32_16x16x32_bf16 v[12:15], v[132:135], v[148:151], v[12:15]
	s_setprio 0
	v_add_u32_e32 v120, 0x18000, v239
	s_barrier
	ds_read_b128 v[128:131], v120
	ds_read_b128 v[132:135], v120 offset:1024
	ds_read_b128 v[152:155], v120 offset:2048
	ds_read_b128 v[156:159], v120 offset:3072
	ds_read_b128 v[184:187], v241 offset:32768
	ds_read_b128 v[188:191], v241 offset:33792
	ds_read_b128 v[176:179], v241 offset:34816
	ds_read_b128 v[180:183], v241 offset:35840
	ds_read_b128 v[168:171], v241 offset:36864
	ds_read_b128 v[172:175], v241 offset:37888
	ds_read_b128 v[160:163], v241 offset:38912
	ds_read_b128 v[164:167], v241 offset:39936
	s_add_i32 s34, s62, s63
	s_mul_i32 s34, s34, s19
	s_add_i32 s34, s34, s18
	s_cmp_lt_i32 s34, 0xa000
	s_cselect_b64 s[82:83], -1, 0
	s_cmp_gt_i32 s34, 0x9fff
	s_cbranch_scc1 .LBB0_917
	s_lshl_b32 s35, s34, 1
	s_and_b32 s35, s35, 0xe0
	s_and_b32 s37, s34, 0x780
	s_or_b32 s54, s35, s37
	s_add_i32 s37, s37, s35
	s_ashr_i32 s36, s34, 11
	s_addk_i32 s37, 0x780
	s_cmpk_lt_u32 s35, 0x80
	s_cselect_b32 s35, s54, s37
	s_ashr_i32 s37, s36, 31
	s_lshl_b64 s[54:55], s[36:37], 23
	s_lshl_b32 s36, s34, 7
	s_and_b32 s56, s36, 0x780
	s_lshl_b32 s36, s56, 12
	s_or_b32 s35, s35, s36
	s_or_b32 s36, s54, s35
	s_mov_b32 s37, s55
	v_lshl_add_u64 v[120:121], s[36:37], 2, v[214:215]
	s_add_i32 m0, s84, 0x20000
	s_mov_b64 s[36:37], 0x20000
	global_load_lds_dwordx4 v[120:121], off nt
	v_lshl_add_u64 v[120:121], v[120:121], 0, s[36:37]
	s_mov_b32 m0, s85
	s_lshl_b32 s34, s34, 12
	global_load_lds_dwordx4 v[120:121], off nt
	s_and_b32 s34, s34, 0x7f0000
	s_or_b32 s34, s56, s34
	s_or_b32 s54, s54, s34
	s_add_i32 s62, s62, 1
	s_branch .LBB0_917

.LBB0_2052:
	s_add_u32 s0, s0, 0x80000
	s_addc_u32 s1, s1, 0
	s_mov_b32 m0, s65
	v_lshl_add_u64 v[176:177], s[0:1], 0, v[192:193]
	global_load_lds_dwordx4 v[176:177], off
	v_lshl_add_u64 v[176:177], s[0:1], 0, v[196:197]
	s_mov_b32 m0, s66
	s_nop 0
	global_load_lds_dwordx4 v[176:177], off
	s_waitcnt lgkmcnt(8)
	s_barrier
	s_waitcnt lgkmcnt(0)
	s_setprio 3
	s_waitcnt lgkmcnt(0)
	v_mfma_f32_16x16x32_bf16 v[124:127], v[128:131], v[168:171], v[124:127]
	v_mfma_f32_16x16x32_bf16 v[120:123], v[136:139], v[168:171], v[120:123]
	v_mfma_f32_16x16x32_bf16 v[116:119], v[128:131], v[160:163], v[116:119]
	v_mfma_f32_16x16x32_bf16 v[112:115], v[136:139], v[160:163], v[112:115]
	v_mfma_f32_16x16x32_bf16 v[100:103], v[128:131], v[152:155], v[100:103]
	v_mfma_f32_16x16x32_bf16 v[96:99], v[136:139], v[152:155], v[96:99]
	v_mfma_f32_16x16x32_bf16 v[84:87], v[128:131], v[144:147], v[84:87]
	v_mfma_f32_16x16x32_bf16 v[80:83], v[136:139], v[144:147], v[80:83]
	v_mfma_f32_16x16x32_bf16 v[124:127], v[132:135], v[172:175], v[124:127]
	v_mfma_f32_16x16x32_bf16 v[120:123], v[140:143], v[172:175], v[120:123]
	v_mfma_f32_16x16x32_bf16 v[116:119], v[132:135], v[164:167], v[116:119]
	v_mfma_f32_16x16x32_bf16 v[112:115], v[140:143], v[164:167], v[112:115]
	v_mfma_f32_16x16x32_bf16 v[100:103], v[132:135], v[156:159], v[100:103]
	v_mfma_f32_16x16x32_bf16 v[96:99], v[140:143], v[156:159], v[96:99]
	v_mfma_f32_16x16x32_bf16 v[84:87], v[132:135], v[148:151], v[84:87]
	v_mfma_f32_16x16x32_bf16 v[80:83], v[140:143], v[148:151], v[80:83]
	s_setprio 0
	s_barrier
	s_add_i32 s48, 0, 0x1c000
	s_mov_b32 m0, s76
	v_add_u32_e32 v188, s48, v232
	v_lshl_add_u64 v[222:223], v[222:223], 0, s[10:11]
	ds_read_b128 v[176:179], v188
	ds_read_b128 v[180:183], v188 offset:1024
	ds_read_b128 v[184:187], v188 offset:2048
	ds_read_b128 v[188:191], v188 offset:3072
	global_load_lds_dwordx4 v[222:223], off
	v_lshl_add_u64 v[222:223], v[224:225], 0, s[10:11]
	s_mov_b32 m0, s77
	s_nop 0
	global_load_lds_dwordx4 v[222:223], off
	s_barrier
	s_waitcnt lgkmcnt(0)
	s_setprio 3
	s_waitcnt lgkmcnt(0)
	v_mfma_f32_16x16x32_bf16 v[108:111], v[176:179], v[168:171], v[108:111]
	v_mfma_f32_16x16x32_bf16 v[104:107], v[184:187], v[168:171], v[104:107]
	v_mfma_f32_16x16x32_bf16 v[92:95], v[176:179], v[160:163], v[92:95]
	v_mfma_f32_16x16x32_bf16 v[88:91], v[184:187], v[160:163], v[88:91]
	v_mfma_f32_16x16x32_bf16 v[76:79], v[176:179], v[152:155], v[76:79]
	v_mfma_f32_16x16x32_bf16 v[72:75], v[184:187], v[152:155], v[72:75]
	v_mfma_f32_16x16x32_bf16 v[68:71], v[176:179], v[144:147], v[68:71]
	v_mfma_f32_16x16x32_bf16 v[64:67], v[184:187], v[144:147], v[64:67]
	v_mfma_f32_16x16x32_bf16 v[108:111], v[180:183], v[172:175], v[108:111]
	v_mfma_f32_16x16x32_bf16 v[104:107], v[188:191], v[172:175], v[104:107]
	v_mfma_f32_16x16x32_bf16 v[92:95], v[180:183], v[164:167], v[92:95]
	v_mfma_f32_16x16x32_bf16 v[88:91], v[188:191], v[164:167], v[88:91]
	v_mfma_f32_16x16x32_bf16 v[76:79], v[180:183], v[156:159], v[76:79]
	v_mfma_f32_16x16x32_bf16 v[72:75], v[188:191], v[156:159], v[72:75]
	v_mfma_f32_16x16x32_bf16 v[68:71], v[180:183], v[148:151], v[68:71]
	v_mfma_f32_16x16x32_bf16 v[64:67], v[188:191], v[148:151], v[64:67]
	s_setprio 0
	s_mov_b32 m0, s78
	v_lshl_add_u64 v[222:223], v[226:227], 0, s[10:11]
	s_barrier
	ds_read_b128 v[144:147], v235 offset:49152
	ds_read_b128 v[148:151], v235 offset:50176
	ds_read_b128 v[152:155], v235 offset:51200
	ds_read_b128 v[156:159], v235 offset:52224
	ds_read_b128 v[160:163], v235 offset:53248
	ds_read_b128 v[164:167], v235 offset:54272
	ds_read_b128 v[168:171], v235 offset:55296
	ds_read_b128 v[172:175], v235 offset:56320
	global_load_lds_dwordx4 v[222:223], off
	v_lshl_add_u64 v[222:223], v[228:229], 0, s[10:11]
	s_mov_b32 m0, s79
	s_nop 0
	global_load_lds_dwordx4 v[222:223], off
	s_barrier
	s_waitcnt lgkmcnt(0)
	s_setprio 3
	s_waitcnt lgkmcnt(0)
	v_mfma_f32_16x16x32_bf16 v[60:63], v[128:131], v[144:147], v[60:63]
	v_mfma_f32_16x16x32_bf16 v[52:55], v[136:139], v[144:147], v[52:55]
	v_mfma_f32_16x16x32_bf16 v[44:47], v[128:131], v[152:155], v[44:47]
	v_mfma_f32_16x16x32_bf16 v[32:35], v[136:139], v[152:155], v[32:35]
	v_mfma_f32_16x16x32_bf16 v[20:23], v[128:131], v[160:163], v[20:23]
	v_mfma_f32_16x16x32_bf16 v[16:19], v[136:139], v[160:163], v[16:19]
	v_mfma_f32_16x16x32_bf16 v[4:7], v[128:131], v[168:171], v[4:7]
	v_mfma_f32_16x16x32_bf16 v[0:3], v[136:139], v[168:171], v[0:3]
	v_mfma_f32_16x16x32_bf16 v[60:63], v[132:135], v[148:151], v[60:63]
	v_mfma_f32_16x16x32_bf16 v[52:55], v[140:143], v[148:151], v[52:55]
	v_mfma_f32_16x16x32_bf16 v[44:47], v[132:135], v[156:159], v[44:47]
	v_mfma_f32_16x16x32_bf16 v[32:35], v[140:143], v[156:159], v[32:35]
	v_mfma_f32_16x16x32_bf16 v[20:23], v[132:135], v[164:167], v[20:23]
	v_mfma_f32_16x16x32_bf16 v[16:19], v[140:143], v[164:167], v[16:19]
	v_mfma_f32_16x16x32_bf16 v[4:7], v[132:135], v[172:175], v[4:7]
	v_mfma_f32_16x16x32_bf16 v[0:3], v[140:143], v[172:175], v[0:3]
	s_setprio 0
	s_barrier
	s_add_u32 s0, s44, 0x80080
	s_addc_u32 s1, s45, 0
	s_add_i32 s44, s48, s58
	v_lshl_add_u64 v[128:129], s[0:1], 0, v[194:195]
	s_mov_b32 m0, s44
	s_nop 0
	global_load_lds_dwordx4 v[128:129], off
	v_lshl_add_u64 v[128:129], s[0:1], 0, v[198:199]
	s_add_i32 m0, s44, 0x2000
	s_nop 0
	global_load_lds_dwordx4 v[128:129], off
	s_waitcnt vmcnt(6)
	s_barrier
	s_setprio 3
	v_mfma_f32_16x16x32_bf16 v[56:59], v[176:179], v[144:147], v[56:59]
	v_mfma_f32_16x16x32_bf16 v[48:51], v[184:187], v[144:147], v[48:51]
	v_mfma_f32_16x16x32_bf16 v[40:43], v[176:179], v[152:155], v[40:43]
	v_mfma_f32_16x16x32_bf16 v[36:39], v[184:187], v[152:155], v[36:39]
	v_mfma_f32_16x16x32_bf16 v[28:31], v[176:179], v[160:163], v[28:31]
	v_mfma_f32_16x16x32_bf16 v[24:27], v[184:187], v[160:163], v[24:27]
	v_mfma_f32_16x16x32_bf16 v[12:15], v[176:179], v[168:171], v[12:15]
	v_mfma_f32_16x16x32_bf16 v[8:11], v[184:187], v[168:171], v[8:11]
	v_mfma_f32_16x16x32_bf16 v[56:59], v[180:183], v[148:151], v[56:59]
	v_mfma_f32_16x16x32_bf16 v[48:51], v[188:191], v[148:151], v[48:51]
	v_mfma_f32_16x16x32_bf16 v[40:43], v[180:183], v[156:159], v[40:43]
	v_mfma_f32_16x16x32_bf16 v[36:39], v[188:191], v[156:159], v[36:39]
	v_mfma_f32_16x16x32_bf16 v[28:31], v[180:183], v[164:167], v[28:31]
	v_mfma_f32_16x16x32_bf16 v[24:27], v[188:191], v[164:167], v[24:27]
	v_mfma_f32_16x16x32_bf16 v[12:15], v[180:183], v[172:175], v[12:15]
	v_mfma_f32_16x16x32_bf16 v[8:11], v[188:191], v[172:175], v[8:11]
	s_setprio 0
	s_add_i32 s91, s91, 2
	s_add_u32 s42, s42, 0x100
	s_addc_u32 s43, s43, 0
	s_add_u32 s29, s29, 0x100
	s_addc_u32 s41, s41, 0
	s_cmp_gt_u32 s91, 29
	s_barrier
	s_cbranch_scc1 .LBB0_2065
.LBB0_2053:
	ds_read_b128 v[144:147], v234
	ds_read_b128 v[148:151], v234 offset:1024
	ds_read_b128 v[152:155], v234 offset:2048
	ds_read_b128 v[156:159], v234 offset:3072
	s_xor_b64 s[48:49], s[38:39], -1
	v_lshl_add_u64 v[128:129], s[42:43], 0, v[208:209]
	s_add_i32 m0, s59, 0xc000
	ds_read_b128 v[184:187], v235
	ds_read_b128 v[188:191], v235 offset:1024
	ds_read_b128 v[176:179], v235 offset:2048
	ds_read_b128 v[180:183], v235 offset:3072
	ds_read_b128 v[168:171], v235 offset:4096
	ds_read_b128 v[172:175], v235 offset:5120
	ds_read_b128 v[160:163], v235 offset:6144
	ds_read_b128 v[164:167], v235 offset:7168
	global_load_lds_dwordx4 v[128:129], off
	v_lshl_add_u64 v[128:129], s[42:43], 0, v[210:211]
	s_add_i32 m0, s59, 0xe000
	s_nop 0
	global_load_lds_dwordx4 v[128:129], off
	s_waitcnt lgkmcnt(8)
	s_barrier
	s_waitcnt lgkmcnt(0)
	s_setprio 3
	s_waitcnt lgkmcnt(0)
	v_mfma_f32_16x16x32_bf16 v[124:127], v[144:147], v[184:187], v[124:127]
	v_mfma_f32_16x16x32_bf16 v[120:123], v[152:155], v[184:187], v[120:123]
	v_mfma_f32_16x16x32_bf16 v[116:119], v[144:147], v[176:179], v[116:119]
	v_mfma_f32_16x16x32_bf16 v[112:115], v[152:155], v[176:179], v[112:115]
	v_mfma_f32_16x16x32_bf16 v[100:103], v[144:147], v[168:171], v[100:103]
	v_mfma_f32_16x16x32_bf16 v[96:99], v[152:155], v[168:171], v[96:99]
	v_mfma_f32_16x16x32_bf16 v[84:87], v[144:147], v[160:163], v[84:87]
	v_mfma_f32_16x16x32_bf16 v[80:83], v[152:155], v[160:163], v[80:83]
	v_mfma_f32_16x16x32_bf16 v[124:127], v[148:151], v[188:191], v[124:127]
	v_mfma_f32_16x16x32_bf16 v[120:123], v[156:159], v[188:191], v[120:123]
	v_mfma_f32_16x16x32_bf16 v[116:119], v[148:151], v[180:183], v[116:119]
	v_mfma_f32_16x16x32_bf16 v[112:115], v[156:159], v[180:183], v[112:115]
	v_mfma_f32_16x16x32_bf16 v[100:103], v[148:151], v[172:175], v[100:103]
	v_mfma_f32_16x16x32_bf16 v[96:99], v[156:159], v[172:175], v[96:99]
	v_mfma_f32_16x16x32_bf16 v[84:87], v[148:151], v[164:167], v[84:87]
	v_mfma_f32_16x16x32_bf16 v[80:83], v[156:159], v[164:167], v[80:83]
	s_setprio 0
	s_barrier
	ds_read_b128 v[128:131], v236
	ds_read_b128 v[132:135], v236 offset:1024
	ds_read_b128 v[136:139], v236 offset:2048
	ds_read_b128 v[140:143], v236 offset:3072
	s_and_b64 vcc, exec, s[48:49]
	s_cbranch_vccnz .LBB0_2055
	v_add_u32_e32 v218, v231, v230
	ds_read2_b32 v[212:213], v218 offset1:32
	ds_read2_b32 v[214:215], v218 offset0:64 offset1:96
	ds_read2_b32 v[216:217], v218 offset0:128 offset1:160
	ds_read2_b32 v[218:219], v218 offset0:192 offset1:224

.LBB0_2057:
	s_setprio 3
	s_waitcnt lgkmcnt(0)
	v_mfma_f32_16x16x32_bf16 v[108:111], v[128:131], v[184:187], v[108:111]
	v_mfma_f32_16x16x32_bf16 v[104:107], v[136:139], v[184:187], v[104:107]
	v_mfma_f32_16x16x32_bf16 v[92:95], v[128:131], v[176:179], v[92:95]
	v_mfma_f32_16x16x32_bf16 v[88:91], v[136:139], v[176:179], v[88:91]
	v_mfma_f32_16x16x32_bf16 v[76:79], v[128:131], v[168:171], v[76:79]
	v_mfma_f32_16x16x32_bf16 v[72:75], v[136:139], v[168:171], v[72:75]
	v_mfma_f32_16x16x32_bf16 v[68:71], v[128:131], v[160:163], v[68:71]
	v_mfma_f32_16x16x32_bf16 v[64:67], v[136:139], v[160:163], v[64:67]
	v_mfma_f32_16x16x32_bf16 v[108:111], v[132:135], v[188:191], v[108:111]
	v_mfma_f32_16x16x32_bf16 v[104:107], v[140:143], v[188:191], v[104:107]
	v_mfma_f32_16x16x32_bf16 v[92:95], v[132:135], v[180:183], v[92:95]
	v_mfma_f32_16x16x32_bf16 v[88:91], v[140:143], v[180:183], v[88:91]
	v_mfma_f32_16x16x32_bf16 v[76:79], v[132:135], v[172:175], v[76:79]
	v_mfma_f32_16x16x32_bf16 v[72:75], v[140:143], v[172:175], v[72:75]
	v_mfma_f32_16x16x32_bf16 v[68:71], v[132:135], v[164:167], v[68:71]
	v_mfma_f32_16x16x32_bf16 v[64:67], v[140:143], v[164:167], v[64:67]
	s_setprio 0
	s_barrier
	ds_read_b128 v[184:187], v235 offset:16384
	ds_read_b128 v[188:191], v235 offset:17408
	ds_read_b128 v[176:179], v235 offset:18432
	ds_read_b128 v[180:183], v235 offset:19456
	ds_read_b128 v[168:171], v235 offset:20480
	ds_read_b128 v[172:175], v235 offset:21504
	ds_read_b128 v[160:163], v235 offset:22528
	ds_read_b128 v[164:167], v235 offset:23552
	s_and_b64 vcc, exec, s[0:1]
	s_cbranch_vccnz .LBB0_2059
	v_lshl_add_u64 v[226:227], v[204:205], 0, s[12:13]
	global_store_dwordx2 v[226:227], v[220:221], off
.LBB0_2059:
	s_add_u32 s38, s42, 0xfff80080
	s_addc_u32 s39, s43, -1
	s_and_b64 s[0:1], s[54:55], exec
	s_cselect_b32 s1, s35, s39
	s_cselect_b32 s0, s34, s38
	s_mov_b32 m0, s59
	v_lshl_add_u64 v[226:227], s[0:1], 0, v[192:193]
	global_load_lds_dwordx4 v[226:227], off
	v_lshl_add_u64 v[228:229], s[0:1], 0, v[196:197]
	s_mov_b32 m0, s62
	s_nop 0
	global_load_lds_dwordx4 v[228:229], off
	s_barrier
	s_waitcnt lgkmcnt(0)
	s_setprio 3
	s_waitcnt lgkmcnt(0)
	v_mfma_f32_16x16x32_bf16 v[60:63], v[144:147], v[184:187], v[60:63]
	v_mfma_f32_16x16x32_bf16 v[52:55], v[152:155], v[184:187], v[52:55]
	v_mfma_f32_16x16x32_bf16 v[44:47], v[144:147], v[176:179], v[44:47]
	v_mfma_f32_16x16x32_bf16 v[32:35], v[152:155], v[176:179], v[32:35]
	v_mfma_f32_16x16x32_bf16 v[20:23], v[144:147], v[168:171], v[20:23]
	v_mfma_f32_16x16x32_bf16 v[16:19], v[152:155], v[168:171], v[16:19]
	v_mfma_f32_16x16x32_bf16 v[4:7], v[144:147], v[160:163], v[4:7]
	v_mfma_f32_16x16x32_bf16 v[0:3], v[152:155], v[160:163], v[0:3]
	v_mfma_f32_16x16x32_bf16 v[60:63], v[148:151], v[188:191], v[60:63]
	v_mfma_f32_16x16x32_bf16 v[52:55], v[156:159], v[188:191], v[52:55]
	v_mfma_f32_16x16x32_bf16 v[44:47], v[148:151], v[180:183], v[44:47]
	v_mfma_f32_16x16x32_bf16 v[32:35], v[156:159], v[180:183], v[32:35]
	v_mfma_f32_16x16x32_bf16 v[20:23], v[148:151], v[172:175], v[20:23]
	v_mfma_f32_16x16x32_bf16 v[16:19], v[156:159], v[172:175], v[16:19]
	v_mfma_f32_16x16x32_bf16 v[4:7], v[148:151], v[164:167], v[4:7]
	v_mfma_f32_16x16x32_bf16 v[0:3], v[156:159], v[164:167], v[0:3]
	s_setprio 0
	s_barrier
	s_add_u32 s38, s44, 0x80000
	s_addc_u32 s39, s45, 0
	s_mov_b32 m0, s63
	v_lshl_add_u64 v[144:145], s[38:39], 0, v[194:195]
	global_load_lds_dwordx4 v[144:145], off
	v_lshl_add_u64 v[144:145], s[38:39], 0, v[198:199]
	s_mov_b32 m0, s64
	s_mov_b64 s[38:39], -1
	global_load_lds_dwordx4 v[144:145], off
	s_and_b64 vcc, exec, s[48:49]
	s_cbranch_vccz .LBB0_2061
	s_waitcnt vmcnt(6)
	s_mov_b64 s[38:39], 0

;     __device__ __forceinline__ void decode(int j, size_t& soff, int& sld, size_t& doff) const {
;         if (gu) { const int e = j >> 11, r = j & 2047, nt = r >> 4, kt = r & 15, n0 = nt * 32, w = n0 & 255, tile = n0 >> 8;
;             const int sc = (w < 128) ? 128 * tile + w : 2048 + 128 * tile + (w - 128);
;             sld = 4096; soff = (size_t)e * 2048 * 4096 + (size_t)(kt * 128) * 4096 + sc; doff = (size_t)e * 4096 * 2048 + (size_t)n0 * 2048 + kt * 128; }
.LBB0_2063:
	s_barrier
	s_setprio 3
	v_mfma_f32_16x16x32_bf16 v[56:59], v[128:131], v[184:187], v[56:59]
	v_mfma_f32_16x16x32_bf16 v[48:51], v[136:139], v[184:187], v[48:51]
	v_mfma_f32_16x16x32_bf16 v[40:43], v[128:131], v[176:179], v[40:43]
	v_mfma_f32_16x16x32_bf16 v[36:39], v[136:139], v[176:179], v[36:39]
	v_mfma_f32_16x16x32_bf16 v[28:31], v[128:131], v[168:171], v[28:31]
	v_mfma_f32_16x16x32_bf16 v[24:27], v[136:139], v[168:171], v[24:27]
	v_mfma_f32_16x16x32_bf16 v[12:15], v[128:131], v[160:163], v[12:15]
	v_mfma_f32_16x16x32_bf16 v[8:11], v[136:139], v[160:163], v[8:11]
	v_mfma_f32_16x16x32_bf16 v[56:59], v[132:135], v[188:191], v[56:59]
	v_mfma_f32_16x16x32_bf16 v[48:51], v[140:143], v[188:191], v[48:51]
	v_mfma_f32_16x16x32_bf16 v[40:43], v[132:135], v[180:183], v[40:43]
	v_mfma_f32_16x16x32_bf16 v[36:39], v[140:143], v[180:183], v[36:39]
	v_mfma_f32_16x16x32_bf16 v[28:31], v[132:135], v[172:175], v[28:31]
	v_mfma_f32_16x16x32_bf16 v[24:27], v[140:143], v[172:175], v[24:27]
	v_mfma_f32_16x16x32_bf16 v[12:15], v[132:135], v[164:167], v[12:15]
	v_mfma_f32_16x16x32_bf16 v[8:11], v[140:143], v[164:167], v[8:11]
	s_setprio 0
	v_add_u32_e32 v140, 0x18000, v233
	s_barrier
	ds_read_b128 v[128:131], v140
	ds_read_b128 v[132:135], v140 offset:1024
	ds_read_b128 v[136:139], v140 offset:2048
	ds_read_b128 v[140:143], v140 offset:3072
	ds_read_b128 v[168:171], v235 offset:32768
	ds_read_b128 v[172:175], v235 offset:33792
	ds_read_b128 v[160:163], v235 offset:34816
	ds_read_b128 v[164:167], v235 offset:35840
	ds_read_b128 v[152:155], v235 offset:36864
	ds_read_b128 v[156:159], v235 offset:37888
	ds_read_b128 v[144:147], v235 offset:38912
	ds_read_b128 v[148:151], v235 offset:39936
	s_mul_i32 s38, s80, s19
	s_add_i32 s48, s33, s38
	s_cmp_lt_i32 s48, 0x10000
	s_cselect_b64 s[38:39], -1, 0
	s_cmp_gt_i32 s48, 0xffff
	s_cbranch_scc1 .LBB0_2052
	s_lshl_b32 s13, s48, 1
	s_and_b32 s13, s13, 0xe0
	s_and_b32 s49, s48, 0x780
	s_or_b32 s54, s13, s49
	s_add_i32 s49, s49, s13
	s_ashr_i32 s12, s48, 11
	s_addk_i32 s49, 0x780
	s_cmpk_lt_u32 s13, 0x80
	s_cselect_b32 s49, s54, s49
	s_lshl_b32 s54, s48, 7
	s_and_b32 s92, s54, 0x780
	s_ashr_i32 s13, s12, 31
	s_lshl_b32 s54, s92, 12
	s_lshl_b64 s[12:13], s[12:13], 23
	s_or_b32 s49, s49, s54
	s_or_b32 s54, s12, s49
	s_mov_b32 s55, s13
	v_lshl_add_u64 v[176:177], s[54:55], 2, v[206:207]
	s_add_i32 m0, s82, 0x20000
	s_lshl_b32 s48, s48, 12
	global_load_lds_dwordx4 v[176:177], off nt
	v_lshl_add_u64 v[176:177], v[176:177], 0, s[14:15]
	s_mov_b32 m0, s83
	s_and_b32 s48, s48, 0x7f0000
	global_load_lds_dwordx4 v[176:177], off nt
	s_or_b32 s48, s92, s48
	s_or_b32 s12, s12, s48
	s_add_i32 s80, s80, 1
	s_branch .LBB0_2052

.LBB0_2168:
	ds_read_b128 v[156:159], v145
	ds_read_b128 v[160:163], v145 offset:1024
	ds_read_b128 v[164:167], v145 offset:2048
	ds_read_b128 v[168:171], v145 offset:3072
	s_add_u32 s28, s16, 0xfff80080
	s_addc_u32 s29, s17, -1
	s_cmp_eq_u32 s56, 28
	s_cselect_b32 s31, s13, s29
	s_cselect_b32 s30, s12, s28
	s_cselect_b32 s29, s15, s55
	s_cselect_b32 s28, s14, s54
	v_lshl_add_u64 v[142:143], s[16:17], 0, v[136:137]
	s_add_i32 m0, s38, 0xc000
	ds_read_b128 v[172:175], v146
	ds_read_b128 v[176:179], v146 offset:1024
	ds_read_b128 v[180:183], v146 offset:2048
	ds_read_b128 v[184:187], v146 offset:3072
	ds_read_b128 v[188:191], v146 offset:4096
	ds_read_b128 v[192:195], v146 offset:5120
	ds_read_b128 v[196:199], v146 offset:6144
	ds_read_b128 v[200:203], v146 offset:7168
	global_load_lds_dwordx4 v[142:143], off
	v_lshl_add_u64 v[142:143], s[16:17], 0, v[138:139]
	s_add_i32 m0, s38, 0xe000
	s_nop 0
	global_load_lds_dwordx4 v[142:143], off
	s_waitcnt lgkmcnt(8)
	s_barrier
	s_waitcnt lgkmcnt(0)
	s_setprio 3
	s_waitcnt lgkmcnt(0)
	v_mfma_f32_16x16x32_bf16 v[124:127], v[156:159], v[172:175], v[124:127]
	v_mfma_f32_16x16x32_bf16 v[120:123], v[164:167], v[172:175], v[120:123]
	v_mfma_f32_16x16x32_bf16 v[108:111], v[156:159], v[180:183], v[108:111]
	v_mfma_f32_16x16x32_bf16 v[104:107], v[164:167], v[180:183], v[104:107]
	v_mfma_f32_16x16x32_bf16 v[92:95], v[156:159], v[188:191], v[92:95]
	v_mfma_f32_16x16x32_bf16 v[88:91], v[164:167], v[188:191], v[88:91]
	v_mfma_f32_16x16x32_bf16 v[76:79], v[156:159], v[196:199], v[76:79]
	v_mfma_f32_16x16x32_bf16 v[72:75], v[164:167], v[196:199], v[72:75]
	v_mfma_f32_16x16x32_bf16 v[124:127], v[160:163], v[176:179], v[124:127]
	v_mfma_f32_16x16x32_bf16 v[120:123], v[168:171], v[176:179], v[120:123]
	v_mfma_f32_16x16x32_bf16 v[108:111], v[160:163], v[184:187], v[108:111]
	v_mfma_f32_16x16x32_bf16 v[104:107], v[168:171], v[184:187], v[104:107]
	v_mfma_f32_16x16x32_bf16 v[92:95], v[160:163], v[192:195], v[92:95]
	v_mfma_f32_16x16x32_bf16 v[88:91], v[168:171], v[192:195], v[88:91]
	v_mfma_f32_16x16x32_bf16 v[76:79], v[160:163], v[200:203], v[76:79]
	v_mfma_f32_16x16x32_bf16 v[72:75], v[168:171], v[200:203], v[72:75]
	s_setprio 0
	s_barrier
	s_add_i32 s57, s45, s37
	v_lshl_add_u64 v[142:143], s[28:29], 0, v[130:131]
	s_mov_b32 m0, s57
	ds_read_b128 v[204:207], v147
	ds_read_b128 v[208:211], v147 offset:1024
	ds_read_b128 v[212:215], v147 offset:2048
	ds_read_b128 v[216:219], v147 offset:3072
	global_load_lds_dwordx4 v[142:143], off
	v_lshl_add_u64 v[220:221], s[28:29], 0, v[134:135]
	s_add_i32 m0, s57, 0x2000
	s_nop 0
	global_load_lds_dwordx4 v[220:221], off
	s_barrier
	s_waitcnt lgkmcnt(0)
	s_setprio 3
	s_waitcnt lgkmcnt(0)
	v_mfma_f32_16x16x32_bf16 v[116:119], v[204:207], v[172:175], v[116:119]
	v_mfma_f32_16x16x32_bf16 v[112:115], v[212:215], v[172:175], v[112:115]
	v_mfma_f32_16x16x32_bf16 v[100:103], v[204:207], v[180:183], v[100:103]
	v_mfma_f32_16x16x32_bf16 v[96:99], v[212:215], v[180:183], v[96:99]
	v_mfma_f32_16x16x32_bf16 v[84:87], v[204:207], v[188:191], v[84:87]
	v_mfma_f32_16x16x32_bf16 v[80:83], v[212:215], v[188:191], v[80:83]
	v_mfma_f32_16x16x32_bf16 v[68:71], v[204:207], v[196:199], v[68:71]
	v_mfma_f32_16x16x32_bf16 v[64:67], v[212:215], v[196:199], v[64:67]
	v_mfma_f32_16x16x32_bf16 v[116:119], v[208:211], v[176:179], v[116:119]
	v_mfma_f32_16x16x32_bf16 v[112:115], v[216:219], v[176:179], v[112:115]
	v_mfma_f32_16x16x32_bf16 v[100:103], v[208:211], v[184:187], v[100:103]
	v_mfma_f32_16x16x32_bf16 v[96:99], v[216:219], v[184:187], v[96:99]
	v_mfma_f32_16x16x32_bf16 v[84:87], v[208:211], v[192:195], v[84:87]
	v_mfma_f32_16x16x32_bf16 v[80:83], v[216:219], v[192:195], v[80:83]
	v_mfma_f32_16x16x32_bf16 v[68:71], v[208:211], v[200:203], v[68:71]
	v_mfma_f32_16x16x32_bf16 v[64:67], v[216:219], v[200:203], v[64:67]
	s_setprio 0
	s_mov_b32 m0, s38
	v_lshl_add_u64 v[222:223], s[30:31], 0, v[128:129]
	s_barrier
	ds_read_b128 v[172:175], v146 offset:16384
	ds_read_b128 v[176:179], v146 offset:17408
	ds_read_b128 v[180:183], v146 offset:18432
	ds_read_b128 v[184:187], v146 offset:19456
	ds_read_b128 v[188:191], v146 offset:20480
	ds_read_b128 v[192:195], v146 offset:21504
	ds_read_b128 v[196:199], v146 offset:22528
	ds_read_b128 v[200:203], v146 offset:23552
	global_load_lds_dwordx4 v[222:223], off
	v_lshl_add_u64 v[224:225], s[30:31], 0, v[132:133]
	s_mov_b32 m0, s39
	s_nop 0
	global_load_lds_dwordx4 v[224:225], off
	s_barrier
	s_waitcnt lgkmcnt(0)
	s_setprio 3
	s_waitcnt lgkmcnt(0)
	v_mfma_f32_16x16x32_bf16 v[60:63], v[156:159], v[172:175], v[60:63]
	v_mfma_f32_16x16x32_bf16 v[56:59], v[164:167], v[172:175], v[56:59]
	v_mfma_f32_16x16x32_bf16 v[44:47], v[156:159], v[180:183], v[44:47]
	v_mfma_f32_16x16x32_bf16 v[40:43], v[164:167], v[180:183], v[40:43]
	v_mfma_f32_16x16x32_bf16 v[28:31], v[156:159], v[188:191], v[28:31]
	v_mfma_f32_16x16x32_bf16 v[24:27], v[164:167], v[188:191], v[24:27]
	v_mfma_f32_16x16x32_bf16 v[12:15], v[156:159], v[196:199], v[12:15]
	v_mfma_f32_16x16x32_bf16 v[8:11], v[164:167], v[196:199], v[8:11]
	v_mfma_f32_16x16x32_bf16 v[60:63], v[160:163], v[176:179], v[60:63]
	v_mfma_f32_16x16x32_bf16 v[56:59], v[168:171], v[176:179], v[56:59]
	v_mfma_f32_16x16x32_bf16 v[44:47], v[160:163], v[184:187], v[44:47]
	v_mfma_f32_16x16x32_bf16 v[40:43], v[168:171], v[184:187], v[40:43]
	v_mfma_f32_16x16x32_bf16 v[28:31], v[160:163], v[192:195], v[28:31]
	v_mfma_f32_16x16x32_bf16 v[24:27], v[168:171], v[192:195], v[24:27]
	v_mfma_f32_16x16x32_bf16 v[12:15], v[160:163], v[200:203], v[12:15]
	v_mfma_f32_16x16x32_bf16 v[8:11], v[168:171], v[200:203], v[8:11]
	s_setprio 0
	s_barrier
	s_add_u32 s58, s28, 0x80000
	s_addc_u32 s59, s29, 0
	s_add_i32 s57, s48, s37
	v_lshl_add_u64 v[156:157], s[58:59], 0, v[130:131]
	s_mov_b32 m0, s57
	s_nop 0
	global_load_lds_dwordx4 v[156:157], off
	v_lshl_add_u64 v[156:157], s[58:59], 0, v[134:135]
	s_add_i32 m0, s57, 0x2000
	s_nop 0
	global_load_lds_dwordx4 v[156:157], off
	s_waitcnt vmcnt(6)
	s_barrier
	s_setprio 3
	v_mfma_f32_16x16x32_bf16 v[52:55], v[204:207], v[172:175], v[52:55]
	v_mfma_f32_16x16x32_bf16 v[48:51], v[212:215], v[172:175], v[48:51]
	v_mfma_f32_16x16x32_bf16 v[36:39], v[204:207], v[180:183], v[36:39]
	v_mfma_f32_16x16x32_bf16 v[32:35], v[212:215], v[180:183], v[32:35]
	v_mfma_f32_16x16x32_bf16 v[20:23], v[204:207], v[188:191], v[20:23]
	v_mfma_f32_16x16x32_bf16 v[16:19], v[212:215], v[188:191], v[16:19]
	v_mfma_f32_16x16x32_bf16 v[4:7], v[204:207], v[196:199], v[4:7]
	v_mfma_f32_16x16x32_bf16 v[0:3], v[212:215], v[196:199], v[0:3]
	v_mfma_f32_16x16x32_bf16 v[52:55], v[208:211], v[176:179], v[52:55]
	v_mfma_f32_16x16x32_bf16 v[48:51], v[216:219], v[176:179], v[48:51]
	v_mfma_f32_16x16x32_bf16 v[36:39], v[208:211], v[184:187], v[36:39]
	v_mfma_f32_16x16x32_bf16 v[32:35], v[216:219], v[184:187], v[32:35]
	v_mfma_f32_16x16x32_bf16 v[20:23], v[208:211], v[192:195], v[20:23]
	v_mfma_f32_16x16x32_bf16 v[16:19], v[216:219], v[192:195], v[16:19]
	v_mfma_f32_16x16x32_bf16 v[4:7], v[208:211], v[200:203], v[4:7]
	v_mfma_f32_16x16x32_bf16 v[0:3], v[216:219], v[200:203], v[0:3]
	s_setprio 0
	s_add_i32 s57, 0, 0x18000
	v_add_u32_e32 v140, s57, v144
	s_barrier
	ds_read_b128 v[156:159], v140
	ds_read_b128 v[160:163], v140 offset:1024
	ds_read_b128 v[164:167], v140 offset:2048
	ds_read_b128 v[168:171], v140 offset:3072
	s_add_u32 s30, s30, 0x80000
	s_addc_u32 s31, s31, 0
	s_mov_b32 m0, s40
	v_lshl_add_u64 v[204:205], s[30:31], 0, v[128:129]
	ds_read_b128 v[172:175], v146 offset:32768
	ds_read_b128 v[176:179], v146 offset:33792
	ds_read_b128 v[180:183], v146 offset:34816
	ds_read_b128 v[184:187], v146 offset:35840
	ds_read_b128 v[188:191], v146 offset:36864
	ds_read_b128 v[192:195], v146 offset:37888
	ds_read_b128 v[196:199], v146 offset:38912
	ds_read_b128 v[200:203], v146 offset:39936
	global_load_lds_dwordx4 v[204:205], off
	v_lshl_add_u64 v[204:205], s[30:31], 0, v[132:133]
	s_mov_b32 m0, s41
	s_nop 0
	global_load_lds_dwordx4 v[204:205], off
	s_waitcnt lgkmcnt(8)
	s_barrier
	s_waitcnt lgkmcnt(0)
	s_setprio 3
	s_waitcnt lgkmcnt(0)
	v_mfma_f32_16x16x32_bf16 v[124:127], v[156:159], v[172:175], v[124:127]
	v_mfma_f32_16x16x32_bf16 v[120:123], v[164:167], v[172:175], v[120:123]
	v_mfma_f32_16x16x32_bf16 v[108:111], v[156:159], v[180:183], v[108:111]
	v_mfma_f32_16x16x32_bf16 v[104:107], v[164:167], v[180:183], v[104:107]
	v_mfma_f32_16x16x32_bf16 v[92:95], v[156:159], v[188:191], v[92:95]
	v_mfma_f32_16x16x32_bf16 v[88:91], v[164:167], v[188:191], v[88:91]
	v_mfma_f32_16x16x32_bf16 v[76:79], v[156:159], v[196:199], v[76:79]
	v_mfma_f32_16x16x32_bf16 v[72:75], v[164:167], v[196:199], v[72:75]
	v_mfma_f32_16x16x32_bf16 v[124:127], v[160:163], v[176:179], v[124:127]
	v_mfma_f32_16x16x32_bf16 v[120:123], v[168:171], v[176:179], v[120:123]
	v_mfma_f32_16x16x32_bf16 v[108:111], v[160:163], v[184:187], v[108:111]
	v_mfma_f32_16x16x32_bf16 v[104:107], v[168:171], v[184:187], v[104:107]
	v_mfma_f32_16x16x32_bf16 v[92:95], v[160:163], v[192:195], v[92:95]
	v_mfma_f32_16x16x32_bf16 v[88:91], v[168:171], v[192:195], v[88:91]
	v_mfma_f32_16x16x32_bf16 v[76:79], v[160:163], v[200:203], v[76:79]
	v_mfma_f32_16x16x32_bf16 v[72:75], v[168:171], v[200:203], v[72:75]
	s_setprio 0
	s_barrier
	s_add_i32 s30, 0, 0x1c000
	s_add_i32 s31, s57, s37
	v_add_u32_e32 v140, s30, v144
	v_lshl_add_u64 v[142:143], v[142:143], 0, s[6:7]
	s_mov_b32 m0, s31
	ds_read_b128 v[204:207], v140
	ds_read_b128 v[208:211], v140 offset:1024
	ds_read_b128 v[212:215], v140 offset:2048
	ds_read_b128 v[216:219], v140 offset:3072
	global_load_lds_dwordx4 v[142:143], off
	v_lshl_add_u64 v[142:143], v[220:221], 0, s[6:7]
	s_add_i32 m0, s31, 0x2000
	s_nop 0
	global_load_lds_dwordx4 v[142:143], off
	s_barrier
	s_waitcnt lgkmcnt(0)
	s_setprio 3
	s_waitcnt lgkmcnt(0)
	v_mfma_f32_16x16x32_bf16 v[116:119], v[204:207], v[172:175], v[116:119]
	v_mfma_f32_16x16x32_bf16 v[112:115], v[212:215], v[172:175], v[112:115]
	v_mfma_f32_16x16x32_bf16 v[100:103], v[204:207], v[180:183], v[100:103]
	v_mfma_f32_16x16x32_bf16 v[96:99], v[212:215], v[180:183], v[96:99]
	v_mfma_f32_16x16x32_bf16 v[84:87], v[204:207], v[188:191], v[84:87]
	v_mfma_f32_16x16x32_bf16 v[80:83], v[212:215], v[188:191], v[80:83]
	v_mfma_f32_16x16x32_bf16 v[68:71], v[204:207], v[196:199], v[68:71]
	v_mfma_f32_16x16x32_bf16 v[64:67], v[212:215], v[196:199], v[64:67]
	v_mfma_f32_16x16x32_bf16 v[116:119], v[208:211], v[176:179], v[116:119]
	v_mfma_f32_16x16x32_bf16 v[112:115], v[216:219], v[176:179], v[112:115]
	v_mfma_f32_16x16x32_bf16 v[100:103], v[208:211], v[184:187], v[100:103]
	v_mfma_f32_16x16x32_bf16 v[96:99], v[216:219], v[184:187], v[96:99]
	v_mfma_f32_16x16x32_bf16 v[84:87], v[208:211], v[192:195], v[84:87]
	v_mfma_f32_16x16x32_bf16 v[80:83], v[216:219], v[192:195], v[80:83]
	v_mfma_f32_16x16x32_bf16 v[68:71], v[208:211], v[200:203], v[68:71]
	v_mfma_f32_16x16x32_bf16 v[64:67], v[216:219], v[200:203], v[64:67]
	s_setprio 0
	s_mov_b32 m0, s43
	v_lshl_add_u64 v[142:143], v[222:223], 0, s[6:7]
	s_barrier
	ds_read_b128 v[172:175], v146 offset:49152
	ds_read_b128 v[176:179], v146 offset:50176
	ds_read_b128 v[180:183], v146 offset:51200
	ds_read_b128 v[184:187], v146 offset:52224
	ds_read_b128 v[188:191], v146 offset:53248
	ds_read_b128 v[192:195], v146 offset:54272
	ds_read_b128 v[196:199], v146 offset:55296
	ds_read_b128 v[200:203], v146 offset:56320
	global_load_lds_dwordx4 v[142:143], off
	v_lshl_add_u64 v[142:143], v[224:225], 0, s[6:7]
	s_mov_b32 m0, s44
	s_nop 0
	global_load_lds_dwordx4 v[142:143], off
	s_barrier
;     __device__ __forceinline__ void operator()(const f32x4 (&acc)[2][2][4][2], const Unit& u, int wr, int wc, int fr, int fq, const Pre& pr) const {
;         const float (&rsv)[8] = pr.rsv;
; #pragma unroll
;         for (int ai = 0; ai < 2; ++ai)
; #pragma unroll
;             for (int m = 0; m < 4; ++m) {
;                 const int row = u.pm * 256 + ai * 128 + wr * 64 + m * 16 + fr; const float rs = __builtin_amdgcn_rsqf(rsv[ai * 4 + m] * (1.0f / DM) + NORM_EPS);
; #pragma unroll
;                 for (int bj = 0; bj < 2; ++bj) st_bf16x8(out + (size_t)row * ldo + u.pn * 256 + 128 * bj + 32 * wc + 8 * fq, acc[ai][bj][m][0] * rs, acc[ai][bj][m][1] * rs);
;             }
	s_waitcnt lgkmcnt(0)
	s_setprio 3
	s_waitcnt lgkmcnt(0)
	v_mfma_f32_16x16x32_bf16 v[60:63], v[156:159], v[172:175], v[60:63]
	v_mfma_f32_16x16x32_bf16 v[56:59], v[164:167], v[172:175], v[56:59]
	v_mfma_f32_16x16x32_bf16 v[44:47], v[156:159], v[180:183], v[44:47]
	v_mfma_f32_16x16x32_bf16 v[40:43], v[164:167], v[180:183], v[40:43]
	v_mfma_f32_16x16x32_bf16 v[28:31], v[156:159], v[188:191], v[28:31]
	v_mfma_f32_16x16x32_bf16 v[24:27], v[164:167], v[188:191], v[24:27]
	v_mfma_f32_16x16x32_bf16 v[12:15], v[156:159], v[196:199], v[12:15]
	v_mfma_f32_16x16x32_bf16 v[8:11], v[164:167], v[196:199], v[8:11]
	v_mfma_f32_16x16x32_bf16 v[60:63], v[160:163], v[176:179], v[60:63]
	v_mfma_f32_16x16x32_bf16 v[56:59], v[168:171], v[176:179], v[56:59]
	v_mfma_f32_16x16x32_bf16 v[44:47], v[160:163], v[184:187], v[44:47]
	v_mfma_f32_16x16x32_bf16 v[40:43], v[168:171], v[184:187], v[40:43]
	v_mfma_f32_16x16x32_bf16 v[28:31], v[160:163], v[192:195], v[28:31]
	v_mfma_f32_16x16x32_bf16 v[24:27], v[168:171], v[192:195], v[24:27]
	v_mfma_f32_16x16x32_bf16 v[12:15], v[160:163], v[200:203], v[12:15]
	v_mfma_f32_16x16x32_bf16 v[8:11], v[168:171], v[200:203], v[8:11]
	s_setprio 0
	s_barrier
	s_add_u32 s28, s28, 0x80080
	s_addc_u32 s29, s29, 0
	s_add_i32 s30, s30, s37
	v_lshl_add_u64 v[142:143], s[28:29], 0, v[130:131]
	s_mov_b32 m0, s30
	s_nop 0
	global_load_lds_dwordx4 v[142:143], off
	v_lshl_add_u64 v[142:143], s[28:29], 0, v[134:135]
	s_add_i32 m0, s30, 0x2000
	s_nop 0
	global_load_lds_dwordx4 v[142:143], off
	s_waitcnt vmcnt(6)
	s_barrier
	s_setprio 3
	v_mfma_f32_16x16x32_bf16 v[52:55], v[204:207], v[172:175], v[52:55]
	v_mfma_f32_16x16x32_bf16 v[48:51], v[212:215], v[172:175], v[48:51]
	v_mfma_f32_16x16x32_bf16 v[36:39], v[204:207], v[180:183], v[36:39]
	v_mfma_f32_16x16x32_bf16 v[32:35], v[212:215], v[180:183], v[32:35]
	v_mfma_f32_16x16x32_bf16 v[20:23], v[204:207], v[188:191], v[20:23]
	v_mfma_f32_16x16x32_bf16 v[16:19], v[212:215], v[188:191], v[16:19]
	v_mfma_f32_16x16x32_bf16 v[4:7], v[204:207], v[196:199], v[4:7]
	v_mfma_f32_16x16x32_bf16 v[0:3], v[212:215], v[196:199], v[0:3]
	v_mfma_f32_16x16x32_bf16 v[52:55], v[208:211], v[176:179], v[52:55]
	v_mfma_f32_16x16x32_bf16 v[48:51], v[216:219], v[176:179], v[48:51]
	v_mfma_f32_16x16x32_bf16 v[36:39], v[208:211], v[184:187], v[36:39]
	v_mfma_f32_16x16x32_bf16 v[32:35], v[216:219], v[184:187], v[32:35]
	v_mfma_f32_16x16x32_bf16 v[20:23], v[208:211], v[192:195], v[20:23]
	v_mfma_f32_16x16x32_bf16 v[16:19], v[216:219], v[192:195], v[16:19]
	v_mfma_f32_16x16x32_bf16 v[4:7], v[208:211], v[200:203], v[4:7]
	v_mfma_f32_16x16x32_bf16 v[0:3], v[216:219], v[200:203], v[0:3]
	s_setprio 0
	s_add_i32 s56, s56, 2
	s_add_u32 s16, s16, 0x100
	s_addc_u32 s17, s17, 0
	s_add_u32 s54, s54, 0x100
	s_addc_u32 s55, s55, 0
	s_cmp_gt_u32 s56, 29
	s_barrier
	s_cbranch_scc0 .LBB0_2168
	v_mbcnt_lo_u32_b32 v142, -1, 0
	v_mbcnt_hi_u32_b32 v142, -1, v142
	s_waitcnt vmcnt(0)
	v_fmamk_f32 v141, v141, 0x3a000000, v148
	v_and_or_b32 v140, v142, 15, s11
	s_lshl_b32 s16, s53, 8
	v_rsq_f32_e32 v156, v141
	v_ashrrev_i32_e32 v141, 31, v140
	s_ashr_i32 s17, s16, 31
	v_ashrrev_i32_e32 v142, 1, v142
	v_lshlrev_b64 v[158:159], 10, v[140:141]
	v_and_b32_e32 v142, -8, v142
	v_lshl_add_u64 v[158:159], s[4:5], 0, v[158:159]
	s_lshl_b64 s[16:17], s[16:17], 1
	v_ashrrev_i32_e32 v143, 31, v142
	v_lshl_add_u64 v[158:159], v[158:159], 0, s[16:17]
	v_lshl_add_u64 v[158:159], v[158:159], 0, s[0:1]
	v_lshlrev_b64 v[142:143], 1, v[142:143]
	v_lshl_add_u64 v[158:159], v[158:159], 0, v[142:143]
	v_pk_mul_f32 v[126:127], v[156:157], v[126:127] op_sel_hi:[0,1]
	v_pk_mul_f32 v[124:125], v[156:157], v[124:125] op_sel_hi:[0,1]
	v_pk_mul_f32 v[160:161], v[156:157], v[122:123] op_sel_hi:[0,1]
	v_pk_mul_f32 v[122:123], v[156:157], v[120:121] op_sel_hi:[0,1]
	v_cvt_pk_bf16_f32 v120, v124, v125
	v_cvt_pk_bf16_f32 v121, v126, v127
	v_cvt_pk_bf16_f32 v122, v122, v123
	v_cvt_pk_bf16_f32 v123, v160, v161
	global_store_dwordx4 v[158:159], v[120:123], off
	v_pk_mul_f32 v[118:119], v[156:157], v[118:119] op_sel_hi:[0,1]
	v_pk_mul_f32 v[116:117], v[156:157], v[116:117] op_sel_hi:[0,1]
	v_pk_mul_f32 v[120:121], v[156:157], v[114:115] op_sel_hi:[0,1]
	v_pk_mul_f32 v[114:115], v[156:157], v[112:113] op_sel_hi:[0,1]
	v_cvt_pk_bf16_f32 v112, v116, v117
	v_cvt_pk_bf16_f32 v113, v118, v119
	v_cvt_pk_bf16_f32 v114, v114, v115
	v_cvt_pk_bf16_f32 v115, v120, v121
	global_store_dwordx4 v[158:159], v[112:115], off offset:256
	s_and_b64 vcc, exec, s[8:9]
	s_mov_b32 s30, s10
	v_or_b32_e32 v112, 16, v140
	v_fmamk_f32 v113, v155, 0x3a000000, v148
	v_rsq_f32_e32 v114, v113
	v_ashrrev_i32_e32 v113, 31, v112
	v_lshlrev_b64 v[112:113], 10, v[112:113]
	v_lshl_add_u64 v[112:113], s[4:5], 0, v[112:113]
	v_lshl_add_u64 v[112:113], v[112:113], 0, s[16:17]
	v_lshl_add_u64 v[112:113], v[112:113], 0, s[0:1]
	v_lshl_add_u64 v[112:113], v[112:113], 0, v[142:143]
	v_pk_mul_f32 v[110:111], v[114:115], v[110:111] op_sel_hi:[0,1]
	v_pk_mul_f32 v[108:109], v[114:115], v[108:109] op_sel_hi:[0,1]
	v_pk_mul_f32 v[116:117], v[114:115], v[106:107] op_sel_hi:[0,1]
	v_pk_mul_f32 v[106:107], v[114:115], v[104:105] op_sel_hi:[0,1]
	v_cvt_pk_bf16_f32 v104, v108, v109
	v_cvt_pk_bf16_f32 v105, v110, v111
	v_cvt_pk_bf16_f32 v106, v106, v107
	v_cvt_pk_bf16_f32 v107, v116, v117
	global_store_dwordx4 v[112:113], v[104:107], off
	v_pk_mul_f32 v[102:103], v[114:115], v[102:103] op_sel_hi:[0,1]
	v_pk_mul_f32 v[100:101], v[114:115], v[100:101] op_sel_hi:[0,1]
	v_pk_mul_f32 v[104:105], v[114:115], v[98:99] op_sel_hi:[0,1]
	v_pk_mul_f32 v[98:99], v[114:115], v[96:97] op_sel_hi:[0,1]
	v_cvt_pk_bf16_f32 v96, v100, v101
	v_cvt_pk_bf16_f32 v97, v102, v103
;     __device__ __forceinline__ void operator()(const f32x4 (&acc)[2][2][4][2], const Unit& u, int wr, int wc, int fr, int fq, const Pre& pr) const {
;         const float (&rsv)[8] = pr.rsv;
; #pragma unroll
;         for (int ai = 0; ai < 2; ++ai)
; #pragma unroll
;             for (int m = 0; m < 4; ++m) {
;                 const int row = u.pm * 256 + ai * 128 + wr * 64 + m * 16 + fr; const float rs = __builtin_amdgcn_rsqf(rsv[ai * 4 + m] * (1.0f / DM) + NORM_EPS);
; #pragma unroll
;                 for (int bj = 0; bj < 2; ++bj) st_bf16x8(out + (size_t)row * ldo + u.pn * 256 + 128 * bj + 32 * wc + 8 * fq, acc[ai][bj][m][0] * rs, acc[ai][bj][m][1] * rs);
;             }
	v_cvt_pk_bf16_f32 v98, v98, v99
	v_cvt_pk_bf16_f32 v99, v104, v105
	global_store_dwordx4 v[112:113], v[96:99], off offset:256
	s_mov_b32 s53, s52
	s_mov_b64 s[28:29], s[14:15]
	v_or_b32_e32 v96, 32, v140
	v_fmamk_f32 v97, v154, 0x3a000000, v148
	v_rsq_f32_e32 v98, v97
	v_ashrrev_i32_e32 v97, 31, v96
	v_lshlrev_b64 v[96:97], 10, v[96:97]
	v_lshl_add_u64 v[96:97], s[4:5], 0, v[96:97]
	v_lshl_add_u64 v[96:97], v[96:97], 0, s[16:17]
	v_lshl_add_u64 v[96:97], v[96:97], 0, s[0:1]
	v_lshl_add_u64 v[96:97], v[96:97], 0, v[142:143]
	v_pk_mul_f32 v[94:95], v[98:99], v[94:95] op_sel_hi:[0,1]
	v_pk_mul_f32 v[92:93], v[98:99], v[92:93] op_sel_hi:[0,1]
	v_pk_mul_f32 v[100:101], v[98:99], v[90:91] op_sel_hi:[0,1]
	v_pk_mul_f32 v[90:91], v[98:99], v[88:89] op_sel_hi:[0,1]
	v_cvt_pk_bf16_f32 v88, v92, v93
	v_cvt_pk_bf16_f32 v89, v94, v95
	v_cvt_pk_bf16_f32 v90, v90, v91
	v_cvt_pk_bf16_f32 v91, v100, v101
	global_store_dwordx4 v[96:97], v[88:91], off
	v_pk_mul_f32 v[86:87], v[98:99], v[86:87] op_sel_hi:[0,1]
	v_pk_mul_f32 v[84:85], v[98:99], v[84:85] op_sel_hi:[0,1]
	v_pk_mul_f32 v[88:89], v[98:99], v[82:83] op_sel_hi:[0,1]
	v_pk_mul_f32 v[82:83], v[98:99], v[80:81] op_sel_hi:[0,1]
	v_cvt_pk_bf16_f32 v80, v84, v85
	v_cvt_pk_bf16_f32 v81, v86, v87
	v_cvt_pk_bf16_f32 v82, v82, v83
	v_cvt_pk_bf16_f32 v83, v88, v89
	global_store_dwordx4 v[96:97], v[80:83], off offset:256
	s_nop 1
	v_or_b32_e32 v80, 48, v140
	v_fmamk_f32 v81, v153, 0x3a000000, v148
	v_rsq_f32_e32 v82, v81
	v_ashrrev_i32_e32 v81, 31, v80
	v_lshlrev_b64 v[80:81], 10, v[80:81]
	v_lshl_add_u64 v[80:81], s[4:5], 0, v[80:81]
	v_lshl_add_u64 v[80:81], v[80:81], 0, s[16:17]
	v_lshl_add_u64 v[80:81], v[80:81], 0, s[0:1]
	v_lshl_add_u64 v[80:81], v[80:81], 0, v[142:143]
	v_pk_mul_f32 v[78:79], v[82:83], v[78:79] op_sel_hi:[0,1]
	v_pk_mul_f32 v[76:77], v[82:83], v[76:77] op_sel_hi:[0,1]
	v_pk_mul_f32 v[84:85], v[82:83], v[74:75] op_sel_hi:[0,1]
	v_pk_mul_f32 v[74:75], v[82:83], v[72:73] op_sel_hi:[0,1]
	v_cvt_pk_bf16_f32 v72, v76, v77
	v_cvt_pk_bf16_f32 v73, v78, v79
	v_cvt_pk_bf16_f32 v74, v74, v75
	v_cvt_pk_bf16_f32 v75, v84, v85
	global_store_dwordx4 v[80:81], v[72:75], off
	v_pk_mul_f32 v[70:71], v[82:83], v[70:71] op_sel_hi:[0,1]
	v_pk_mul_f32 v[68:69], v[82:83], v[68:69] op_sel_hi:[0,1]
	v_pk_mul_f32 v[72:73], v[82:83], v[66:67] op_sel_hi:[0,1]
	v_pk_mul_f32 v[66:67], v[82:83], v[64:65] op_sel_hi:[0,1]
	v_cvt_pk_bf16_f32 v64, v68, v69
	v_cvt_pk_bf16_f32 v65, v70, v71
	v_cvt_pk_bf16_f32 v66, v66, v67
	v_cvt_pk_bf16_f32 v67, v72, v73
	global_store_dwordx4 v[80:81], v[64:67], off offset:256
	s_nop 1
	v_add_u32_e32 v64, 0x80, v140
	v_fmamk_f32 v65, v152, 0x3a000000, v148
	v_rsq_f32_e32 v66, v65
	v_ashrrev_i32_e32 v65, 31, v64
	v_lshlrev_b64 v[64:65], 10, v[64:65]
	v_lshl_add_u64 v[64:65], s[4:5], 0, v[64:65]
	v_lshl_add_u64 v[64:65], v[64:65], 0, s[16:17]
	v_lshl_add_u64 v[64:65], v[64:65], 0, s[0:1]
	v_lshl_add_u64 v[64:65], v[64:65], 0, v[142:143]
	v_pk_mul_f32 v[62:63], v[66:67], v[62:63] op_sel_hi:[0,1]
	v_pk_mul_f32 v[60:61], v[66:67], v[60:61] op_sel_hi:[0,1]
	v_pk_mul_f32 v[68:69], v[66:67], v[58:59] op_sel_hi:[0,1]
	v_pk_mul_f32 v[58:59], v[66:67], v[56:57] op_sel_hi:[0,1]
	v_cvt_pk_bf16_f32 v56, v60, v61
	v_cvt_pk_bf16_f32 v57, v62, v63
	v_cvt_pk_bf16_f32 v58, v58, v59
	v_cvt_pk_bf16_f32 v59, v68, v69
	global_store_dwordx4 v[64:65], v[56:59], off
	v_pk_mul_f32 v[54:55], v[66:67], v[54:55] op_sel_hi:[0,1]
	v_pk_mul_f32 v[52:53], v[66:67], v[52:53] op_sel_hi:[0,1]
	v_pk_mul_f32 v[56:57], v[66:67], v[50:51] op_sel_hi:[0,1]
	v_pk_mul_f32 v[50:51], v[66:67], v[48:49] op_sel_hi:[0,1]
	v_cvt_pk_bf16_f32 v48, v52, v53
	v_cvt_pk_bf16_f32 v49, v54, v55
	v_cvt_pk_bf16_f32 v50, v50, v51
	v_cvt_pk_bf16_f32 v51, v56, v57
;     __device__ __forceinline__ void operator()(const f32x4 (&acc)[2][2][4][2], const Unit& u, int wr, int wc, int fr, int fq, const Pre& pr) const {
;         const float (&rsv)[8] = pr.rsv;
; #pragma unroll
;         for (int ai = 0; ai < 2; ++ai)
; #pragma unroll
;             for (int m = 0; m < 4; ++m) {
;                 const int row = u.pm * 256 + ai * 128 + wr * 64 + m * 16 + fr; const float rs = __builtin_amdgcn_rsqf(rsv[ai * 4 + m] * (1.0f / DM) + NORM_EPS);
; #pragma unroll
;                 for (int bj = 0; bj < 2; ++bj) st_bf16x8(out + (size_t)row * ldo + u.pn * 256 + 128 * bj + 32 * wc + 8 * fq, acc[ai][bj][m][0] * rs, acc[ai][bj][m][1] * rs);
;             }
	global_store_dwordx4 v[64:65], v[48:51], off offset:256
	s_nop 1
	v_add_u32_e32 v48, 0x90, v140
	v_fmamk_f32 v49, v151, 0x3a000000, v148
	v_rsq_f32_e32 v50, v49
	v_ashrrev_i32_e32 v49, 31, v48
	v_lshlrev_b64 v[48:49], 10, v[48:49]
	v_lshl_add_u64 v[48:49], s[4:5], 0, v[48:49]
	v_lshl_add_u64 v[48:49], v[48:49], 0, s[16:17]
	v_lshl_add_u64 v[48:49], v[48:49], 0, s[0:1]
	v_lshl_add_u64 v[48:49], v[48:49], 0, v[142:143]
	v_pk_mul_f32 v[46:47], v[50:51], v[46:47] op_sel_hi:[0,1]
	v_pk_mul_f32 v[44:45], v[50:51], v[44:45] op_sel_hi:[0,1]
	v_pk_mul_f32 v[52:53], v[50:51], v[42:43] op_sel_hi:[0,1]
	v_pk_mul_f32 v[42:43], v[50:51], v[40:41] op_sel_hi:[0,1]
	v_cvt_pk_bf16_f32 v40, v44, v45
	v_cvt_pk_bf16_f32 v41, v46, v47
	v_cvt_pk_bf16_f32 v42, v42, v43
	v_cvt_pk_bf16_f32 v43, v52, v53
	global_store_dwordx4 v[48:49], v[40:43], off
	v_pk_mul_f32 v[38:39], v[50:51], v[38:39] op_sel_hi:[0,1]
	v_pk_mul_f32 v[36:37], v[50:51], v[36:37] op_sel_hi:[0,1]
	v_pk_mul_f32 v[40:41], v[50:51], v[34:35] op_sel_hi:[0,1]
	v_pk_mul_f32 v[34:35], v[50:51], v[32:33] op_sel_hi:[0,1]
	v_cvt_pk_bf16_f32 v32, v36, v37
	v_cvt_pk_bf16_f32 v33, v38, v39
	v_cvt_pk_bf16_f32 v34, v34, v35
	v_cvt_pk_bf16_f32 v35, v40, v41
	global_store_dwordx4 v[48:49], v[32:35], off offset:256
	s_nop 1
	v_add_u32_e32 v32, 0xa0, v140
	v_fmamk_f32 v33, v150, 0x3a000000, v148
	v_rsq_f32_e32 v34, v33
	v_ashrrev_i32_e32 v33, 31, v32
	v_lshlrev_b64 v[32:33], 10, v[32:33]
	v_lshl_add_u64 v[32:33], s[4:5], 0, v[32:33]
	v_lshl_add_u64 v[32:33], v[32:33], 0, s[16:17]
	v_lshl_add_u64 v[32:33], v[32:33], 0, s[0:1]
	v_lshl_add_u64 v[32:33], v[32:33], 0, v[142:143]
	v_pk_mul_f32 v[30:31], v[34:35], v[30:31] op_sel_hi:[0,1]
	v_pk_mul_f32 v[28:29], v[34:35], v[28:29] op_sel_hi:[0,1]
	v_pk_mul_f32 v[36:37], v[34:35], v[26:27] op_sel_hi:[0,1]
	v_pk_mul_f32 v[26:27], v[34:35], v[24:25] op_sel_hi:[0,1]
	v_cvt_pk_bf16_f32 v24, v28, v29
	v_cvt_pk_bf16_f32 v25, v30, v31
	v_cvt_pk_bf16_f32 v26, v26, v27
	v_cvt_pk_bf16_f32 v27, v36, v37
	global_store_dwordx4 v[32:33], v[24:27], off
	v_pk_mul_f32 v[22:23], v[34:35], v[22:23] op_sel_hi:[0,1]
	v_pk_mul_f32 v[20:21], v[34:35], v[20:21] op_sel_hi:[0,1]
	v_pk_mul_f32 v[24:25], v[34:35], v[18:19] op_sel_hi:[0,1]
	v_pk_mul_f32 v[18:19], v[34:35], v[16:17] op_sel_hi:[0,1]
	v_cvt_pk_bf16_f32 v16, v20, v21
	v_cvt_pk_bf16_f32 v17, v22, v23
	v_cvt_pk_bf16_f32 v18, v18, v19
	v_cvt_pk_bf16_f32 v19, v24, v25
	global_store_dwordx4 v[32:33], v[16:19], off offset:256
	s_nop 1
	v_add_u32_e32 v16, 0xb0, v140
	v_fmamk_f32 v17, v149, 0x3a000000, v148
	v_rsq_f32_e32 v18, v17
	v_ashrrev_i32_e32 v17, 31, v16
	v_lshlrev_b64 v[16:17], 10, v[16:17]
	v_lshl_add_u64 v[16:17], s[4:5], 0, v[16:17]
	v_lshl_add_u64 v[16:17], v[16:17], 0, s[16:17]
	v_lshl_add_u64 v[16:17], v[16:17], 0, s[0:1]
	v_lshl_add_u64 v[16:17], v[16:17], 0, v[142:143]
	v_pk_mul_f32 v[14:15], v[18:19], v[14:15] op_sel_hi:[0,1]
	v_pk_mul_f32 v[12:13], v[18:19], v[12:13] op_sel_hi:[0,1]
	v_pk_mul_f32 v[20:21], v[18:19], v[10:11] op_sel_hi:[0,1]
	v_pk_mul_f32 v[10:11], v[18:19], v[8:9] op_sel_hi:[0,1]
	v_cvt_pk_bf16_f32 v8, v12, v13
	v_cvt_pk_bf16_f32 v9, v14, v15
	v_cvt_pk_bf16_f32 v10, v10, v11
	v_cvt_pk_bf16_f32 v11, v20, v21
	global_store_dwordx4 v[16:17], v[8:11], off
	s_mov_b64 s[16:17], s[12:13]
	v_pk_mul_f32 v[6:7], v[18:19], v[6:7] op_sel_hi:[0,1]
	v_pk_mul_f32 v[8:9], v[18:19], v[2:3] op_sel_hi:[0,1]
	v_pk_mul_f32 v[2:3], v[18:19], v[0:1] op_sel_hi:[0,1]
	v_pk_mul_f32 v[4:5], v[18:19], v[4:5] op_sel_hi:[0,1]
	v_cvt_pk_bf16_f32 v0, v4, v5
	v_cvt_pk_bf16_f32 v1, v6, v7
	v_cvt_pk_bf16_f32 v2, v2, v3
	v_cvt_pk_bf16_f32 v3, v8, v9
	global_store_dwordx4 v[16:17], v[0:3], off offset:256
	s_cbranch_vccz .LBB0_2161
	s_waitcnt vmcnt(0)
	s_cmpk_gt_u32 s96, 0xff
	s_cbranch_scc1 .LBB0_2172
	s_barrier

.LBB0_2485:
	ds_read_b128 v[128:131], v179
	ds_read_b128 v[132:135], v179 offset:1024
	ds_read_b128 v[136:139], v179 offset:2048
	ds_read_b128 v[140:143], v179 offset:3072
	s_add_u32 s30, s28, 0xfffe0080
	s_addc_u32 s31, s29, -1
	s_cmp_eq_u32 s63, 4
	s_cselect_b32 s35, s13, s31
	s_cselect_b32 s34, s12, s30
	s_cselect_b32 s31, s15, s62
	s_cselect_b32 s30, s14, s11
	v_lshl_add_u64 v[176:177], s[28:29], 0, v[168:169]
	s_add_i32 m0, s17, 0xc000
	ds_read_b128 v[144:147], v180
	ds_read_b128 v[148:151], v180 offset:1024
	ds_read_b128 v[152:155], v180 offset:2048
	ds_read_b128 v[156:159], v180 offset:3072
	ds_read_b128 v[172:175], v180 offset:4096
	ds_read_b128 v[182:185], v180 offset:5120
	ds_read_b128 v[186:189], v180 offset:6144
	ds_read_b128 v[190:193], v180 offset:7168
	global_load_lds_dwordx4 v[176:177], off
	v_lshl_add_u64 v[176:177], s[28:29], 0, v[170:171]
	s_add_i32 m0, s17, 0xe000
	s_nop 0
	global_load_lds_dwordx4 v[176:177], off
	s_waitcnt lgkmcnt(8)
	s_barrier
	s_waitcnt lgkmcnt(0)
	s_setprio 3
	s_waitcnt lgkmcnt(0)
	v_mfma_f32_16x16x32_bf16 v[124:127], v[128:131], v[144:147], v[124:127]
	v_mfma_f32_16x16x32_bf16 v[120:123], v[136:139], v[144:147], v[120:123]
	v_mfma_f32_16x16x32_bf16 v[112:115], v[128:131], v[152:155], v[112:115]
	v_mfma_f32_16x16x32_bf16 v[104:107], v[136:139], v[152:155], v[104:107]
	v_mfma_f32_16x16x32_bf16 v[96:99], v[128:131], v[172:175], v[96:99]
	v_mfma_f32_16x16x32_bf16 v[88:91], v[136:139], v[172:175], v[88:91]
	v_mfma_f32_16x16x32_bf16 v[80:83], v[128:131], v[186:189], v[80:83]
	v_mfma_f32_16x16x32_bf16 v[72:75], v[136:139], v[186:189], v[72:75]
	v_mfma_f32_16x16x32_bf16 v[124:127], v[132:135], v[148:151], v[124:127]
	v_mfma_f32_16x16x32_bf16 v[120:123], v[140:143], v[148:151], v[120:123]
	v_mfma_f32_16x16x32_bf16 v[112:115], v[132:135], v[156:159], v[112:115]
	v_mfma_f32_16x16x32_bf16 v[104:107], v[140:143], v[156:159], v[104:107]
	v_mfma_f32_16x16x32_bf16 v[96:99], v[132:135], v[182:185], v[96:99]
	v_mfma_f32_16x16x32_bf16 v[88:91], v[140:143], v[182:185], v[88:91]
	v_mfma_f32_16x16x32_bf16 v[80:83], v[132:135], v[190:193], v[80:83]
	v_mfma_f32_16x16x32_bf16 v[72:75], v[140:143], v[190:193], v[72:75]
	s_setprio 0
	s_barrier
	s_add_i32 s64, s49, s39
	v_lshl_add_u64 v[176:177], s[30:31], 0, v[162:163]
	s_mov_b32 m0, s64
	ds_read_b128 v[194:197], v181
	ds_read_b128 v[198:201], v181 offset:1024
	ds_read_b128 v[202:205], v181 offset:2048
	ds_read_b128 v[206:209], v181 offset:3072
	global_load_lds_dwordx4 v[176:177], off
	v_lshl_add_u64 v[210:211], s[30:31], 0, v[166:167]
	s_add_i32 m0, s64, 0x2000
	s_nop 0
	global_load_lds_dwordx4 v[210:211], off
	s_barrier
	s_waitcnt lgkmcnt(0)
	s_setprio 3
	s_waitcnt lgkmcnt(0)
	v_mfma_f32_16x16x32_bf16 v[116:119], v[194:197], v[144:147], v[116:119]
	v_mfma_f32_16x16x32_bf16 v[108:111], v[202:205], v[144:147], v[108:111]
	v_mfma_f32_16x16x32_bf16 v[100:103], v[194:197], v[152:155], v[100:103]
	v_mfma_f32_16x16x32_bf16 v[92:95], v[202:205], v[152:155], v[92:95]
	v_mfma_f32_16x16x32_bf16 v[84:87], v[194:197], v[172:175], v[84:87]
	v_mfma_f32_16x16x32_bf16 v[76:79], v[202:205], v[172:175], v[76:79]
	v_mfma_f32_16x16x32_bf16 v[68:71], v[194:197], v[186:189], v[68:71]
	v_mfma_f32_16x16x32_bf16 v[64:67], v[202:205], v[186:189], v[64:67]
	v_mfma_f32_16x16x32_bf16 v[116:119], v[198:201], v[148:151], v[116:119]
	v_mfma_f32_16x16x32_bf16 v[108:111], v[206:209], v[148:151], v[108:111]
	v_mfma_f32_16x16x32_bf16 v[100:103], v[198:201], v[156:159], v[100:103]
	v_mfma_f32_16x16x32_bf16 v[92:95], v[206:209], v[156:159], v[92:95]
	v_mfma_f32_16x16x32_bf16 v[84:87], v[198:201], v[182:185], v[84:87]
	v_mfma_f32_16x16x32_bf16 v[76:79], v[206:209], v[182:185], v[76:79]
	v_mfma_f32_16x16x32_bf16 v[68:71], v[198:201], v[190:193], v[68:71]
	v_mfma_f32_16x16x32_bf16 v[64:67], v[206:209], v[190:193], v[64:67]
	s_setprio 0
	s_mov_b32 m0, s17
	v_lshl_add_u64 v[212:213], s[34:35], 0, v[160:161]
	s_barrier
	ds_read_b128 v[144:147], v180 offset:16384
	ds_read_b128 v[148:151], v180 offset:17408
	ds_read_b128 v[152:155], v180 offset:18432
	ds_read_b128 v[156:159], v180 offset:19456
	ds_read_b128 v[172:175], v180 offset:20480
	ds_read_b128 v[182:185], v180 offset:21504
	ds_read_b128 v[186:189], v180 offset:22528
	ds_read_b128 v[190:193], v180 offset:23552
	global_load_lds_dwordx4 v[212:213], off
	v_lshl_add_u64 v[214:215], s[34:35], 0, v[164:165]
	s_mov_b32 m0, s40
	s_nop 0
	global_load_lds_dwordx4 v[214:215], off
	s_barrier
	s_waitcnt lgkmcnt(0)
	s_setprio 3
	s_waitcnt lgkmcnt(0)
	v_mfma_f32_16x16x32_bf16 v[60:63], v[128:131], v[144:147], v[60:63]
	v_mfma_f32_16x16x32_bf16 v[56:59], v[136:139], v[144:147], v[56:59]
	v_mfma_f32_16x16x32_bf16 v[48:51], v[128:131], v[152:155], v[48:51]
	v_mfma_f32_16x16x32_bf16 v[40:43], v[136:139], v[152:155], v[40:43]
	v_mfma_f32_16x16x32_bf16 v[32:35], v[128:131], v[172:175], v[32:35]
	v_mfma_f32_16x16x32_bf16 v[24:27], v[136:139], v[172:175], v[24:27]
	v_mfma_f32_16x16x32_bf16 v[16:19], v[128:131], v[186:189], v[16:19]
	v_mfma_f32_16x16x32_bf16 v[8:11], v[136:139], v[186:189], v[8:11]
	v_mfma_f32_16x16x32_bf16 v[60:63], v[132:135], v[148:151], v[60:63]
	v_mfma_f32_16x16x32_bf16 v[56:59], v[140:143], v[148:151], v[56:59]
	v_mfma_f32_16x16x32_bf16 v[48:51], v[132:135], v[156:159], v[48:51]
	v_mfma_f32_16x16x32_bf16 v[40:43], v[140:143], v[156:159], v[40:43]
	v_mfma_f32_16x16x32_bf16 v[32:35], v[132:135], v[182:185], v[32:35]
	v_mfma_f32_16x16x32_bf16 v[24:27], v[140:143], v[182:185], v[24:27]
	v_mfma_f32_16x16x32_bf16 v[16:19], v[132:135], v[190:193], v[16:19]
	v_mfma_f32_16x16x32_bf16 v[8:11], v[140:143], v[190:193], v[8:11]
	s_setprio 0
	s_barrier
	s_add_u32 s64, s30, 0x20000
	s_addc_u32 s65, s31, 0
	s_add_i32 s66, s52, s39
	v_lshl_add_u64 v[128:129], s[64:65], 0, v[162:163]
	s_mov_b32 m0, s66
	s_nop 0
	global_load_lds_dwordx4 v[128:129], off
	v_lshl_add_u64 v[128:129], s[64:65], 0, v[166:167]
	s_add_i32 m0, s66, 0x2000
	s_nop 0
	global_load_lds_dwordx4 v[128:129], off
	s_waitcnt vmcnt(6)
	s_barrier
	s_setprio 3
	v_mfma_f32_16x16x32_bf16 v[52:55], v[194:197], v[144:147], v[52:55]
	v_mfma_f32_16x16x32_bf16 v[44:47], v[202:205], v[144:147], v[44:47]
	v_mfma_f32_16x16x32_bf16 v[36:39], v[194:197], v[152:155], v[36:39]
	v_mfma_f32_16x16x32_bf16 v[28:31], v[202:205], v[152:155], v[28:31]
	v_mfma_f32_16x16x32_bf16 v[20:23], v[194:197], v[172:175], v[20:23]
	v_mfma_f32_16x16x32_bf16 v[12:15], v[202:205], v[172:175], v[12:15]
	v_mfma_f32_16x16x32_bf16 v[4:7], v[194:197], v[186:189], v[4:7]
	v_mfma_f32_16x16x32_bf16 v[0:3], v[202:205], v[186:189], v[0:3]
	v_mfma_f32_16x16x32_bf16 v[52:55], v[198:201], v[148:151], v[52:55]
	v_mfma_f32_16x16x32_bf16 v[44:47], v[206:209], v[148:151], v[44:47]
	v_mfma_f32_16x16x32_bf16 v[36:39], v[198:201], v[156:159], v[36:39]
	v_mfma_f32_16x16x32_bf16 v[28:31], v[206:209], v[156:159], v[28:31]
	v_mfma_f32_16x16x32_bf16 v[20:23], v[198:201], v[182:185], v[20:23]
	v_mfma_f32_16x16x32_bf16 v[12:15], v[206:209], v[182:185], v[12:15]
	v_mfma_f32_16x16x32_bf16 v[4:7], v[198:201], v[190:193], v[4:7]
	v_mfma_f32_16x16x32_bf16 v[0:3], v[206:209], v[190:193], v[0:3]
	s_setprio 0
	s_add_i32 s64, 0, 0x18000
	v_add_u32_e32 v140, s64, v178
	s_barrier
	ds_read_b128 v[128:131], v140
	ds_read_b128 v[132:135], v140 offset:1024
	ds_read_b128 v[136:139], v140 offset:2048
	ds_read_b128 v[140:143], v140 offset:3072
	s_add_u32 s34, s34, 0x20000
	s_addc_u32 s35, s35, 0
	s_mov_b32 m0, s41
	v_lshl_add_u64 v[194:195], s[34:35], 0, v[160:161]
	ds_read_b128 v[144:147], v180 offset:32768
	ds_read_b128 v[148:151], v180 offset:33792
	ds_read_b128 v[152:155], v180 offset:34816
	ds_read_b128 v[156:159], v180 offset:35840
	ds_read_b128 v[172:175], v180 offset:36864
	ds_read_b128 v[182:185], v180 offset:37888
	ds_read_b128 v[186:189], v180 offset:38912
	ds_read_b128 v[190:193], v180 offset:39936
	global_load_lds_dwordx4 v[194:195], off
	v_lshl_add_u64 v[194:195], s[34:35], 0, v[164:165]
	s_mov_b32 m0, s42
	s_nop 0
	global_load_lds_dwordx4 v[194:195], off
	s_waitcnt lgkmcnt(8)
	s_barrier
	s_waitcnt lgkmcnt(0)
	s_setprio 3
	s_waitcnt lgkmcnt(0)
	v_mfma_f32_16x16x32_bf16 v[124:127], v[128:131], v[144:147], v[124:127]
	v_mfma_f32_16x16x32_bf16 v[120:123], v[136:139], v[144:147], v[120:123]
	v_mfma_f32_16x16x32_bf16 v[112:115], v[128:131], v[152:155], v[112:115]
	v_mfma_f32_16x16x32_bf16 v[104:107], v[136:139], v[152:155], v[104:107]
	v_mfma_f32_16x16x32_bf16 v[96:99], v[128:131], v[172:175], v[96:99]
	v_mfma_f32_16x16x32_bf16 v[88:91], v[136:139], v[172:175], v[88:91]
	v_mfma_f32_16x16x32_bf16 v[80:83], v[128:131], v[186:189], v[80:83]
	v_mfma_f32_16x16x32_bf16 v[72:75], v[136:139], v[186:189], v[72:75]
	v_mfma_f32_16x16x32_bf16 v[124:127], v[132:135], v[148:151], v[124:127]
	v_mfma_f32_16x16x32_bf16 v[120:123], v[140:143], v[148:151], v[120:123]
	v_mfma_f32_16x16x32_bf16 v[112:115], v[132:135], v[156:159], v[112:115]
	v_mfma_f32_16x16x32_bf16 v[104:107], v[140:143], v[156:159], v[104:107]
	v_mfma_f32_16x16x32_bf16 v[96:99], v[132:135], v[182:185], v[96:99]
	v_mfma_f32_16x16x32_bf16 v[88:91], v[140:143], v[182:185], v[88:91]
	v_mfma_f32_16x16x32_bf16 v[80:83], v[132:135], v[190:193], v[80:83]
	v_mfma_f32_16x16x32_bf16 v[72:75], v[140:143], v[190:193], v[72:75]
	s_setprio 0
	s_barrier
	s_add_i32 s34, 0, 0x1c000
	s_add_i32 s35, s64, s39
	v_add_u32_e32 v206, s34, v178
	v_lshl_add_u64 v[176:177], v[176:177], 0, s[6:7]
	s_mov_b32 m0, s35
	ds_read_b128 v[194:197], v206
	ds_read_b128 v[198:201], v206 offset:1024
	ds_read_b128 v[202:205], v206 offset:2048
	ds_read_b128 v[206:209], v206 offset:3072
	global_load_lds_dwordx4 v[176:177], off
	v_lshl_add_u64 v[176:177], v[210:211], 0, s[6:7]
	s_add_i32 m0, s35, 0x2000
	s_nop 0
	global_load_lds_dwordx4 v[176:177], off
	s_barrier
	s_waitcnt lgkmcnt(0)
	s_setprio 3
	s_waitcnt lgkmcnt(0)
	v_mfma_f32_16x16x32_bf16 v[116:119], v[194:197], v[144:147], v[116:119]
	v_mfma_f32_16x16x32_bf16 v[108:111], v[202:205], v[144:147], v[108:111]
	v_mfma_f32_16x16x32_bf16 v[100:103], v[194:197], v[152:155], v[100:103]
	v_mfma_f32_16x16x32_bf16 v[92:95], v[202:205], v[152:155], v[92:95]
	v_mfma_f32_16x16x32_bf16 v[84:87], v[194:197], v[172:175], v[84:87]
	v_mfma_f32_16x16x32_bf16 v[76:79], v[202:205], v[172:175], v[76:79]
	v_mfma_f32_16x16x32_bf16 v[68:71], v[194:197], v[186:189], v[68:71]
	v_mfma_f32_16x16x32_bf16 v[64:67], v[202:205], v[186:189], v[64:67]
	v_mfma_f32_16x16x32_bf16 v[116:119], v[198:201], v[148:151], v[116:119]
	v_mfma_f32_16x16x32_bf16 v[108:111], v[206:209], v[148:151], v[108:111]
	v_mfma_f32_16x16x32_bf16 v[100:103], v[198:201], v[156:159], v[100:103]
	v_mfma_f32_16x16x32_bf16 v[92:95], v[206:209], v[156:159], v[92:95]
	v_mfma_f32_16x16x32_bf16 v[84:87], v[198:201], v[182:185], v[84:87]
	v_mfma_f32_16x16x32_bf16 v[76:79], v[206:209], v[182:185], v[76:79]
	v_mfma_f32_16x16x32_bf16 v[68:71], v[198:201], v[190:193], v[68:71]
	v_mfma_f32_16x16x32_bf16 v[64:67], v[206:209], v[190:193], v[64:67]
	s_setprio 0
	s_mov_b32 m0, s45
	v_lshl_add_u64 v[176:177], v[212:213], 0, s[6:7]
	s_barrier
	ds_read_b128 v[144:147], v180 offset:49152
	ds_read_b128 v[148:151], v180 offset:50176
	ds_read_b128 v[152:155], v180 offset:51200
	ds_read_b128 v[156:159], v180 offset:52224
	ds_read_b128 v[172:175], v180 offset:53248
	ds_read_b128 v[182:185], v180 offset:54272
	ds_read_b128 v[186:189], v180 offset:55296
	ds_read_b128 v[190:193], v180 offset:56320
	global_load_lds_dwordx4 v[176:177], off
	v_lshl_add_u64 v[176:177], v[214:215], 0, s[6:7]
	s_mov_b32 m0, s48
	s_nop 0
	global_load_lds_dwordx4 v[176:177], off
	s_barrier
;     __device__ __forceinline__ void operator()(const f32x4 (&acc)[2][2][4][2], const Unit& u, int wr, int wc, int fr, int fq, const Pre&) const {
;         const size_t off0 = (size_t)(u.pm * 256 + wr * 64 + fr) * DM + u.pn * 256 + 32 * wc + 8 * fq;
;         u32x4 rb[2][4][2];
;         if (!RF32) {
; #pragma unroll
;             for (int ai = 0; ai < 2; ++ai)
; #pragma unroll
;                 for (int m = 0; m < 4; ++m)
; #pragma unroll
;                     for (int bj = 0; bj < 2; ++bj) rb[ai][m][bj] = *(const u32x4*)((const bf16_t*)resid + off0 + (size_t)(ai * 128 + m * 16) * DM + 128 * bj);
	s_waitcnt lgkmcnt(0)
	s_setprio 3
	s_waitcnt lgkmcnt(0)
	v_mfma_f32_16x16x32_bf16 v[60:63], v[128:131], v[144:147], v[60:63]
	v_mfma_f32_16x16x32_bf16 v[56:59], v[136:139], v[144:147], v[56:59]
	v_mfma_f32_16x16x32_bf16 v[48:51], v[128:131], v[152:155], v[48:51]
	v_mfma_f32_16x16x32_bf16 v[40:43], v[136:139], v[152:155], v[40:43]
	v_mfma_f32_16x16x32_bf16 v[32:35], v[128:131], v[172:175], v[32:35]
	v_mfma_f32_16x16x32_bf16 v[24:27], v[136:139], v[172:175], v[24:27]
	v_mfma_f32_16x16x32_bf16 v[16:19], v[128:131], v[186:189], v[16:19]
	v_mfma_f32_16x16x32_bf16 v[8:11], v[136:139], v[186:189], v[8:11]
	v_mfma_f32_16x16x32_bf16 v[60:63], v[132:135], v[148:151], v[60:63]
	v_mfma_f32_16x16x32_bf16 v[56:59], v[140:143], v[148:151], v[56:59]
	v_mfma_f32_16x16x32_bf16 v[48:51], v[132:135], v[156:159], v[48:51]
	v_mfma_f32_16x16x32_bf16 v[40:43], v[140:143], v[156:159], v[40:43]
	v_mfma_f32_16x16x32_bf16 v[32:35], v[132:135], v[182:185], v[32:35]
	v_mfma_f32_16x16x32_bf16 v[24:27], v[140:143], v[182:185], v[24:27]
	v_mfma_f32_16x16x32_bf16 v[16:19], v[132:135], v[190:193], v[16:19]
	v_mfma_f32_16x16x32_bf16 v[8:11], v[140:143], v[190:193], v[8:11]
	s_setprio 0
	s_barrier
	s_add_u32 s30, s30, 0x20080
	s_addc_u32 s31, s31, 0
	s_add_i32 s34, s34, s39
	v_lshl_add_u64 v[128:129], s[30:31], 0, v[162:163]
	s_mov_b32 m0, s34
	s_nop 0
	global_load_lds_dwordx4 v[128:129], off
	v_lshl_add_u64 v[128:129], s[30:31], 0, v[166:167]
	s_add_i32 m0, s34, 0x2000
	s_nop 0
	global_load_lds_dwordx4 v[128:129], off
	s_waitcnt vmcnt(6)
	s_barrier
	s_setprio 3
	v_mfma_f32_16x16x32_bf16 v[52:55], v[194:197], v[144:147], v[52:55]
	v_mfma_f32_16x16x32_bf16 v[44:47], v[202:205], v[144:147], v[44:47]
	v_mfma_f32_16x16x32_bf16 v[36:39], v[194:197], v[152:155], v[36:39]
	v_mfma_f32_16x16x32_bf16 v[28:31], v[202:205], v[152:155], v[28:31]
	v_mfma_f32_16x16x32_bf16 v[20:23], v[194:197], v[172:175], v[20:23]
	v_mfma_f32_16x16x32_bf16 v[12:15], v[202:205], v[172:175], v[12:15]
	v_mfma_f32_16x16x32_bf16 v[4:7], v[194:197], v[186:189], v[4:7]
	v_mfma_f32_16x16x32_bf16 v[0:3], v[202:205], v[186:189], v[0:3]
	v_mfma_f32_16x16x32_bf16 v[52:55], v[198:201], v[148:151], v[52:55]
	v_mfma_f32_16x16x32_bf16 v[44:47], v[206:209], v[148:151], v[44:47]
	v_mfma_f32_16x16x32_bf16 v[36:39], v[198:201], v[156:159], v[36:39]
	v_mfma_f32_16x16x32_bf16 v[28:31], v[206:209], v[156:159], v[28:31]
	v_mfma_f32_16x16x32_bf16 v[20:23], v[198:201], v[182:185], v[20:23]
	v_mfma_f32_16x16x32_bf16 v[12:15], v[206:209], v[182:185], v[12:15]
	v_mfma_f32_16x16x32_bf16 v[4:7], v[198:201], v[190:193], v[4:7]
	v_mfma_f32_16x16x32_bf16 v[0:3], v[206:209], v[190:193], v[0:3]
	s_setprio 0
	s_add_i32 s63, s63, 2
	s_add_u32 s28, s28, 0x100
	s_addc_u32 s29, s29, 0
	s_add_u32 s11, s11, 0x100
	s_addc_u32 s62, s62, 0
	s_cmp_gt_u32 s63, 5
	s_barrier
	s_cbranch_scc0 .LBB0_2485
	s_lshl_b32 s11, s16, 8
	v_mbcnt_lo_u32_b32 v130, -1, 0
	v_mbcnt_hi_u32_b32 v130, -1, v130
	s_add_i32 s11, s11, s44
	v_and_or_b32 v128, v130, 15, s11
	s_lshl_b32 s28, s61, 8
	v_ashrrev_i32_e32 v130, 1, v130
	s_ashr_i32 s29, s28, 31
	v_and_b32_e32 v130, -8, v130
	v_ashrrev_i32_e32 v129, 31, v128
	v_ashrrev_i32_e32 v131, 31, v130
	s_or_b64 s[28:29], s[28:29], s[0:1]
	v_lshlrev_b64 v[128:129], 11, v[128:129]
	v_lshl_add_u64 v[130:131], s[28:29], 0, v[130:131]
	v_lshl_add_u64 v[128:129], v[130:131], 0, v[128:129]
	v_lshlrev_b64 v[210:211], 1, v[128:129]
	v_lshl_add_u64 v[128:129], s[2:3], 0, v[210:211]
	v_add_co_u32_e32 v130, vcc, s43, v128
	global_load_dwordx4 v[172:175], v[128:129], off
	global_load_dwordx4 v[182:185], v[128:129], off offset:256
	v_addc_co_u32_e32 v131, vcc, 0, v129, vcc
	global_load_dwordx4 v[186:189], v[130:131], off
	global_load_dwordx4 v[190:193], v[130:131], off offset:256
	v_add_co_u32_e32 v130, vcc, s53, v128
	s_mov_b32 s16, s10
	s_nop 0
	v_addc_co_u32_e32 v131, vcc, 0, v129, vcc
	global_load_dwordx4 v[194:197], v[130:131], off
	global_load_dwordx4 v[198:201], v[130:131], off offset:256
	v_add_co_u32_e32 v130, vcc, s54, v128
	s_mov_b32 s61, s60
	s_nop 0
	v_addc_co_u32_e32 v131, vcc, 0, v129, vcc
	global_load_dwordx4 v[202:205], v[130:131], off
	global_load_dwordx4 v[206:209], v[130:131], off offset:256
	v_add_co_u32_e32 v130, vcc, s55, v128
	s_mov_b64 s[30:31], s[14:15]
	s_nop 0
	v_addc_co_u32_e32 v131, vcc, 0, v129, vcc
	v_add_co_u32_e32 v132, vcc, s56, v128
	s_mov_b64 s[28:29], s[12:13]
	s_nop 0
	v_addc_co_u32_e32 v133, vcc, 0, v129, vcc
	v_add_co_u32_e32 v134, vcc, s57, v128
	s_waitcnt vmcnt(0)
; __device__ __forceinline__ float bf_lo(unsigned w) { return __uint_as_float(w << 16); }
; __device__ __forceinline__ float bf_hi(unsigned w) { return __uint_as_float(w & 0xffff0000u); }
;     __device__ __forceinline__ void operator()(const f32x4 (&acc)[2][2][4][2], const Unit& u, int wr, int wc, int fr, int fq, const Pre&) const {
;     ...
; #pragma unroll
;         for (int ai = 0; ai < 2; ++ai) {
;             f32x4 r0[4][2], r1[4][2];
; #pragma unroll
;             for (int m = 0; m < 4; ++m)
; #pragma unroll
;                 for (int bj = 0; bj < 2; ++bj) {
;                     const size_t off = off0 + (size_t)(ai * 128 + m * 16) * DM + 128 * bj;
;                     if (RF32) { r0[m][bj] = *(const f32x4*)((const float*)resid + off); r1[m][bj] = *(const f32x4*)((const float*)resid + off + 4); }
;                     else { const u32x4 rbv = rb[ai][m][bj];
;                         r0[m][bj] = (f32x4){bf_lo(rbv.x), bf_hi(rbv.x), bf_lo(rbv.y), bf_hi(rbv.y)}; r1[m][bj] = (f32x4){bf_lo(rbv.z), bf_hi(rbv.z), bf_lo(rbv.w), bf_hi(rbv.w)}; }
;                 }
; #pragma unroll
;             for (int m = 0; m < 4; ++m) {
;                 const int row = u.pm * 256 + ai * 128 + wr * 64 + m * 16 + fr; float sq = 0.f;
; #pragma unroll
;                 for (int bj = 0; bj < 2; ++bj) {
;                     const size_t off = off0 + (size_t)(ai * 128 + m * 16) * DM + 128 * bj;
;                     const f32x4 v0 = acc[ai][bj][m][0] + r0[m][bj], v1 = acc[ai][bj][m][1] + r1[m][bj];
;                     st_bf16x8(hb + off, v0, v1);
;                     sq += v0[0] * v0[0] + v0[1] * v0[1] + v0[2] * v0[2] + v0[3] * v0[3] + v1[0] * v1[0] + v1[1] * v1[1] + v1[2] * v1[2] + v1[3] * v1[3];
;                 }
	v_lshlrev_b32_e32 v212, 16, v172
	v_addc_co_u32_e32 v135, vcc, 0, v129, vcc
	v_add_co_u32_e32 v128, vcc, s58, v128
	v_and_b32_e32 v213, 0xffff0000, v172
	s_nop 0
	v_addc_co_u32_e32 v129, vcc, 0, v129, vcc
	global_load_dwordx4 v[156:159], v[130:131], off
	global_load_dwordx4 v[152:155], v[130:131], off offset:256
	global_load_dwordx4 v[148:151], v[132:133], off
	global_load_dwordx4 v[144:147], v[132:133], off offset:256
	global_load_dwordx4 v[140:143], v[134:135], off
	global_load_dwordx4 v[136:139], v[134:135], off offset:256
	s_nop 0
	global_load_dwordx4 v[132:135], v[128:129], off
	s_nop 0
	global_load_dwordx4 v[128:131], v[128:129], off offset:256
	v_lshlrev_b32_e32 v214, 16, v173
	v_and_b32_e32 v215, 0xffff0000, v173
	v_lshlrev_b32_e32 v216, 16, v174
	v_and_b32_e32 v217, 0xffff0000, v174
	v_lshlrev_b32_e32 v218, 16, v175
	v_and_b32_e32 v219, 0xffff0000, v175
	v_lshlrev_b32_e32 v220, 16, v182
	v_and_b32_e32 v221, 0xffff0000, v182
	v_lshlrev_b32_e32 v182, 16, v183
	v_and_b32_e32 v183, 0xffff0000, v183
	v_lshlrev_b32_e32 v222, 16, v184
	v_and_b32_e32 v223, 0xffff0000, v184
	v_lshlrev_b32_e32 v184, 16, v185
	v_and_b32_e32 v185, 0xffff0000, v185
	v_lshlrev_b32_e32 v172, 16, v208
	v_and_b32_e32 v173, 0xffff0000, v208
	v_lshlrev_b32_e32 v176, 16, v209
	v_and_b32_e32 v177, 0xffff0000, v209
	v_pk_add_f32 v[126:127], v[126:127], v[214:215]
	v_pk_add_f32 v[124:125], v[124:125], v[212:213]
	v_pk_add_f32 v[208:209], v[122:123], v[218:219]
	v_pk_add_f32 v[212:213], v[120:121], v[216:217]
	v_lshl_add_u64 v[120:121], s[4:5], 0, v[210:211]
	v_cvt_pk_bf16_f32 v122, v124, v125
	v_cvt_pk_bf16_f32 v123, v126, v127
	v_lshlrev_b32_e32 v224, 16, v186
	v_and_b32_e32 v225, 0xffff0000, v186
	v_lshlrev_b32_e32 v186, 16, v187
	v_and_b32_e32 v187, 0xffff0000, v187
	v_cvt_pk_bf16_f32 v124, v212, v213
	v_cvt_pk_bf16_f32 v125, v208, v209
	global_store_dwordx4 v[120:121], v[122:125], off
	v_pk_add_f32 v[118:119], v[118:119], v[182:183]
	v_pk_add_f32 v[116:117], v[116:117], v[220:221]
	v_pk_add_f32 v[122:123], v[110:111], v[184:185]
	v_pk_add_f32 v[110:111], v[108:109], v[222:223]
	v_cvt_pk_bf16_f32 v108, v116, v117
	v_cvt_pk_bf16_f32 v109, v118, v119
	v_lshlrev_b32_e32 v226, 16, v188
	v_and_b32_e32 v227, 0xffff0000, v188
	v_lshlrev_b32_e32 v188, 16, v189
	v_and_b32_e32 v189, 0xffff0000, v189
	v_cvt_pk_bf16_f32 v110, v110, v111
	v_cvt_pk_bf16_f32 v111, v122, v123
	global_store_dwordx4 v[120:121], v[108:111], off offset:256
	v_lshlrev_b32_e32 v228, 16, v190
	v_and_b32_e32 v229, 0xffff0000, v190
	v_pk_add_f32 v[108:109], v[114:115], v[186:187]
	v_pk_add_f32 v[110:111], v[112:113], v[224:225]
	v_pk_add_f32 v[112:113], v[106:107], v[188:189]
	v_pk_add_f32 v[106:107], v[104:105], v[226:227]
	v_cvt_pk_bf16_f32 v104, v110, v111
	v_cvt_pk_bf16_f32 v105, v108, v109
	v_add_co_u32_e32 v108, vcc, s43, v120
	v_lshlrev_b32_e32 v190, 16, v191
	v_and_b32_e32 v191, 0xffff0000, v191
	v_lshlrev_b32_e32 v230, 16, v192
	v_and_b32_e32 v231, 0xffff0000, v192
	v_lshlrev_b32_e32 v192, 16, v193
	v_and_b32_e32 v193, 0xffff0000, v193
	v_addc_co_u32_e32 v109, vcc, 0, v121, vcc
	v_lshlrev_b32_e32 v232, 16, v194
	v_and_b32_e32 v233, 0xffff0000, v194
	v_lshlrev_b32_e32 v194, 16, v195
	v_and_b32_e32 v195, 0xffff0000, v195
	v_cvt_pk_bf16_f32 v106, v106, v107
	v_cvt_pk_bf16_f32 v107, v112, v113
	global_store_dwordx4 v[108:109], v[104:107], off
	v_pk_add_f32 v[102:103], v[102:103], v[190:191]
	v_pk_add_f32 v[100:101], v[100:101], v[228:229]
	v_pk_add_f32 v[104:105], v[94:95], v[192:193]
	v_pk_add_f32 v[94:95], v[92:93], v[230:231]
	v_cvt_pk_bf16_f32 v92, v100, v101
	v_cvt_pk_bf16_f32 v93, v102, v103
	v_lshlrev_b32_e32 v234, 16, v196
	v_and_b32_e32 v235, 0xffff0000, v196
	v_lshlrev_b32_e32 v196, 16, v197
	v_and_b32_e32 v197, 0xffff0000, v197
	v_cvt_pk_bf16_f32 v94, v94, v95
	v_cvt_pk_bf16_f32 v95, v104, v105
	global_store_dwordx4 v[108:109], v[92:95], off offset:256
	v_lshlrev_b32_e32 v236, 16, v198
	v_and_b32_e32 v237, 0xffff0000, v198
	v_pk_add_f32 v[92:93], v[98:99], v[194:195]
	v_pk_add_f32 v[94:95], v[96:97], v[232:233]
	v_pk_add_f32 v[96:97], v[90:91], v[196:197]
	v_pk_add_f32 v[90:91], v[88:89], v[234:235]
	v_cvt_pk_bf16_f32 v88, v94, v95
	v_cvt_pk_bf16_f32 v89, v92, v93
	v_add_co_u32_e32 v92, vcc, s53, v120
	v_lshlrev_b32_e32 v198, 16, v199
	v_and_b32_e32 v199, 0xffff0000, v199
	v_lshlrev_b32_e32 v238, 16, v200
	v_and_b32_e32 v239, 0xffff0000, v200
	v_lshlrev_b32_e32 v200, 16, v201
	v_and_b32_e32 v201, 0xffff0000, v201
	v_addc_co_u32_e32 v93, vcc, 0, v121, vcc
	v_lshlrev_b32_e32 v240, 16, v202
	v_and_b32_e32 v241, 0xffff0000, v202
	v_lshlrev_b32_e32 v202, 16, v203
	v_and_b32_e32 v203, 0xffff0000, v203
	v_cvt_pk_bf16_f32 v90, v90, v91
	v_cvt_pk_bf16_f32 v91, v96, v97
	global_store_dwordx4 v[92:93], v[88:91], off
	v_pk_add_f32 v[86:87], v[86:87], v[198:199]
	v_pk_add_f32 v[84:85], v[84:85], v[236:237]
	v_pk_add_f32 v[88:89], v[78:79], v[200:201]
	v_pk_add_f32 v[78:79], v[76:77], v[238:239]
	v_cvt_pk_bf16_f32 v76, v84, v85
	v_cvt_pk_bf16_f32 v77, v86, v87
	v_lshlrev_b32_e32 v242, 16, v204
	v_and_b32_e32 v243, 0xffff0000, v204
	v_lshlrev_b32_e32 v204, 16, v205
	v_and_b32_e32 v205, 0xffff0000, v205
	v_cvt_pk_bf16_f32 v78, v78, v79
	v_cvt_pk_bf16_f32 v79, v88, v89
	global_store_dwordx4 v[92:93], v[76:79], off offset:256
	v_lshlrev_b32_e32 v174, 16, v206
	v_and_b32_e32 v175, 0xffff0000, v206
	v_pk_add_f32 v[76:77], v[82:83], v[202:203]
	v_pk_add_f32 v[78:79], v[80:81], v[240:241]
	v_pk_add_f32 v[80:81], v[74:75], v[204:205]
	v_pk_add_f32 v[74:75], v[72:73], v[242:243]
	v_cvt_pk_bf16_f32 v72, v78, v79
	v_cvt_pk_bf16_f32 v73, v76, v77
	v_add_co_u32_e32 v76, vcc, s54, v120
	v_lshlrev_b32_e32 v206, 16, v207
	s_nop 0
	v_addc_co_u32_e32 v77, vcc, 0, v121, vcc
	v_and_b32_e32 v207, 0xffff0000, v207
	v_cvt_pk_bf16_f32 v74, v74, v75
	v_cvt_pk_bf16_f32 v75, v80, v81
	global_store_dwordx4 v[76:77], v[72:75], off
	v_pk_add_f32 v[70:71], v[70:71], v[206:207]
	v_pk_add_f32 v[68:69], v[68:69], v[174:175]
	v_pk_add_f32 v[72:73], v[66:67], v[176:177]
	v_pk_add_f32 v[66:67], v[64:65], v[172:173]
	v_cvt_pk_bf16_f32 v64, v68, v69
	v_cvt_pk_bf16_f32 v65, v70, v71
	s_waitcnt vmcnt(0)
; __device__ __forceinline__ float bf_lo(unsigned w) { return __uint_as_float(w << 16); }
; __device__ __forceinline__ float bf_hi(unsigned w) { return __uint_as_float(w & 0xffff0000u); }
;     __device__ __forceinline__ void operator()(const f32x4 (&acc)[2][2][4][2], const Unit& u, int wr, int wc, int fr, int fq, const Pre&) const {
;     ...
;         for (int ai = 0; ai < 2; ++ai) {
;             f32x4 r0[4][2], r1[4][2];
; #pragma unroll
;             for (int m = 0; m < 4; ++m)
; #pragma unroll
;                 for (int bj = 0; bj < 2; ++bj) {
;                     const size_t off = off0 + (size_t)(ai * 128 + m * 16) * DM + 128 * bj;
;                     if (RF32) { r0[m][bj] = *(const f32x4*)((const float*)resid + off); r1[m][bj] = *(const f32x4*)((const float*)resid + off + 4); }
;                     else { const u32x4 rbv = rb[ai][m][bj];
;                         r0[m][bj] = (f32x4){bf_lo(rbv.x), bf_hi(rbv.x), bf_lo(rbv.y), bf_hi(rbv.y)}; r1[m][bj] = (f32x4){bf_lo(rbv.z), bf_hi(rbv.z), bf_lo(rbv.w), bf_hi(rbv.w)}; }
;                 }
; #pragma unroll
;             for (int m = 0; m < 4; ++m) {
;                 const int row = u.pm * 256 + ai * 128 + wr * 64 + m * 16 + fr; float sq = 0.f;
; #pragma unroll
;                 for (int bj = 0; bj < 2; ++bj) {
;                     const size_t off = off0 + (size_t)(ai * 128 + m * 16) * DM + 128 * bj;
;                     const f32x4 v0 = acc[ai][bj][m][0] + r0[m][bj], v1 = acc[ai][bj][m][1] + r1[m][bj];
;                     st_bf16x8(hb + off, v0, v1);
;                     sq += v0[0] * v0[0] + v0[1] * v0[1] + v0[2] * v0[2] + v0[3] * v0[3] + v1[0] * v1[0] + v1[1] * v1[1] + v1[2] * v1[2] + v1[3] * v1[3];
;                 }
	v_lshlrev_b32_e32 v78, 16, v159
	v_cvt_pk_bf16_f32 v66, v66, v67
	v_cvt_pk_bf16_f32 v67, v72, v73
	v_lshlrev_b32_e32 v72, 16, v156
	v_and_b32_e32 v73, 0xffff0000, v156
	global_store_dwordx4 v[76:77], v[64:67], off offset:256
	v_lshlrev_b32_e32 v76, 16, v158
	v_and_b32_e32 v77, 0xffff0000, v158
	v_and_b32_e32 v79, 0xffff0000, v159
	v_pk_add_f32 v[60:61], v[60:61], v[72:73]
	v_lshlrev_b32_e32 v74, 16, v157
	v_and_b32_e32 v75, 0xffff0000, v157
	v_pk_add_f32 v[72:73], v[58:59], v[78:79]
	v_pk_add_f32 v[58:59], v[56:57], v[76:77]
	v_cvt_pk_bf16_f32 v56, v60, v61
	v_add_co_u32_e32 v60, vcc, s55, v120
	v_lshlrev_b32_e32 v80, 16, v152
	v_and_b32_e32 v81, 0xffff0000, v152
	v_lshlrev_b32_e32 v82, 16, v153
	v_and_b32_e32 v83, 0xffff0000, v153
	v_lshlrev_b32_e32 v84, 16, v154
	v_and_b32_e32 v85, 0xffff0000, v154
	v_lshlrev_b32_e32 v86, 16, v155
	v_and_b32_e32 v87, 0xffff0000, v155
	v_pk_add_f32 v[62:63], v[62:63], v[74:75]
	v_addc_co_u32_e32 v61, vcc, 0, v121, vcc
	v_cvt_pk_bf16_f32 v57, v62, v63
	v_lshlrev_b32_e32 v90, 16, v149
	v_and_b32_e32 v91, 0xffff0000, v149
	v_cvt_pk_bf16_f32 v58, v58, v59
	v_cvt_pk_bf16_f32 v59, v72, v73
	global_store_dwordx4 v[60:61], v[56:59], off
	v_pk_add_f32 v[54:55], v[54:55], v[82:83]
	v_pk_add_f32 v[52:53], v[52:53], v[80:81]
	v_pk_add_f32 v[56:57], v[46:47], v[86:87]
	v_pk_add_f32 v[46:47], v[44:45], v[84:85]
	v_cvt_pk_bf16_f32 v44, v52, v53
	v_cvt_pk_bf16_f32 v45, v54, v55
	v_lshlrev_b32_e32 v88, 16, v148
	v_and_b32_e32 v89, 0xffff0000, v148
	v_lshlrev_b32_e32 v92, 16, v150
	v_and_b32_e32 v93, 0xffff0000, v150
	v_lshlrev_b32_e32 v94, 16, v151
	v_and_b32_e32 v95, 0xffff0000, v151
	v_cvt_pk_bf16_f32 v46, v46, v47
	v_cvt_pk_bf16_f32 v47, v56, v57
	global_store_dwordx4 v[60:61], v[44:47], off offset:256
	v_lshlrev_b32_e32 v96, 16, v144
	v_and_b32_e32 v97, 0xffff0000, v144
	v_pk_add_f32 v[44:45], v[50:51], v[90:91]
	v_pk_add_f32 v[46:47], v[48:49], v[88:89]
	v_pk_add_f32 v[48:49], v[42:43], v[94:95]
	v_pk_add_f32 v[42:43], v[40:41], v[92:93]
	v_cvt_pk_bf16_f32 v40, v46, v47
	v_cvt_pk_bf16_f32 v41, v44, v45
	v_add_co_u32_e32 v44, vcc, s56, v120
	v_lshlrev_b32_e32 v98, 16, v145
	v_and_b32_e32 v99, 0xffff0000, v145
	v_lshlrev_b32_e32 v100, 16, v146
	v_and_b32_e32 v101, 0xffff0000, v146
	v_lshlrev_b32_e32 v102, 16, v147
	v_and_b32_e32 v103, 0xffff0000, v147
	v_addc_co_u32_e32 v45, vcc, 0, v121, vcc
	v_lshlrev_b32_e32 v106, 16, v141
	v_and_b32_e32 v107, 0xffff0000, v141
	v_cvt_pk_bf16_f32 v42, v42, v43
	v_cvt_pk_bf16_f32 v43, v48, v49
	global_store_dwordx4 v[44:45], v[40:43], off
	v_pk_add_f32 v[38:39], v[38:39], v[98:99]
	v_pk_add_f32 v[36:37], v[36:37], v[96:97]
	v_pk_add_f32 v[40:41], v[30:31], v[102:103]
	v_pk_add_f32 v[30:31], v[28:29], v[100:101]
	v_cvt_pk_bf16_f32 v28, v36, v37
	v_cvt_pk_bf16_f32 v29, v38, v39
	v_lshlrev_b32_e32 v104, 16, v140
	v_and_b32_e32 v105, 0xffff0000, v140
	v_lshlrev_b32_e32 v108, 16, v142
	v_and_b32_e32 v109, 0xffff0000, v142
	v_lshlrev_b32_e32 v110, 16, v143
	v_and_b32_e32 v111, 0xffff0000, v143
	v_cvt_pk_bf16_f32 v30, v30, v31
	v_cvt_pk_bf16_f32 v31, v40, v41
	global_store_dwordx4 v[44:45], v[28:31], off offset:256
	v_lshlrev_b32_e32 v112, 16, v136
	v_and_b32_e32 v113, 0xffff0000, v136
	v_pk_add_f32 v[28:29], v[34:35], v[106:107]
	v_pk_add_f32 v[30:31], v[32:33], v[104:105]
	v_pk_add_f32 v[32:33], v[26:27], v[110:111]
	v_pk_add_f32 v[26:27], v[24:25], v[108:109]
	v_cvt_pk_bf16_f32 v24, v30, v31
	v_cvt_pk_bf16_f32 v25, v28, v29
	v_add_co_u32_e32 v28, vcc, s57, v120
	v_lshlrev_b32_e32 v114, 16, v137
	v_and_b32_e32 v115, 0xffff0000, v137
	v_lshlrev_b32_e32 v116, 16, v138
	v_and_b32_e32 v117, 0xffff0000, v138
	v_lshlrev_b32_e32 v118, 16, v139
	v_and_b32_e32 v119, 0xffff0000, v139
	v_addc_co_u32_e32 v29, vcc, 0, v121, vcc
	v_lshlrev_b32_e32 v124, 16, v133
	v_and_b32_e32 v125, 0xffff0000, v133
	v_cvt_pk_bf16_f32 v26, v26, v27
	v_cvt_pk_bf16_f32 v27, v32, v33
	global_store_dwordx4 v[28:29], v[24:27], off
	v_pk_add_f32 v[22:23], v[22:23], v[114:115]
	v_pk_add_f32 v[20:21], v[20:21], v[112:113]
	v_pk_add_f32 v[24:25], v[14:15], v[118:119]
	v_pk_add_f32 v[14:15], v[12:13], v[116:117]
	v_cvt_pk_bf16_f32 v12, v20, v21
	v_cvt_pk_bf16_f32 v13, v22, v23
	v_lshlrev_b32_e32 v122, 16, v132
	v_and_b32_e32 v123, 0xffff0000, v132
	v_lshlrev_b32_e32 v126, 16, v134
	v_and_b32_e32 v127, 0xffff0000, v134
	v_lshlrev_b32_e32 v132, 16, v135
	v_and_b32_e32 v133, 0xffff0000, v135
	v_cvt_pk_bf16_f32 v14, v14, v15
	v_cvt_pk_bf16_f32 v15, v24, v25
	global_store_dwordx4 v[28:29], v[12:15], off offset:256
	v_lshlrev_b32_e32 v64, 16, v130
	v_and_b32_e32 v65, 0xffff0000, v130
	v_pk_add_f32 v[12:13], v[18:19], v[124:125]
	v_pk_add_f32 v[14:15], v[16:17], v[122:123]
	v_pk_add_f32 v[16:17], v[10:11], v[132:133]
	v_pk_add_f32 v[10:11], v[8:9], v[126:127]
	v_cvt_pk_bf16_f32 v8, v14, v15
	v_cvt_pk_bf16_f32 v9, v12, v13
	v_add_co_u32_e32 v12, vcc, s58, v120
	v_lshlrev_b32_e32 v68, 16, v131
	v_and_b32_e32 v69, 0xffff0000, v131
	v_addc_co_u32_e32 v13, vcc, 0, v121, vcc
	v_lshlrev_b32_e32 v66, 16, v128
	v_and_b32_e32 v67, 0xffff0000, v128
	v_lshlrev_b32_e32 v70, 16, v129
	v_and_b32_e32 v71, 0xffff0000, v129
	v_cvt_pk_bf16_f32 v10, v10, v11
	v_cvt_pk_bf16_f32 v11, v16, v17
	global_store_dwordx4 v[12:13], v[8:11], off
	s_and_b64 vcc, exec, s[8:9]
	v_pk_add_f32 v[6:7], v[6:7], v[70:71]
	v_pk_add_f32 v[8:9], v[2:3], v[68:69]
	v_pk_add_f32 v[2:3], v[0:1], v[64:65]
	v_pk_add_f32 v[4:5], v[4:5], v[66:67]
	s_nop 0
	v_cvt_pk_bf16_f32 v0, v4, v5
	v_cvt_pk_bf16_f32 v1, v6, v7
	v_cvt_pk_bf16_f32 v2, v2, v3
	v_cvt_pk_bf16_f32 v3, v8, v9
	global_store_dwordx4 v[12:13], v[0:3], off offset:256
	s_cbranch_vccz .LBB0_2478
	s_waitcnt vmcnt(0)
	s_cmpk_gt_u32 s96, 0xff
	s_cbranch_scc1 .LBB0_2489
	s_barrier

.LBB0_2704:
	s_add_u32 s0, s0, 0x40000
	s_addc_u32 s1, s1, 0
	s_mov_b32 m0, s67
	v_lshl_add_u64 v[48:49], s[0:1], 0, v[198:199]
	global_load_lds_dwordx4 v[48:49], off
	v_lshl_add_u64 v[48:49], s[0:1], 0, v[194:195]
	s_mov_b32 m0, s68
	s_nop 0
	global_load_lds_dwordx4 v[48:49], off
	s_waitcnt lgkmcnt(8)
	s_barrier
	s_waitcnt lgkmcnt(0)
	s_setprio 3
	s_waitcnt lgkmcnt(0)
	v_mfma_f32_16x16x128_f8f6f4 v[188:191], v[8:15], v[40:47], v[188:191]
	v_mfma_f32_16x16x128_f8f6f4 v[184:187], v[0:7], v[40:47], v[184:187]
	v_mfma_f32_16x16x128_f8f6f4 v[172:175], v[8:15], v[32:39], v[172:175]
	v_mfma_f32_16x16x128_f8f6f4 v[164:167], v[0:7], v[32:39], v[164:167]
	v_mfma_f32_16x16x128_f8f6f4 v[156:159], v[8:15], v[24:31], v[156:159]
	v_mfma_f32_16x16x128_f8f6f4 v[148:151], v[0:7], v[24:31], v[148:151]
	v_mfma_f32_16x16x128_f8f6f4 v[140:143], v[8:15], v[16:23], v[140:143]
	v_mfma_f32_16x16x128_f8f6f4 v[132:135], v[0:7], v[16:23], v[132:135]
	s_setprio 0
	s_barrier
	s_add_i32 s0, 0, 0x1c000
	s_mov_b32 m0, s77
	v_add_u32_e32 v60, s0, v244
	v_lshl_add_u64 v[234:235], v[234:235], 0, s[14:15]
	ds_read_b128 v[48:51], v60
	ds_read_b128 v[52:55], v60 offset:1024
	ds_read_b128 v[56:59], v60 offset:2048
	ds_read_b128 v[60:63], v60 offset:3072
	global_load_lds_dwordx4 v[234:235], off
	v_lshl_add_u64 v[234:235], v[236:237], 0, s[14:15]
	s_mov_b32 m0, s78
	s_nop 0
	global_load_lds_dwordx4 v[234:235], off
	s_barrier
	s_waitcnt lgkmcnt(0)
	s_setprio 3
	s_waitcnt lgkmcnt(0)
	v_mfma_f32_16x16x128_f8f6f4 v[180:183], v[48:55], v[40:47], v[180:183]
	v_mfma_f32_16x16x128_f8f6f4 v[176:179], v[56:63], v[40:47], v[176:179]
	v_mfma_f32_16x16x128_f8f6f4 v[168:171], v[48:55], v[32:39], v[168:171]
	v_mfma_f32_16x16x128_f8f6f4 v[160:163], v[56:63], v[32:39], v[160:163]
	v_mfma_f32_16x16x128_f8f6f4 v[152:155], v[48:55], v[24:31], v[152:155]
	v_mfma_f32_16x16x128_f8f6f4 v[144:147], v[56:63], v[24:31], v[144:147]
	v_mfma_f32_16x16x128_f8f6f4 v[136:139], v[48:55], v[16:23], v[136:139]
	v_mfma_f32_16x16x128_f8f6f4 v[128:131], v[56:63], v[16:23], v[128:131]
	s_setprio 0
	s_mov_b32 m0, s79
	v_lshl_add_u64 v[234:235], v[238:239], 0, s[14:15]
	s_barrier
	ds_read_b128 v[16:19], v246 offset:49152
	ds_read_b128 v[20:23], v246 offset:50176
	ds_read_b128 v[24:27], v246 offset:51200
	ds_read_b128 v[28:31], v246 offset:52224
	ds_read_b128 v[32:35], v246 offset:53248
	ds_read_b128 v[36:39], v246 offset:54272
	ds_read_b128 v[40:43], v246 offset:55296
	ds_read_b128 v[44:47], v246 offset:56320
	global_load_lds_dwordx4 v[234:235], off
	v_lshl_add_u64 v[234:235], v[240:241], 0, s[14:15]
	s_mov_b32 m0, s80
	s_nop 0
	global_load_lds_dwordx4 v[234:235], off
	s_barrier
	s_waitcnt lgkmcnt(0)
	s_setprio 3
	s_waitcnt lgkmcnt(0)
	v_mfma_f32_16x16x128_f8f6f4 v[116:119], v[8:15], v[16:23], v[116:119]
	v_mfma_f32_16x16x128_f8f6f4 v[108:111], v[0:7], v[16:23], v[108:111]
	v_mfma_f32_16x16x128_f8f6f4 v[100:103], v[8:15], v[24:31], v[100:103]
	v_mfma_f32_16x16x128_f8f6f4 v[92:95], v[0:7], v[24:31], v[92:95]
	v_mfma_f32_16x16x128_f8f6f4 v[84:87], v[8:15], v[32:39], v[84:87]
	v_mfma_f32_16x16x128_f8f6f4 v[76:79], v[0:7], v[32:39], v[76:79]
	v_mfma_f32_16x16x128_f8f6f4 v[68:71], v[8:15], v[40:47], v[68:71]
	v_mfma_f32_16x16x128_f8f6f4 v[64:67], v[0:7], v[40:47], v[64:67]
	s_setprio 0
	s_barrier
	v_lshl_add_u64 v[0:1], v[232:233], 0, s[16:17]
	s_add_i32 s0, s0, s61
	v_lshl_add_u64 v[2:3], v[0:1], 0, v[196:197]
	s_mov_b32 m0, s0
	v_lshl_add_u64 v[0:1], v[0:1], 0, v[192:193]
	global_load_lds_dwordx4 v[2:3], off
	s_add_i32 m0, s0, 0x2000
	s_nop 0
	global_load_lds_dwordx4 v[0:1], off
	s_waitcnt vmcnt(6)
	s_barrier
	s_setprio 3
	v_mfma_f32_16x16x128_f8f6f4 v[124:127], v[48:55], v[16:23], v[124:127]
	v_mfma_f32_16x16x128_f8f6f4 v[120:123], v[56:63], v[16:23], v[120:123]
	v_mfma_f32_16x16x128_f8f6f4 v[112:115], v[48:55], v[24:31], v[112:115]
	v_mfma_f32_16x16x128_f8f6f4 v[104:107], v[56:63], v[24:31], v[104:107]
	v_mfma_f32_16x16x128_f8f6f4 v[96:99], v[48:55], v[32:39], v[96:99]
	v_mfma_f32_16x16x128_f8f6f4 v[88:91], v[56:63], v[32:39], v[88:91]
	v_mfma_f32_16x16x128_f8f6f4 v[80:83], v[48:55], v[40:47], v[80:83]
	v_mfma_f32_16x16x128_f8f6f4 v[72:75], v[56:63], v[40:47], v[72:75]
	s_setprio 0
	s_add_i32 s39, s39, 2
	s_add_u32 s52, s52, 0x100
	s_addc_u32 s53, s53, 0
	s_cmp_gt_u32 s39, 13
	v_lshl_add_u64 v[230:231], v[230:231], 0, s[30:31]
	s_barrier
	s_cbranch_scc1 .LBB0_2717
.LBB0_2705:
	v_add_u32_e32 v225, 0, v244
	v_add_u32_e32 v12, 0x10000, v225
	ds_read_b128 v[0:3], v12
	ds_read_b128 v[4:7], v12 offset:1024
	ds_read_b128 v[8:11], v12 offset:2048
	ds_read_b128 v[12:15], v12 offset:3072
	s_xor_b64 s[54:55], s[46:47], -1
	v_lshl_add_u64 v[16:17], s[52:53], 0, v[210:211]
	s_add_i32 m0, s51, 0xc000
	ds_read_b128 v[56:59], v246
	ds_read_b128 v[60:63], v246 offset:1024
	ds_read_b128 v[48:51], v246 offset:2048
	ds_read_b128 v[52:55], v246 offset:3072
	ds_read_b128 v[40:43], v246 offset:4096
	ds_read_b128 v[44:47], v246 offset:5120
	ds_read_b128 v[32:35], v246 offset:6144
	ds_read_b128 v[36:39], v246 offset:7168
	global_load_lds_dwordx4 v[16:17], off
	v_lshl_add_u64 v[16:17], s[52:53], 0, v[212:213]
	s_add_i32 m0, s51, 0xe000
	s_nop 0
	global_load_lds_dwordx4 v[16:17], off
	s_waitcnt lgkmcnt(8)
	s_barrier
	s_waitcnt lgkmcnt(0)
	s_setprio 3
	s_waitcnt lgkmcnt(0)
	v_mfma_f32_16x16x128_f8f6f4 v[188:191], v[0:7], v[56:63], v[188:191]
	v_mfma_f32_16x16x128_f8f6f4 v[184:187], v[8:15], v[56:63], v[184:187]
	v_mfma_f32_16x16x128_f8f6f4 v[172:175], v[0:7], v[48:55], v[172:175]
	v_mfma_f32_16x16x128_f8f6f4 v[164:167], v[8:15], v[48:55], v[164:167]
	v_mfma_f32_16x16x128_f8f6f4 v[156:159], v[0:7], v[40:47], v[156:159]
	v_mfma_f32_16x16x128_f8f6f4 v[148:151], v[8:15], v[40:47], v[148:151]
	v_mfma_f32_16x16x128_f8f6f4 v[140:143], v[0:7], v[32:39], v[140:143]
	v_mfma_f32_16x16x128_f8f6f4 v[132:135], v[8:15], v[32:39], v[132:135]
	s_setprio 0
	s_barrier
	v_add_u32_e32 v20, 0x14000, v225
	ds_read_b128 v[24:27], v20
	ds_read_b128 v[28:31], v20 offset:1024
	ds_read_b128 v[16:19], v20 offset:2048
	ds_read_b128 v[20:23], v20 offset:3072
	s_and_b64 vcc, exec, s[54:55]
	s_cbranch_vccnz .LBB0_2707
	v_add_u32_e32 v220, v243, v242
	ds_read2_b32 v[214:215], v220 offset1:32
	ds_read2_b32 v[216:217], v220 offset0:64 offset1:96
	ds_read2_b32 v[218:219], v220 offset0:128 offset1:160
	ds_read2_b32 v[220:221], v220 offset0:192 offset1:224

.LBB0_2709:
	s_setprio 3
	s_waitcnt lgkmcnt(0)
	v_mfma_f32_16x16x128_f8f6f4 v[180:183], v[24:31], v[56:63], v[180:183]
	v_mfma_f32_16x16x128_f8f6f4 v[176:179], v[16:23], v[56:63], v[176:179]
	v_mfma_f32_16x16x128_f8f6f4 v[168:171], v[24:31], v[48:55], v[168:171]
	v_mfma_f32_16x16x128_f8f6f4 v[160:163], v[16:23], v[48:55], v[160:163]
	v_mfma_f32_16x16x128_f8f6f4 v[152:155], v[24:31], v[40:47], v[152:155]
	v_mfma_f32_16x16x128_f8f6f4 v[144:147], v[16:23], v[40:47], v[144:147]
	v_mfma_f32_16x16x128_f8f6f4 v[136:139], v[24:31], v[32:39], v[136:139]
	v_mfma_f32_16x16x128_f8f6f4 v[128:131], v[16:23], v[32:39], v[128:131]
	s_setprio 0
	s_barrier
	ds_read_b128 v[56:59], v246 offset:16384
	ds_read_b128 v[60:63], v246 offset:17408
	ds_read_b128 v[48:51], v246 offset:18432
	ds_read_b128 v[52:55], v246 offset:19456
	ds_read_b128 v[40:43], v246 offset:20480
	ds_read_b128 v[44:47], v246 offset:21504
	ds_read_b128 v[32:35], v246 offset:22528
	ds_read_b128 v[36:39], v246 offset:23552
	s_and_b64 vcc, exec, s[2:3]
	s_cbranch_vccnz .LBB0_2711
	v_lshl_add_u64 v[238:239], v[206:207], 0, s[28:29]
	global_store_dwordx2 v[238:239], v[222:223], off
.LBB0_2711:
	s_add_u32 s2, s52, 0xfffc0080
	s_addc_u32 s3, s53, -1
	s_and_b64 s[0:1], s[0:1], exec
	s_cselect_b32 s1, s45, s3
	s_cselect_b32 s0, s44, s2
	s_mov_b32 m0, s51
	v_lshl_add_u64 v[238:239], s[0:1], 0, v[198:199]
	global_load_lds_dwordx4 v[238:239], off
	v_lshl_add_u64 v[240:241], s[0:1], 0, v[194:195]
	s_mov_b32 m0, s64
	s_nop 0
	global_load_lds_dwordx4 v[240:241], off
	s_barrier
	s_waitcnt lgkmcnt(0)
	s_setprio 3
	s_waitcnt lgkmcnt(0)
	v_mfma_f32_16x16x128_f8f6f4 v[116:119], v[0:7], v[56:63], v[116:119]
	v_mfma_f32_16x16x128_f8f6f4 v[108:111], v[8:15], v[56:63], v[108:111]
	v_mfma_f32_16x16x128_f8f6f4 v[100:103], v[0:7], v[48:55], v[100:103]
	v_mfma_f32_16x16x128_f8f6f4 v[92:95], v[8:15], v[48:55], v[92:95]
	v_mfma_f32_16x16x128_f8f6f4 v[84:87], v[0:7], v[40:47], v[84:87]
	v_mfma_f32_16x16x128_f8f6f4 v[76:79], v[8:15], v[40:47], v[76:79]
	v_mfma_f32_16x16x128_f8f6f4 v[68:71], v[0:7], v[32:39], v[68:71]
	v_mfma_f32_16x16x128_f8f6f4 v[64:67], v[8:15], v[32:39], v[64:67]
	s_setprio 0
	s_barrier
	v_lshl_add_u64 v[0:1], v[232:233], 0, s[8:9]
	s_mov_b32 m0, s65
	v_lshl_add_u64 v[2:3], v[0:1], 0, v[196:197]
	global_load_lds_dwordx4 v[2:3], off
	v_lshl_add_u64 v[0:1], v[0:1], 0, v[192:193]
	s_mov_b32 m0, s66
	s_mov_b64 s[2:3], -1
	global_load_lds_dwordx4 v[0:1], off
	s_and_b64 vcc, exec, s[54:55]
	s_cbranch_vccz .LBB0_2713
	s_waitcnt vmcnt(6)
	s_mov_b64 s[2:3], 0

;     __device__ __forceinline__ void decode(int j, size_t& soff, int& sld, size_t& doff) const {
;     ...
;         else { const int e = j >> 10, r = j & 1023, nt = r >> 4, kt = r & 15, n0 = nt * 32;
;             sld = 2048; soff = (size_t)e * 2048 * 2048 + (size_t)(kt * 128) * 2048 + n0; doff = (size_t)e * 2048 * 2048 + (size_t)n0 * 2048 + kt * 128; }
.LBB0_2715:
	s_barrier
	s_setprio 3
	v_mfma_f32_16x16x128_f8f6f4 v[124:127], v[24:31], v[56:63], v[124:127]
	v_mfma_f32_16x16x128_f8f6f4 v[120:123], v[16:23], v[56:63], v[120:123]
	v_mfma_f32_16x16x128_f8f6f4 v[112:115], v[24:31], v[48:55], v[112:115]
	v_mfma_f32_16x16x128_f8f6f4 v[104:107], v[16:23], v[48:55], v[104:107]
	v_mfma_f32_16x16x128_f8f6f4 v[96:99], v[24:31], v[40:47], v[96:99]
	v_mfma_f32_16x16x128_f8f6f4 v[88:91], v[16:23], v[40:47], v[88:91]
	v_mfma_f32_16x16x128_f8f6f4 v[80:83], v[24:31], v[32:39], v[80:83]
	v_mfma_f32_16x16x128_f8f6f4 v[72:75], v[16:23], v[32:39], v[72:75]
	s_setprio 0
	v_add_u32_e32 v4, 0x18000, v225
	s_barrier
	ds_read_b128 v[8:11], v4
	ds_read_b128 v[12:15], v4 offset:1024
	ds_read_b128 v[0:3], v4 offset:2048
	ds_read_b128 v[4:7], v4 offset:3072
	ds_read_b128 v[40:43], v246 offset:32768
	ds_read_b128 v[44:47], v246 offset:33792
	ds_read_b128 v[32:35], v246 offset:34816
	ds_read_b128 v[36:39], v246 offset:35840
	ds_read_b128 v[24:27], v246 offset:36864
	ds_read_b128 v[28:31], v246 offset:37888
	ds_read_b128 v[16:19], v246 offset:38912
	ds_read_b128 v[20:23], v246 offset:39936
	s_mul_i32 s2, s49, s19
	s_add_i32 s2, s2, s18
	s_cmp_lt_i32 s2, 0x8000
	s_cselect_b64 s[46:47], -1, 0
	s_cmpk_gt_i32 s2, 0x7fff
	s_cbranch_scc1 .LBB0_2704
	s_lshl_b32 s3, s2, 1
	s_ashr_i32 s54, s2, 10
	s_and_b32 s41, s3, 0x7e0
	s_ashr_i32 s55, s54, 31
	s_lshl_b64 s[28:29], s[54:55], 22
	s_lshl_b32 s2, s2, 7
	s_lshl_b32 s3, s41, 11
	s_and_b32 s2, s2, 0x780
	s_or_b32 s3, s28, s3
	s_or_b32 s28, s3, s2
	s_lshl_b32 s2, s2, 13
	s_add_u32 s87, s72, s2
	s_addc_u32 s88, s73, 0
	s_lshl_b64 s[2:3], s[54:55], 24
	s_add_u32 s2, s87, s2
	s_addc_u32 s3, s88, s3
	s_lshl_b32 s41, s41, 2
	s_add_u32 s2, s2, s41
	s_addc_u32 s3, s3, 0
	v_lshl_add_u64 v[48:49], s[2:3], 0, v[208:209]
	v_lshl_add_u64 v[48:49], v[48:49], 0, v[200:201]
	s_add_i32 m0, s83, 0x20000
	s_add_i32 s49, s49, 1
	global_load_lds_dwordx4 v[48:49], off nt
	v_lshl_add_u64 v[48:49], v[48:49], 0, s[34:35]
	s_mov_b32 m0, s84
	s_nop 0
	global_load_lds_dwordx4 v[48:49], off nt
	s_branch .LBB0_2704

.LBB0_2796:
	ds_read_b128 v[0:3], v175
	ds_read_b128 v[4:7], v175 offset:1024
	ds_read_b128 v[8:11], v175 offset:2048
	ds_read_b128 v[12:15], v175 offset:3072
	s_add_u32 s34, s30, 0xfffc0080
	s_addc_u32 s35, s31, -1
	s_cmp_eq_u32 s57, 12
	s_cselect_b32 s37, s15, s35
	s_cselect_b32 s36, s14, s34
	s_cselect_b32 s35, s17, s55
	s_cselect_b32 s34, s16, s13
	v_lshl_add_u64 v[16:17], s[30:31], 0, v[160:161]
	s_add_i32 m0, s29, 0xc000
	ds_read_b128 v[188:191], v176
	ds_read_b128 v[192:195], v176 offset:1024
	ds_read_b128 v[196:199], v176 offset:2048
	ds_read_b128 v[200:203], v176 offset:3072
	ds_read_b128 v[204:207], v176 offset:4096
	ds_read_b128 v[208:211], v176 offset:5120
	ds_read_b128 v[212:215], v176 offset:6144
	ds_read_b128 v[216:219], v176 offset:7168
	global_load_lds_dwordx4 v[16:17], off
	v_lshl_add_u64 v[16:17], s[30:31], 0, v[162:163]
	s_add_i32 m0, s29, 0xe000
	s_nop 0
	global_load_lds_dwordx4 v[16:17], off
	s_waitcnt lgkmcnt(8)
	s_barrier
	s_waitcnt lgkmcnt(0)
	s_setprio 3
	s_waitcnt lgkmcnt(0)
	v_mfma_f32_16x16x128_f8f6f4 v[148:151], v[0:7], v[188:195], v[148:151]
	v_mfma_f32_16x16x128_f8f6f4 v[144:147], v[8:15], v[188:195], v[144:147]
	v_mfma_f32_16x16x128_f8f6f4 v[140:143], v[0:7], v[196:203], v[140:143]
	v_mfma_f32_16x16x128_f8f6f4 v[136:139], v[8:15], v[196:203], v[136:139]
	v_mfma_f32_16x16x128_f8f6f4 v[132:135], v[0:7], v[204:211], v[132:135]
	v_mfma_f32_16x16x128_f8f6f4 v[120:123], v[8:15], v[204:211], v[120:123]
	v_mfma_f32_16x16x128_f8f6f4 v[100:103], v[0:7], v[212:219], v[100:103]
	v_mfma_f32_16x16x128_f8f6f4 v[96:99], v[8:15], v[212:219], v[96:99]
	s_setprio 0
	s_barrier
	s_add_i32 s58, s53, s43
	v_lshl_add_u64 v[166:167], s[34:35], 0, v[156:157]
	s_mov_b32 m0, s58
	ds_read_b128 v[16:19], v178
	ds_read_b128 v[20:23], v178 offset:1024
	ds_read_b128 v[220:223], v178 offset:2048
	ds_read_b128 v[224:227], v178 offset:3072
	global_load_lds_dwordx4 v[166:167], off
	v_lshl_add_u64 v[168:169], s[34:35], 0, v[152:153]
	s_add_i32 m0, s58, 0x2000
	s_nop 0
	global_load_lds_dwordx4 v[168:169], off
	s_barrier
	s_waitcnt lgkmcnt(0)
	s_setprio 3
	s_waitcnt lgkmcnt(0)
	v_mfma_f32_16x16x128_f8f6f4 v[128:131], v[16:23], v[188:195], v[128:131]
	v_mfma_f32_16x16x128_f8f6f4 v[124:127], v[220:227], v[188:195], v[124:127]
	v_mfma_f32_16x16x128_f8f6f4 v[116:119], v[16:23], v[196:203], v[116:119]
	v_mfma_f32_16x16x128_f8f6f4 v[112:115], v[220:227], v[196:203], v[112:115]
	v_mfma_f32_16x16x128_f8f6f4 v[108:111], v[16:23], v[204:211], v[108:111]
	v_mfma_f32_16x16x128_f8f6f4 v[104:107], v[220:227], v[204:211], v[104:107]
	v_mfma_f32_16x16x128_f8f6f4 v[92:95], v[16:23], v[212:219], v[92:95]
	v_mfma_f32_16x16x128_f8f6f4 v[88:91], v[220:227], v[212:219], v[88:91]
	s_setprio 0
	s_mov_b32 m0, s29
	v_lshl_add_u64 v[170:171], s[36:37], 0, v[158:159]
	s_barrier
	ds_read_b128 v[188:191], v176 offset:16384
	ds_read_b128 v[192:195], v176 offset:17408
	ds_read_b128 v[196:199], v176 offset:18432
	ds_read_b128 v[200:203], v176 offset:19456
	ds_read_b128 v[204:207], v176 offset:20480
	ds_read_b128 v[208:211], v176 offset:21504
	ds_read_b128 v[212:215], v176 offset:22528
	ds_read_b128 v[216:219], v176 offset:23552
	global_load_lds_dwordx4 v[170:171], off
	v_lshl_add_u64 v[172:173], s[36:37], 0, v[154:155]
	s_mov_b32 m0, s45
	s_nop 0
	global_load_lds_dwordx4 v[172:173], off
	s_barrier
	s_waitcnt lgkmcnt(0)
	s_setprio 3
	s_waitcnt lgkmcnt(0)
	v_mfma_f32_16x16x128_f8f6f4 v[84:87], v[0:7], v[188:195], v[84:87]
	v_mfma_f32_16x16x128_f8f6f4 v[80:83], v[8:15], v[188:195], v[80:83]
	v_mfma_f32_16x16x128_f8f6f4 v[68:71], v[0:7], v[196:203], v[68:71]
	v_mfma_f32_16x16x128_f8f6f4 v[64:67], v[8:15], v[196:203], v[64:67]
	v_mfma_f32_16x16x128_f8f6f4 v[52:55], v[0:7], v[204:211], v[52:55]
	v_mfma_f32_16x16x128_f8f6f4 v[48:51], v[8:15], v[204:211], v[48:51]
	v_mfma_f32_16x16x128_f8f6f4 v[36:39], v[0:7], v[212:219], v[36:39]
	v_mfma_f32_16x16x128_f8f6f4 v[32:35], v[8:15], v[212:219], v[32:35]
	s_setprio 0
	s_barrier
	s_add_u32 s58, s34, 0x40000
	s_addc_u32 s59, s35, 0
	s_add_i32 s60, s54, s43
	v_lshl_add_u64 v[0:1], s[58:59], 0, v[156:157]
	s_mov_b32 m0, s60
	s_nop 0
	global_load_lds_dwordx4 v[0:1], off
	v_lshl_add_u64 v[0:1], s[58:59], 0, v[152:153]
	s_add_i32 m0, s60, 0x2000
	s_nop 0
	global_load_lds_dwordx4 v[0:1], off
	s_waitcnt vmcnt(6)
	s_barrier
	s_setprio 3
	v_mfma_f32_16x16x128_f8f6f4 v[76:79], v[16:23], v[188:195], v[76:79]
	v_mfma_f32_16x16x128_f8f6f4 v[72:75], v[220:227], v[188:195], v[72:75]
	v_mfma_f32_16x16x128_f8f6f4 v[60:63], v[16:23], v[196:203], v[60:63]
	v_mfma_f32_16x16x128_f8f6f4 v[56:59], v[220:227], v[196:203], v[56:59]
	v_mfma_f32_16x16x128_f8f6f4 v[44:47], v[16:23], v[204:211], v[44:47]
	v_mfma_f32_16x16x128_f8f6f4 v[40:43], v[220:227], v[204:211], v[40:43]
	v_mfma_f32_16x16x128_f8f6f4 v[28:31], v[16:23], v[212:219], v[28:31]
	v_mfma_f32_16x16x128_f8f6f4 v[24:27], v[220:227], v[212:219], v[24:27]
	s_setprio 0
	s_add_i32 s58, 0, 0x18000
	v_add_u32_e32 v12, s58, v174
	s_barrier
	ds_read_b128 v[0:3], v12
	ds_read_b128 v[4:7], v12 offset:1024
	ds_read_b128 v[8:11], v12 offset:2048
	ds_read_b128 v[12:15], v12 offset:3072
	s_add_u32 s36, s36, 0x40000
	s_addc_u32 s37, s37, 0
	s_mov_b32 m0, s46
	v_lshl_add_u64 v[212:213], s[36:37], 0, v[158:159]
	ds_read_b128 v[16:19], v176 offset:32768
	ds_read_b128 v[20:23], v176 offset:33792
	ds_read_b128 v[188:191], v176 offset:34816
	ds_read_b128 v[192:195], v176 offset:35840
	ds_read_b128 v[196:199], v176 offset:36864
	ds_read_b128 v[200:203], v176 offset:37888
	ds_read_b128 v[204:207], v176 offset:38912
	ds_read_b128 v[208:211], v176 offset:39936
	global_load_lds_dwordx4 v[212:213], off
	v_lshl_add_u64 v[212:213], s[36:37], 0, v[154:155]
	s_mov_b32 m0, s47
	s_nop 0
	global_load_lds_dwordx4 v[212:213], off
	s_waitcnt lgkmcnt(8)
	s_barrier
;     __device__ __forceinline__ void operator()(const f32x4 (&acc)[2][2][4][2], const Unit& u, int wr, int wc, int fr, int fq, const Pre& pr) const {
;         const int c0 = 256 * u.pn + 32 * wc + 8 * fq; const float* bp = bdn + (size_t)u.aux * DM + c0;
;         const f32x4 b00 = *(const f32x4*)bp, b01 = *(const f32x4*)(bp + 4), b10 = *(const f32x4*)(bp + 128), b11 = *(const f32x4*)(bp + 132); const float (&gwv)[8] = pr.gwv;
	s_waitcnt lgkmcnt(0)
	s_setprio 3
	s_waitcnt lgkmcnt(0)
	v_mfma_f32_16x16x128_f8f6f4 v[148:151], v[0:7], v[16:23], v[148:151]
	v_mfma_f32_16x16x128_f8f6f4 v[144:147], v[8:15], v[16:23], v[144:147]
	v_mfma_f32_16x16x128_f8f6f4 v[140:143], v[0:7], v[188:195], v[140:143]
	v_mfma_f32_16x16x128_f8f6f4 v[136:139], v[8:15], v[188:195], v[136:139]
	v_mfma_f32_16x16x128_f8f6f4 v[132:135], v[0:7], v[196:203], v[132:135]
	v_mfma_f32_16x16x128_f8f6f4 v[120:123], v[8:15], v[196:203], v[120:123]
	v_mfma_f32_16x16x128_f8f6f4 v[100:103], v[0:7], v[204:211], v[100:103]
	v_mfma_f32_16x16x128_f8f6f4 v[96:99], v[8:15], v[204:211], v[96:99]
	s_setprio 0
	s_barrier
	s_add_i32 s36, 0, 0x1c000
	s_add_i32 s37, s58, s43
	v_add_u32_e32 v165, s36, v174
	v_lshl_add_u64 v[166:167], v[166:167], 0, s[4:5]
	s_mov_b32 m0, s37
	ds_read_b128 v[212:215], v165
	ds_read_b128 v[216:219], v165 offset:1024
	ds_read_b128 v[220:223], v165 offset:2048
	ds_read_b128 v[224:227], v165 offset:3072
	global_load_lds_dwordx4 v[166:167], off
	v_lshl_add_u64 v[166:167], v[168:169], 0, s[4:5]
	s_add_i32 m0, s37, 0x2000
	s_nop 0
	global_load_lds_dwordx4 v[166:167], off
	s_barrier
	s_waitcnt lgkmcnt(0)
	s_setprio 3
	s_waitcnt lgkmcnt(0)
	v_mfma_f32_16x16x128_f8f6f4 v[128:131], v[212:219], v[16:23], v[128:131]
	v_mfma_f32_16x16x128_f8f6f4 v[124:127], v[220:227], v[16:23], v[124:127]
	v_mfma_f32_16x16x128_f8f6f4 v[116:119], v[212:219], v[188:195], v[116:119]
	v_mfma_f32_16x16x128_f8f6f4 v[112:115], v[220:227], v[188:195], v[112:115]
	v_mfma_f32_16x16x128_f8f6f4 v[108:111], v[212:219], v[196:203], v[108:111]
	v_mfma_f32_16x16x128_f8f6f4 v[104:107], v[220:227], v[196:203], v[104:107]
	v_mfma_f32_16x16x128_f8f6f4 v[92:95], v[212:219], v[204:211], v[92:95]
	v_mfma_f32_16x16x128_f8f6f4 v[88:91], v[220:227], v[204:211], v[88:91]
	s_setprio 0
	s_mov_b32 m0, s50
	v_lshl_add_u64 v[166:167], v[170:171], 0, s[4:5]
	s_barrier
	ds_read_b128 v[16:19], v176 offset:49152
	ds_read_b128 v[20:23], v176 offset:50176
	ds_read_b128 v[188:191], v176 offset:51200
	ds_read_b128 v[192:195], v176 offset:52224
	ds_read_b128 v[196:199], v176 offset:53248
	ds_read_b128 v[200:203], v176 offset:54272
	ds_read_b128 v[204:207], v176 offset:55296
	ds_read_b128 v[208:211], v176 offset:56320
	global_load_lds_dwordx4 v[166:167], off
	v_lshl_add_u64 v[166:167], v[172:173], 0, s[4:5]
	s_mov_b32 m0, s51
	s_nop 0
	global_load_lds_dwordx4 v[166:167], off
	s_barrier
	s_waitcnt lgkmcnt(0)
	s_setprio 3
	s_waitcnt lgkmcnt(0)
	v_mfma_f32_16x16x128_f8f6f4 v[84:87], v[0:7], v[16:23], v[84:87]
	v_mfma_f32_16x16x128_f8f6f4 v[80:83], v[8:15], v[16:23], v[80:83]
	v_mfma_f32_16x16x128_f8f6f4 v[68:71], v[0:7], v[188:195], v[68:71]
	v_mfma_f32_16x16x128_f8f6f4 v[64:67], v[8:15], v[188:195], v[64:67]
	v_mfma_f32_16x16x128_f8f6f4 v[52:55], v[0:7], v[196:203], v[52:55]
	v_mfma_f32_16x16x128_f8f6f4 v[48:51], v[8:15], v[196:203], v[48:51]
	v_mfma_f32_16x16x128_f8f6f4 v[36:39], v[0:7], v[204:211], v[36:39]
	v_mfma_f32_16x16x128_f8f6f4 v[32:35], v[8:15], v[204:211], v[32:35]
	s_setprio 0
	s_barrier
	s_add_u32 s34, s34, 0x40080
	s_addc_u32 s35, s35, 0
	s_add_i32 s36, s36, s43
	v_lshl_add_u64 v[0:1], s[34:35], 0, v[156:157]
	s_mov_b32 m0, s36
	s_nop 0
	global_load_lds_dwordx4 v[0:1], off
	v_lshl_add_u64 v[0:1], s[34:35], 0, v[152:153]
	s_add_i32 m0, s36, 0x2000
	s_nop 0
	global_load_lds_dwordx4 v[0:1], off
	s_waitcnt vmcnt(6)
	s_barrier
	s_setprio 3
	v_mfma_f32_16x16x128_f8f6f4 v[76:79], v[212:219], v[16:23], v[76:79]
	v_mfma_f32_16x16x128_f8f6f4 v[72:75], v[220:227], v[16:23], v[72:75]
	v_mfma_f32_16x16x128_f8f6f4 v[60:63], v[212:219], v[188:195], v[60:63]
	v_mfma_f32_16x16x128_f8f6f4 v[56:59], v[220:227], v[188:195], v[56:59]
	v_mfma_f32_16x16x128_f8f6f4 v[44:47], v[212:219], v[196:203], v[44:47]
	v_mfma_f32_16x16x128_f8f6f4 v[40:43], v[220:227], v[196:203], v[40:43]
	v_mfma_f32_16x16x128_f8f6f4 v[28:31], v[212:219], v[204:211], v[28:31]
	v_mfma_f32_16x16x128_f8f6f4 v[24:27], v[220:227], v[204:211], v[24:27]
	s_setprio 0
	s_add_i32 s57, s57, 2
	s_add_u32 s30, s30, 0x100
	s_addc_u32 s31, s31, 0
	s_add_u32 s13, s13, 0x100
	s_addc_u32 s55, s55, 0
	s_cmp_gt_u32 s57, 13
	s_barrier
	s_cbranch_scc0 .LBB0_2796
	s_nop 15
 s_nop 7
	v_mbcnt_lo_u32_b32 v18, -1, 0
	v_mbcnt_hi_u32_b32 v18, -1, v18
	s_lshl_b32 s13, s28, 8
	v_ashrrev_i32_e32 v0, 1, v18
	v_and_b32_e32 v0, -8, v0
	s_or_b32 s13, s13, s49
	v_ashrrev_i32_e32 v165, 31, v164
	v_add_u32_e32 v16, s13, v0
	v_lshlrev_b64 v[0:1], 13, v[164:165]
	v_lshl_add_u64 v[0:1], s[74:75], 0, v[0:1]
	v_ashrrev_i32_e32 v17, 31, v16
	v_lshl_add_u64 v[0:1], v[16:17], 2, v[0:1]
	global_load_dwordx4 v[12:15], v[0:1], off
	global_load_dwordx4 v[8:11], v[0:1], off offset:16
	global_load_dwordx4 v[4:7], v[0:1], off offset:512
	s_nop 0
	global_load_dwordx4 v[0:3], v[0:1], off offset:528
	s_waitcnt vmcnt(0)
;     __device__ __forceinline__ void operator()(const f32x4 (&acc)[2][2][4][2], const Unit& u, int wr, int wc, int fr, int fq, const Pre& pr) const {
;     ...
; #pragma unroll
;         for (int ai = 0; ai < 2; ++ai)
; #pragma unroll
;             for (int m = 0; m < 4; ++m) {
;                 const int row = u.pm * 256 + ai * 128 + wr * 64 + m * 16 + fr; const float gw = gwv[ai * 4 + m] * YS_SCALE;
;                 constexpr float iw = 1.0f / W8_SCALE;
;                 const f32x4 o0 = (acc[ai][0][m][0] * iw + b00) * gw, o1 = (acc[ai][0][m][1] * iw + b01) * gw, o2 = (acc[ai][1][m][0] * iw + b10) * gw, o3 = (acc[ai][1][m][1] * iw + b11) * gw;
;                 *(u32x2*)(ys + (size_t)row * DM + c0) = pack_fp8x8(o0[0], o0[1], o0[2], o0[3], o1[0], o1[1], o1[2], o1[3]);
;                 *(u32x2*)(ys + (size_t)row * DM + c0 + 128) = pack_fp8x8(o2[0], o2[1], o2[2], o2[3], o3[0], o3[1], o3[2], o3[3]);
	v_mul_f32_e32 v20, 0x41800000, v187
	v_mov_b32_e32 v22, 0
	v_mov_b32_e32 v23, 0
	v_mov_b32_e32 v164, 0
	v_mov_b32_e32 v165, 0
	v_mul_f32_e32 v166, 0x41800000, v186
	v_mov_b32_e32 v168, 0
	v_mov_b32_e32 v169, 0
	v_mov_b32_e32 v170, 0
	v_mov_b32_e32 v171, 0
	v_and_or_b32 v18, v18, 15, s48
	v_add_u32_e32 v18, s11, v18
	v_ashrrev_i32_e32 v19, 31, v18
	v_add_u32_e32 v186, 16, v18
	v_lshlrev_b64 v[190:191], 11, v[18:19]
	v_ashrrev_i32_e32 v187, 31, v186
	v_lshl_add_u64 v[190:191], s[2:3], 0, v[190:191]
	v_lshlrev_b64 v[186:187], 11, v[186:187]
	v_mul_f32_e32 v172, 0x41800000, v185
	v_lshl_add_u64 v[190:191], v[190:191], 0, v[16:17]
	v_lshl_add_u64 v[186:187], s[2:3], 0, v[186:187]
	v_lshl_add_u64 v[186:187], v[186:187], 0, v[16:17]
	v_add_u32_e32 v188, 32, v18
	v_ashrrev_i32_e32 v189, 31, v188
	s_and_b64 vcc, exec, s[8:9]
	s_mov_b32 s34, s12
	s_mov_b32 s28, s10
	s_mov_b64 s[36:37], s[16:17]
	s_mov_b64 s[30:31], s[14:15]
	v_pk_fma_f32 v[148:149], v[148:149], s[6:7], v[12:13] op_sel_hi:[1,0,1]
	v_pk_fma_f32 v[144:145], v[144:145], s[6:7], v[8:9] op_sel_hi:[1,0,1]
	v_pk_fma_f32 v[150:151], v[150:151], s[6:7], v[14:15] op_sel_hi:[1,0,1]
	v_pk_fma_f32 v[146:147], v[146:147], s[6:7], v[10:11] op_sel_hi:[1,0,1]
	v_pk_fma_f32 v[130:131], v[130:131], s[6:7], v[6:7] op_sel_hi:[1,0,1]
	v_pk_fma_f32 v[128:129], v[128:129], s[6:7], v[4:5] op_sel_hi:[1,0,1]
	v_pk_fma_f32 v[126:127], v[126:127], s[6:7], v[2:3] op_sel_hi:[1,0,1]
	v_pk_fma_f32 v[124:125], v[124:125], s[6:7], v[0:1] op_sel_hi:[1,0,1]
	v_pk_mul_f32 v[148:149], v[20:21], v[148:149] op_sel_hi:[0,1]
	v_pk_mul_f32 v[144:145], v[20:21], v[144:145] op_sel_hi:[0,1]
	v_pk_fma_f32 v[140:141], v[140:141], s[6:7], v[12:13] op_sel_hi:[1,0,1]
	v_pk_fma_f32 v[136:137], v[136:137], s[6:7], v[8:9] op_sel_hi:[1,0,1]
	v_pk_mul_f32 v[150:151], v[20:21], v[150:151] op_sel_hi:[0,1]
	v_pk_mul_f32 v[146:147], v[20:21], v[146:147] op_sel_hi:[0,1]
	v_pk_mul_f32 v[130:131], v[20:21], v[130:131] op_sel_hi:[0,1]
	v_pk_mul_f32 v[128:129], v[20:21], v[128:129] op_sel_hi:[0,1]
	v_pk_mul_f32 v[126:127], v[20:21], v[126:127] op_sel_hi:[0,1]
	v_pk_mul_f32 v[20:21], v[20:21], v[124:125] op_sel_hi:[0,1]
	v_cvt_pk_fp8_f32 v22, v148, v149
	v_cvt_pk_fp8_f32 v23, v144, v145
	v_pk_fma_f32 v[116:117], v[116:117], s[6:7], v[4:5] op_sel_hi:[1,0,1]
	v_pk_fma_f32 v[112:113], v[112:113], s[6:7], v[0:1] op_sel_hi:[1,0,1]
	v_pk_mul_f32 v[140:141], v[166:167], v[140:141] op_sel_hi:[0,1]
	v_pk_mul_f32 v[136:137], v[166:167], v[136:137] op_sel_hi:[0,1]
	v_cvt_pk_fp8_f32 v164, v128, v129
	v_cvt_pk_fp8_f32 v165, v20, v21
	v_pk_mul_f32 v[116:117], v[166:167], v[116:117] op_sel_hi:[0,1]
	v_pk_mul_f32 v[112:113], v[166:167], v[112:113] op_sel_hi:[0,1]
	v_cvt_pk_fp8_f32 v168, v140, v141
	v_cvt_pk_fp8_f32 v169, v136, v137
	v_cvt_pk_fp8_f32 v170, v116, v117
	v_cvt_pk_fp8_f32 v171, v112, v113
	v_pk_fma_f32 v[142:143], v[142:143], s[6:7], v[14:15] op_sel_hi:[1,0,1]
	v_pk_fma_f32 v[138:139], v[138:139], s[6:7], v[10:11] op_sel_hi:[1,0,1]
	v_cvt_pk_fp8_f32 v22, v150, v151 op_sel:[0,0,1]
	v_cvt_pk_fp8_f32 v23, v146, v147 op_sel:[0,0,1]
	v_pk_fma_f32 v[118:119], v[118:119], s[6:7], v[6:7] op_sel_hi:[1,0,1]
	v_pk_fma_f32 v[114:115], v[114:115], s[6:7], v[2:3] op_sel_hi:[1,0,1]
	v_pk_mul_f32 v[124:125], v[166:167], v[142:143] op_sel_hi:[0,1]
	v_pk_mul_f32 v[138:139], v[166:167], v[138:139] op_sel_hi:[0,1]
	v_cvt_pk_fp8_f32 v164, v130, v131 op_sel:[0,0,1]
	v_cvt_pk_fp8_f32 v165, v126, v127 op_sel:[0,0,1]
	v_pk_mul_f32 v[118:119], v[166:167], v[118:119] op_sel_hi:[0,1]
	v_pk_mul_f32 v[114:115], v[166:167], v[114:115] op_sel_hi:[0,1]
	v_cvt_pk_fp8_f32 v168, v124, v125 op_sel:[0,0,1]
	v_cvt_pk_fp8_f32 v169, v138, v139 op_sel:[0,0,1]
	v_pk_fma_f32 v[120:121], v[120:121], s[6:7], v[8:9] op_sel_hi:[1,0,1]
	v_cvt_pk_fp8_f32 v170, v118, v119 op_sel:[0,0,1]
	v_cvt_pk_fp8_f32 v171, v114, v115 op_sel:[0,0,1]
	global_store_dwordx2 v[190:191], v[22:23], off
	global_store_dwordx2 v[190:191], v[164:165], off offset:128
	global_store_dwordx2 v[186:187], v[168:169], off
	global_store_dwordx2 v[186:187], v[170:171], off offset:128
	v_pk_mul_f32 v[22:23], v[172:173], v[120:121] op_sel_hi:[0,1]
	v_mov_b32_e32 v113, 0
	v_cvt_pk_fp8_f32 v113, v22, v23
	v_pk_fma_f32 v[132:133], v[132:133], s[6:7], v[12:13] op_sel_hi:[1,0,1]
	v_pk_fma_f32 v[122:123], v[122:123], s[6:7], v[10:11] op_sel_hi:[1,0,1]
	v_pk_mul_f32 v[132:133], v[172:173], v[132:133] op_sel_hi:[0,1]
	v_pk_mul_f32 v[20:21], v[172:173], v[122:123] op_sel_hi:[0,1]
	v_pk_fma_f32 v[108:109], v[108:109], s[6:7], v[4:5] op_sel_hi:[1,0,1]
	v_pk_fma_f32 v[104:105], v[104:105], s[6:7], v[0:1] op_sel_hi:[1,0,1]
	v_mov_b32_e32 v112, 0
	v_pk_mul_f32 v[108:109], v[172:173], v[108:109] op_sel_hi:[0,1]
	v_cvt_pk_fp8_f32 v112, v132, v133
	v_pk_mul_f32 v[104:105], v[172:173], v[104:105] op_sel_hi:[0,1]
	v_cvt_pk_fp8_f32 v113, v20, v21 op_sel:[0,0,1]
	v_mov_b32_e32 v20, 0
	v_mov_b32_e32 v21, 0
	v_cvt_pk_fp8_f32 v20, v108, v109
	v_cvt_pk_fp8_f32 v21, v104, v105
	v_pk_fma_f32 v[134:135], v[134:135], s[6:7], v[14:15] op_sel_hi:[1,0,1]
	v_pk_fma_f32 v[110:111], v[110:111], s[6:7], v[6:7] op_sel_hi:[1,0,1]
	v_pk_mul_f32 v[134:135], v[172:173], v[134:135] op_sel_hi:[0,1]
	v_pk_fma_f32 v[106:107], v[106:107], s[6:7], v[2:3] op_sel_hi:[1,0,1]
	v_pk_mul_f32 v[110:111], v[172:173], v[110:111] op_sel_hi:[0,1]
	v_pk_mul_f32 v[22:23], v[172:173], v[106:107] op_sel_hi:[0,1]
	v_cvt_pk_fp8_f32 v112, v134, v135 op_sel:[0,0,1]
	v_lshlrev_b64 v[104:105], 11, v[188:189]
	v_cvt_pk_fp8_f32 v20, v110, v111 op_sel:[0,0,1]
	v_cvt_pk_fp8_f32 v21, v22, v23 op_sel:[0,0,1]
	v_lshl_add_u64 v[22:23], s[2:3], 0, v[104:105]
	v_lshl_add_u64 v[22:23], v[22:23], 0, v[16:17]
;     __device__ __forceinline__ void operator()(const f32x4 (&acc)[2][2][4][2], const Unit& u, int wr, int wc, int fr, int fq, const Pre& pr) const {
;     ...
; #pragma unroll
;         for (int ai = 0; ai < 2; ++ai)
; #pragma unroll
;             for (int m = 0; m < 4; ++m) {
;                 const int row = u.pm * 256 + ai * 128 + wr * 64 + m * 16 + fr; const float gw = gwv[ai * 4 + m] * YS_SCALE;
;                 constexpr float iw = 1.0f / W8_SCALE;
;                 const f32x4 o0 = (acc[ai][0][m][0] * iw + b00) * gw, o1 = (acc[ai][0][m][1] * iw + b01) * gw, o2 = (acc[ai][1][m][0] * iw + b10) * gw, o3 = (acc[ai][1][m][1] * iw + b11) * gw;
;                 *(u32x2*)(ys + (size_t)row * DM + c0) = pack_fp8x8(o0[0], o0[1], o0[2], o0[3], o1[0], o1[1], o1[2], o1[3]);
;                 *(u32x2*)(ys + (size_t)row * DM + c0 + 128) = pack_fp8x8(o2[0], o2[1], o2[2], o2[3], o3[0], o3[1], o3[2], o3[3]);
	global_store_dwordx2 v[22:23], v[112:113], off
	global_store_dwordx2 v[22:23], v[20:21], off offset:128
	v_mul_f32_e32 v22, 0x41800000, v184
	v_pk_fma_f32 v[100:101], v[100:101], s[6:7], v[12:13] op_sel_hi:[1,0,1]
	v_pk_fma_f32 v[96:97], v[96:97], s[6:7], v[8:9] op_sel_hi:[1,0,1]
	v_pk_fma_f32 v[102:103], v[102:103], s[6:7], v[14:15] op_sel_hi:[1,0,1]
	v_pk_mul_f32 v[100:101], v[22:23], v[100:101] op_sel_hi:[0,1]
	v_pk_fma_f32 v[98:99], v[98:99], s[6:7], v[10:11] op_sel_hi:[1,0,1]
	v_pk_mul_f32 v[96:97], v[22:23], v[96:97] op_sel_hi:[0,1]
	v_pk_fma_f32 v[94:95], v[94:95], s[6:7], v[6:7] op_sel_hi:[1,0,1]
	v_pk_fma_f32 v[92:93], v[92:93], s[6:7], v[4:5] op_sel_hi:[1,0,1]
	v_pk_fma_f32 v[90:91], v[90:91], s[6:7], v[2:3] op_sel_hi:[1,0,1]
	v_pk_fma_f32 v[88:89], v[88:89], s[6:7], v[0:1] op_sel_hi:[1,0,1]
	v_mov_b32_e32 v104, 0
	v_mov_b32_e32 v105, 0
	v_pk_mul_f32 v[102:103], v[22:23], v[102:103] op_sel_hi:[0,1]
	v_pk_mul_f32 v[98:99], v[22:23], v[98:99] op_sel_hi:[0,1]
	v_pk_mul_f32 v[94:95], v[22:23], v[94:95] op_sel_hi:[0,1]
	v_pk_mul_f32 v[92:93], v[22:23], v[92:93] op_sel_hi:[0,1]
	v_cvt_pk_fp8_f32 v104, v100, v101
	v_cvt_pk_fp8_f32 v105, v96, v97
	v_pk_mul_f32 v[90:91], v[22:23], v[90:91] op_sel_hi:[0,1]
	v_pk_mul_f32 v[22:23], v[22:23], v[88:89] op_sel_hi:[0,1]
	v_mov_b32_e32 v88, 0
	v_mov_b32_e32 v89, 0
	v_cvt_pk_fp8_f32 v88, v92, v93
	v_cvt_pk_fp8_f32 v89, v22, v23
	v_add_u32_e32 v20, 48, v18
	v_cvt_pk_fp8_f32 v104, v102, v103 op_sel:[0,0,1]
	v_cvt_pk_fp8_f32 v105, v98, v99 op_sel:[0,0,1]
	v_ashrrev_i32_e32 v21, 31, v20
	v_lshlrev_b64 v[20:21], 11, v[20:21]
	v_cvt_pk_fp8_f32 v88, v94, v95 op_sel:[0,0,1]
	v_cvt_pk_fp8_f32 v89, v90, v91 op_sel:[0,0,1]
	v_lshl_add_u64 v[20:21], s[2:3], 0, v[20:21]
	v_lshl_add_u64 v[20:21], v[20:21], 0, v[16:17]
	v_mul_f32_e32 v22, 0x41800000, v183
	v_pk_fma_f32 v[84:85], v[84:85], s[6:7], v[12:13] op_sel_hi:[1,0,1]
	v_pk_fma_f32 v[80:81], v[80:81], s[6:7], v[8:9] op_sel_hi:[1,0,1]
	global_store_dwordx2 v[20:21], v[104:105], off
	global_store_dwordx2 v[20:21], v[88:89], off offset:128
	v_pk_fma_f32 v[86:87], v[86:87], s[6:7], v[14:15] op_sel_hi:[1,0,1]
	v_pk_mul_f32 v[84:85], v[22:23], v[84:85] op_sel_hi:[0,1]
	v_pk_fma_f32 v[82:83], v[82:83], s[6:7], v[10:11] op_sel_hi:[1,0,1]
	v_pk_mul_f32 v[80:81], v[22:23], v[80:81] op_sel_hi:[0,1]
	v_pk_fma_f32 v[78:79], v[78:79], s[6:7], v[6:7] op_sel_hi:[1,0,1]
	v_pk_fma_f32 v[76:77], v[76:77], s[6:7], v[4:5] op_sel_hi:[1,0,1]
	v_pk_fma_f32 v[74:75], v[74:75], s[6:7], v[2:3] op_sel_hi:[1,0,1]
	v_pk_fma_f32 v[72:73], v[72:73], s[6:7], v[0:1] op_sel_hi:[1,0,1]
	v_mov_b32_e32 v88, 0
	v_mov_b32_e32 v89, 0
	v_pk_mul_f32 v[86:87], v[22:23], v[86:87] op_sel_hi:[0,1]
	v_pk_mul_f32 v[82:83], v[22:23], v[82:83] op_sel_hi:[0,1]
	v_pk_mul_f32 v[78:79], v[22:23], v[78:79] op_sel_hi:[0,1]
	v_pk_mul_f32 v[76:77], v[22:23], v[76:77] op_sel_hi:[0,1]
	v_cvt_pk_fp8_f32 v88, v84, v85
	v_cvt_pk_fp8_f32 v89, v80, v81
	v_pk_mul_f32 v[74:75], v[22:23], v[74:75] op_sel_hi:[0,1]
	v_pk_mul_f32 v[22:23], v[22:23], v[72:73] op_sel_hi:[0,1]
	v_mov_b32_e32 v72, 0
	v_mov_b32_e32 v73, 0
	v_cvt_pk_fp8_f32 v72, v76, v77
	v_cvt_pk_fp8_f32 v73, v22, v23
	v_add_u32_e32 v20, 0x80, v18
	v_cvt_pk_fp8_f32 v88, v86, v87 op_sel:[0,0,1]
	v_cvt_pk_fp8_f32 v89, v82, v83 op_sel:[0,0,1]
	v_ashrrev_i32_e32 v21, 31, v20
	v_lshlrev_b64 v[20:21], 11, v[20:21]
	v_cvt_pk_fp8_f32 v72, v78, v79 op_sel:[0,0,1]
	v_cvt_pk_fp8_f32 v73, v74, v75 op_sel:[0,0,1]
	v_lshl_add_u64 v[20:21], s[2:3], 0, v[20:21]
	v_lshl_add_u64 v[20:21], v[20:21], 0, v[16:17]
	v_mul_f32_e32 v22, 0x41800000, v182
	v_pk_fma_f32 v[68:69], v[68:69], s[6:7], v[12:13] op_sel_hi:[1,0,1]
	v_pk_fma_f32 v[64:65], v[64:65], s[6:7], v[8:9] op_sel_hi:[1,0,1]
	global_store_dwordx2 v[20:21], v[88:89], off
	global_store_dwordx2 v[20:21], v[72:73], off offset:128
	v_pk_fma_f32 v[70:71], v[70:71], s[6:7], v[14:15] op_sel_hi:[1,0,1]
	v_pk_mul_f32 v[68:69], v[22:23], v[68:69] op_sel_hi:[0,1]
	v_pk_fma_f32 v[66:67], v[66:67], s[6:7], v[10:11] op_sel_hi:[1,0,1]
	v_pk_mul_f32 v[64:65], v[22:23], v[64:65] op_sel_hi:[0,1]
	v_pk_fma_f32 v[62:63], v[62:63], s[6:7], v[6:7] op_sel_hi:[1,0,1]
	v_pk_fma_f32 v[60:61], v[60:61], s[6:7], v[4:5] op_sel_hi:[1,0,1]
	v_pk_fma_f32 v[58:59], v[58:59], s[6:7], v[2:3] op_sel_hi:[1,0,1]
	v_pk_fma_f32 v[56:57], v[56:57], s[6:7], v[0:1] op_sel_hi:[1,0,1]
	v_mov_b32_e32 v72, 0
	v_mov_b32_e32 v73, 0
	v_pk_mul_f32 v[70:71], v[22:23], v[70:71] op_sel_hi:[0,1]
	v_pk_mul_f32 v[66:67], v[22:23], v[66:67] op_sel_hi:[0,1]
;     __device__ __forceinline__ void operator()(const f32x4 (&acc)[2][2][4][2], const Unit& u, int wr, int wc, int fr, int fq, const Pre& pr) const {
;     ...
; #pragma unroll
;         for (int ai = 0; ai < 2; ++ai)
; #pragma unroll
;             for (int m = 0; m < 4; ++m) {
;                 const int row = u.pm * 256 + ai * 128 + wr * 64 + m * 16 + fr; const float gw = gwv[ai * 4 + m] * YS_SCALE;
;                 constexpr float iw = 1.0f / W8_SCALE;
;                 const f32x4 o0 = (acc[ai][0][m][0] * iw + b00) * gw, o1 = (acc[ai][0][m][1] * iw + b01) * gw, o2 = (acc[ai][1][m][0] * iw + b10) * gw, o3 = (acc[ai][1][m][1] * iw + b11) * gw;
;                 *(u32x2*)(ys + (size_t)row * DM + c0) = pack_fp8x8(o0[0], o0[1], o0[2], o0[3], o1[0], o1[1], o1[2], o1[3]);
;                 *(u32x2*)(ys + (size_t)row * DM + c0 + 128) = pack_fp8x8(o2[0], o2[1], o2[2], o2[3], o3[0], o3[1], o3[2], o3[3]);
	v_pk_mul_f32 v[62:63], v[22:23], v[62:63] op_sel_hi:[0,1]
	v_pk_mul_f32 v[60:61], v[22:23], v[60:61] op_sel_hi:[0,1]
	v_cvt_pk_fp8_f32 v72, v68, v69
	v_cvt_pk_fp8_f32 v73, v64, v65
	v_pk_mul_f32 v[58:59], v[22:23], v[58:59] op_sel_hi:[0,1]
	v_pk_mul_f32 v[22:23], v[22:23], v[56:57] op_sel_hi:[0,1]
	v_mov_b32_e32 v56, 0
	v_mov_b32_e32 v57, 0
	v_cvt_pk_fp8_f32 v56, v60, v61
	v_cvt_pk_fp8_f32 v57, v22, v23
	v_add_u32_e32 v20, 0x90, v18
	v_cvt_pk_fp8_f32 v72, v70, v71 op_sel:[0,0,1]
	v_cvt_pk_fp8_f32 v73, v66, v67 op_sel:[0,0,1]
	v_ashrrev_i32_e32 v21, 31, v20
	v_lshlrev_b64 v[20:21], 11, v[20:21]
	v_cvt_pk_fp8_f32 v56, v62, v63 op_sel:[0,0,1]
	v_cvt_pk_fp8_f32 v57, v58, v59 op_sel:[0,0,1]
	v_lshl_add_u64 v[20:21], s[2:3], 0, v[20:21]
	v_lshl_add_u64 v[20:21], v[20:21], 0, v[16:17]
	v_mul_f32_e32 v22, 0x41800000, v181
	v_pk_fma_f32 v[52:53], v[52:53], s[6:7], v[12:13] op_sel_hi:[1,0,1]
	v_pk_fma_f32 v[48:49], v[48:49], s[6:7], v[8:9] op_sel_hi:[1,0,1]
	global_store_dwordx2 v[20:21], v[72:73], off
	global_store_dwordx2 v[20:21], v[56:57], off offset:128
	v_pk_fma_f32 v[54:55], v[54:55], s[6:7], v[14:15] op_sel_hi:[1,0,1]
	v_pk_mul_f32 v[52:53], v[22:23], v[52:53] op_sel_hi:[0,1]
	v_pk_fma_f32 v[50:51], v[50:51], s[6:7], v[10:11] op_sel_hi:[1,0,1]
	v_pk_mul_f32 v[48:49], v[22:23], v[48:49] op_sel_hi:[0,1]
	v_pk_fma_f32 v[46:47], v[46:47], s[6:7], v[6:7] op_sel_hi:[1,0,1]
	v_pk_fma_f32 v[44:45], v[44:45], s[6:7], v[4:5] op_sel_hi:[1,0,1]
	v_pk_fma_f32 v[42:43], v[42:43], s[6:7], v[2:3] op_sel_hi:[1,0,1]
	v_pk_fma_f32 v[40:41], v[40:41], s[6:7], v[0:1] op_sel_hi:[1,0,1]
	v_mov_b32_e32 v56, 0
	v_mov_b32_e32 v57, 0
	v_pk_mul_f32 v[54:55], v[22:23], v[54:55] op_sel_hi:[0,1]
	v_pk_mul_f32 v[50:51], v[22:23], v[50:51] op_sel_hi:[0,1]
	v_pk_mul_f32 v[46:47], v[22:23], v[46:47] op_sel_hi:[0,1]
	v_pk_mul_f32 v[44:45], v[22:23], v[44:45] op_sel_hi:[0,1]
	v_cvt_pk_fp8_f32 v56, v52, v53
	v_cvt_pk_fp8_f32 v57, v48, v49
	v_pk_mul_f32 v[42:43], v[22:23], v[42:43] op_sel_hi:[0,1]
	v_pk_mul_f32 v[22:23], v[22:23], v[40:41] op_sel_hi:[0,1]
	v_mov_b32_e32 v40, 0
	v_mov_b32_e32 v41, 0
	v_cvt_pk_fp8_f32 v40, v44, v45
	v_cvt_pk_fp8_f32 v41, v22, v23
	v_add_u32_e32 v20, 0xa0, v18
	v_cvt_pk_fp8_f32 v56, v54, v55 op_sel:[0,0,1]
	v_cvt_pk_fp8_f32 v57, v50, v51 op_sel:[0,0,1]
	v_ashrrev_i32_e32 v21, 31, v20
	v_lshlrev_b64 v[20:21], 11, v[20:21]
	v_cvt_pk_fp8_f32 v40, v46, v47 op_sel:[0,0,1]
	v_cvt_pk_fp8_f32 v41, v42, v43 op_sel:[0,0,1]
	v_lshl_add_u64 v[20:21], s[2:3], 0, v[20:21]
	v_lshl_add_u64 v[20:21], v[20:21], 0, v[16:17]
	global_store_dwordx2 v[20:21], v[56:57], off
	global_store_dwordx2 v[20:21], v[40:41], off offset:128
	v_mul_f32_e32 v20, 0x41800000, v180
	v_pk_fma_f32 v[12:13], v[36:37], s[6:7], v[12:13] op_sel_hi:[1,0,1]
	v_pk_fma_f32 v[8:9], v[32:33], s[6:7], v[8:9] op_sel_hi:[1,0,1]
	v_pk_mul_f32 v[12:13], v[20:21], v[12:13] op_sel_hi:[0,1]
	v_pk_mul_f32 v[8:9], v[20:21], v[8:9] op_sel_hi:[0,1]
	v_pk_fma_f32 v[4:5], v[28:29], s[6:7], v[4:5] op_sel_hi:[1,0,1]
	v_pk_fma_f32 v[0:1], v[24:25], s[6:7], v[0:1] op_sel_hi:[1,0,1]
	v_mov_b32_e32 v22, 0
	v_mov_b32_e32 v23, 0
	v_pk_mul_f32 v[4:5], v[20:21], v[4:5] op_sel_hi:[0,1]
	v_cvt_pk_fp8_f32 v22, v12, v13
	v_cvt_pk_fp8_f32 v23, v8, v9
	v_pk_mul_f32 v[0:1], v[20:21], v[0:1] op_sel_hi:[0,1]
	v_mov_b32_e32 v8, 0
	v_mov_b32_e32 v9, 0
	v_cvt_pk_fp8_f32 v8, v4, v5
	v_cvt_pk_fp8_f32 v9, v0, v1
	v_pk_fma_f32 v[14:15], v[38:39], s[6:7], v[14:15] op_sel_hi:[1,0,1]
	v_pk_fma_f32 v[10:11], v[34:35], s[6:7], v[10:11] op_sel_hi:[1,0,1]
	v_add_u32_e32 v18, 0xb0, v18
	v_pk_mul_f32 v[14:15], v[20:21], v[14:15] op_sel_hi:[0,1]
	v_pk_mul_f32 v[10:11], v[20:21], v[10:11] op_sel_hi:[0,1]
	v_pk_fma_f32 v[6:7], v[30:31], s[6:7], v[6:7] op_sel_hi:[1,0,1]
	v_pk_fma_f32 v[2:3], v[26:27], s[6:7], v[2:3] op_sel_hi:[1,0,1]
	v_pk_mul_f32 v[6:7], v[20:21], v[6:7] op_sel_hi:[0,1]
	v_pk_mul_f32 v[2:3], v[20:21], v[2:3] op_sel_hi:[0,1]
	v_cvt_pk_fp8_f32 v22, v14, v15 op_sel:[0,0,1]
	v_cvt_pk_fp8_f32 v23, v10, v11 op_sel:[0,0,1]
	v_ashrrev_i32_e32 v19, 31, v18
	v_lshlrev_b64 v[0:1], 11, v[18:19]
	v_cvt_pk_fp8_f32 v8, v6, v7 op_sel:[0,0,1]
	v_cvt_pk_fp8_f32 v9, v2, v3 op_sel:[0,0,1]
	v_lshl_add_u64 v[0:1], s[2:3], 0, v[0:1]
	v_lshl_add_u64 v[0:1], v[0:1], 0, v[16:17]
	v_mov_b32_e32 v164, v179
	global_store_dwordx2 v[0:1], v[22:23], off
	global_store_dwordx2 v[0:1], v[8:9], off offset:128
	s_cbranch_vccz .LBB0_2793
	s_waitcnt vmcnt(0)
	s_cmpk_gt_u32 s96, 0xff
	s_cbranch_scc1 .LBB0_2800
	s_barrier
